# GEMM K-loops: scalar/address instructions opening load segments 2-4 issued at the end of the wave's previous load segment (before its closing vmcnt wait) so each load segment starts with its LDS reads
# speedup vs baseline: 1.0104x; 1.0104x over previous
.LBB0_193:
	ds_read_b128 v[152:155], v175
	ds_read_b128 v[156:159], v175 offset:1024
	ds_read_b128 v[160:163], v175 offset:2048
	ds_read_b128 v[164:167], v175 offset:3072
	ds_read_b128 v[168:171], v176
	ds_read_b128 v[182:185], v176 offset:1024
	ds_read_b128 v[186:189], v176 offset:2048
	ds_read_b128 v[190:193], v176 offset:3072
	s_add_u32 s38, s36, 0x100
	s_addc_u32 s39, s37, 0
	s_add_u32 s68, s25, s36
	s_addc_u32 s69, s66, s37
	s_cmp_eq_u32 s67, 12
	s_cselect_b64 s[42:43], -1, 0
	s_and_b64 s[40:41], s[42:43], exec
	s_cselect_b32 s70, 0, s38
	s_cselect_b32 s41, s0, s69
	s_cselect_b32 s40, s23, s68
	v_lshl_add_u64 v[228:229], v[148:149], 0, s[36:37]
	s_add_i32 m0, s45, 0xc000
	ds_read_b128 v[196:199], v177
	ds_read_b128 v[200:203], v177 offset:1024
	ds_read_b128 v[204:207], v177 offset:2048
	ds_read_b128 v[208:211], v177 offset:3072
	ds_read_b128 v[212:215], v177 offset:4096
	ds_read_b128 v[216:219], v177 offset:5120
	ds_read_b128 v[220:223], v177 offset:6144
	ds_read_b128 v[224:227], v177 offset:7168
	global_load_lds_dwordx4 v[228:229], off
	v_lshl_add_u64 v[228:229], v[150:151], 0, s[36:37]
	s_add_i32 m0, s45, 0xe000
	s_nop 0
	global_load_lds_dwordx4 v[228:229], off
	s_add_i32 s36, s62, s5
	v_lshl_add_u64 v[228:229], s[40:41], 0, v[134:135]
	s_mov_b32 m0, s36
	s_waitcnt vmcnt(8)
	s_waitcnt lgkmcnt(0)
	s_barrier
	s_setprio 1
	s_waitcnt lgkmcnt(0)
	v_mfma_i32_16x16x64_i8 v[126:129], v[152:155], v[196:199], v[126:129]
	v_mfma_i32_16x16x64_i8 v[122:125], v[160:163], v[196:199], v[122:125]
	v_mfma_i32_16x16x64_i8 v[110:113], v[152:155], v[204:207], v[110:113]
	v_mfma_i32_16x16x64_i8 v[106:109], v[160:163], v[204:207], v[106:109]
	v_mfma_i32_16x16x64_i8 v[94:97], v[152:155], v[212:215], v[94:97]
	v_mfma_i32_16x16x64_i8 v[90:93], v[160:163], v[212:215], v[90:93]
	v_mfma_i32_16x16x64_i8 v[78:81], v[152:155], v[220:223], v[78:81]
	v_mfma_i32_16x16x64_i8 v[74:77], v[160:163], v[220:223], v[74:77]
	v_mfma_i32_16x16x64_i8 v[126:129], v[156:159], v[200:203], v[126:129]
	v_mfma_i32_16x16x64_i8 v[122:125], v[164:167], v[200:203], v[122:125]
	v_mfma_i32_16x16x64_i8 v[110:113], v[156:159], v[208:211], v[110:113]
	v_mfma_i32_16x16x64_i8 v[106:109], v[164:167], v[208:211], v[106:109]
	v_mfma_i32_16x16x64_i8 v[94:97], v[156:159], v[216:219], v[94:97]
	v_mfma_i32_16x16x64_i8 v[90:93], v[164:167], v[216:219], v[90:93]
	v_mfma_i32_16x16x64_i8 v[78:81], v[156:159], v[224:227], v[78:81]
	v_mfma_i32_16x16x64_i8 v[74:77], v[164:167], v[224:227], v[74:77]
	s_setprio 0
	s_setprio 1
	v_mfma_i32_16x16x64_i8 v[118:121], v[168:171], v[196:199], v[118:121]
	v_mfma_i32_16x16x64_i8 v[114:117], v[186:189], v[196:199], v[114:117]
	v_mfma_i32_16x16x64_i8 v[102:105], v[168:171], v[204:207], v[102:105]
	v_mfma_i32_16x16x64_i8 v[98:101], v[186:189], v[204:207], v[98:101]
	v_mfma_i32_16x16x64_i8 v[86:89], v[168:171], v[212:215], v[86:89]
	v_mfma_i32_16x16x64_i8 v[82:85], v[186:189], v[212:215], v[82:85]
	v_mfma_i32_16x16x64_i8 v[70:73], v[168:171], v[220:223], v[70:73]
	v_mfma_i32_16x16x64_i8 v[66:69], v[186:189], v[220:223], v[66:69]
	v_mfma_i32_16x16x64_i8 v[118:121], v[182:185], v[200:203], v[118:121]
	v_mfma_i32_16x16x64_i8 v[114:117], v[190:193], v[200:203], v[114:117]
	v_mfma_i32_16x16x64_i8 v[102:105], v[182:185], v[208:211], v[102:105]
	v_mfma_i32_16x16x64_i8 v[98:101], v[190:193], v[208:211], v[98:101]
	v_mfma_i32_16x16x64_i8 v[86:89], v[182:185], v[216:219], v[86:89]
	v_mfma_i32_16x16x64_i8 v[82:85], v[190:193], v[216:219], v[82:85]
	v_mfma_i32_16x16x64_i8 v[70:73], v[182:185], v[224:227], v[70:73]
	v_mfma_i32_16x16x64_i8 v[66:69], v[190:193], v[224:227], v[66:69]
	s_setprio 0
	s_barrier
	ds_read_b128 v[196:199], v177 offset:16384
	ds_read_b128 v[200:203], v177 offset:17408
	ds_read_b128 v[204:207], v177 offset:18432
	ds_read_b128 v[208:211], v177 offset:19456
	ds_read_b128 v[212:215], v177 offset:20480
	ds_read_b128 v[216:219], v177 offset:21504
	ds_read_b128 v[220:223], v177 offset:22528
	ds_read_b128 v[224:227], v177 offset:23552
	global_load_lds_dwordx4 v[228:229], off
	s_add_i32 m0, s36, 0x2000
	s_add_u32 s36, s40, 0x40000
	v_lshl_add_u64 v[230:231], s[40:41], 0, v[132:133]
	s_addc_u32 s37, s41, 0
	s_add_i32 s68, s63, s5
	global_load_lds_dwordx4 v[230:231], off
	v_lshl_add_u64 v[232:233], s[36:37], 0, v[134:135]
	s_mov_b32 m0, s68
	s_nop 0
	global_load_lds_dwordx4 v[232:233], off
	v_lshl_add_u64 v[232:233], s[36:37], 0, v[132:133]
	s_add_i32 m0, s68, 0x2000
	s_and_b64 s[36:37], s[8:9], s[42:43]
	s_and_b64 s[36:37], s[36:37], exec
	s_cselect_b32 s36, s26, s34
	s_cselect_b32 s37, s27, s35
	s_add_u32 s36, s36, s70
	s_addc_u32 s37, s37, 0
	global_load_lds_dwordx4 v[232:233], off
	v_lshl_add_u64 v[232:233], s[36:37], 0, v[136:137]
	s_mov_b32 m0, s45
	v_lshl_add_u64 v[234:235], s[36:37], 0, v[138:139]
	global_load_lds_dwordx4 v[232:233], off
	s_mov_b32 m0, s46
	s_nop 0
	global_load_lds_dwordx4 v[234:235], off
	s_add_i32 s42, 0, 0x18000
	v_add_u32_e32 v1, s42, v173
	s_add_i32 s43, 0, 0x1c000
	s_waitcnt vmcnt(8)
	s_waitcnt lgkmcnt(0)
	s_barrier
	s_setprio 1
	s_waitcnt lgkmcnt(0)
	v_mfma_i32_16x16x64_i8 v[62:65], v[152:155], v[196:199], v[62:65]
	v_mfma_i32_16x16x64_i8 v[58:61], v[160:163], v[196:199], v[58:61]
	v_mfma_i32_16x16x64_i8 v[46:49], v[152:155], v[204:207], v[46:49]
	v_mfma_i32_16x16x64_i8 v[42:45], v[160:163], v[204:207], v[42:45]
	v_mfma_i32_16x16x64_i8 v[30:33], v[152:155], v[212:215], v[30:33]
	v_mfma_i32_16x16x64_i8 v[26:29], v[160:163], v[212:215], v[26:29]
	v_mfma_i32_16x16x64_i8 v[6:9], v[152:155], v[220:223], v[6:9]
	v_mfma_i32_16x16x64_i8 v[2:5], v[160:163], v[220:223], v[2:5]
	v_mfma_i32_16x16x64_i8 v[62:65], v[156:159], v[200:203], v[62:65]
	v_mfma_i32_16x16x64_i8 v[58:61], v[164:167], v[200:203], v[58:61]
	v_mfma_i32_16x16x64_i8 v[46:49], v[156:159], v[208:211], v[46:49]
	v_mfma_i32_16x16x64_i8 v[42:45], v[164:167], v[208:211], v[42:45]
	v_mfma_i32_16x16x64_i8 v[30:33], v[156:159], v[216:219], v[30:33]
	v_mfma_i32_16x16x64_i8 v[26:29], v[164:167], v[216:219], v[26:29]
	v_mfma_i32_16x16x64_i8 v[6:9], v[156:159], v[224:227], v[6:9]
	v_mfma_i32_16x16x64_i8 v[2:5], v[164:167], v[224:227], v[2:5]
	s_setprio 0
	s_setprio 1
	v_mfma_i32_16x16x64_i8 v[54:57], v[168:171], v[196:199], v[54:57]
	v_mfma_i32_16x16x64_i8 v[50:53], v[186:189], v[196:199], v[50:53]
	v_mfma_i32_16x16x64_i8 v[38:41], v[168:171], v[204:207], v[38:41]
	v_mfma_i32_16x16x64_i8 v[34:37], v[186:189], v[204:207], v[34:37]
	v_mfma_i32_16x16x64_i8 v[14:17], v[168:171], v[212:215], v[14:17]
	v_mfma_i32_16x16x64_i8 v[10:13], v[186:189], v[212:215], v[10:13]
	v_mfma_i32_16x16x64_i8 v[22:25], v[168:171], v[220:223], v[22:25]
	v_mfma_i32_16x16x64_i8 v[18:21], v[186:189], v[220:223], v[18:21]
	v_mfma_i32_16x16x64_i8 v[54:57], v[182:185], v[200:203], v[54:57]
	v_mfma_i32_16x16x64_i8 v[50:53], v[190:193], v[200:203], v[50:53]
	v_mfma_i32_16x16x64_i8 v[38:41], v[182:185], v[208:211], v[38:41]
	v_mfma_i32_16x16x64_i8 v[34:37], v[190:193], v[208:211], v[34:37]
	v_mfma_i32_16x16x64_i8 v[14:17], v[182:185], v[216:219], v[14:17]
	v_mfma_i32_16x16x64_i8 v[10:13], v[190:193], v[216:219], v[10:13]
	v_mfma_i32_16x16x64_i8 v[22:25], v[182:185], v[224:227], v[22:25]
	v_mfma_i32_16x16x64_i8 v[18:21], v[190:193], v[224:227], v[18:21]
	s_setprio 0
	s_barrier
	ds_read_b128 v[152:155], v1
	ds_read_b128 v[156:159], v1 offset:1024
	ds_read_b128 v[160:163], v1 offset:2048
	ds_read_b128 v[164:167], v1 offset:3072
	v_add_u32_e32 v1, s43, v173
	ds_read_b128 v[168:171], v1
	ds_read_b128 v[182:185], v1 offset:1024
	ds_read_b128 v[186:189], v1 offset:2048
	ds_read_b128 v[190:193], v1 offset:3072
	s_add_u32 s36, s36, 0x40000
	s_addc_u32 s37, s37, 0
	s_mov_b32 m0, s47
	v_lshl_add_u64 v[236:237], s[36:37], 0, v[136:137]
	ds_read_b128 v[196:199], v177 offset:32768
	ds_read_b128 v[200:203], v177 offset:33792
	ds_read_b128 v[204:207], v177 offset:34816
	ds_read_b128 v[208:211], v177 offset:35840
	ds_read_b128 v[212:215], v177 offset:36864
	ds_read_b128 v[216:219], v177 offset:37888
	ds_read_b128 v[220:223], v177 offset:38912
	ds_read_b128 v[224:227], v177 offset:39936
	global_load_lds_dwordx4 v[236:237], off
	v_lshl_add_u64 v[236:237], s[36:37], 0, v[138:139]
	s_mov_b32 m0, s49
	s_nop 0
	global_load_lds_dwordx4 v[236:237], off
	s_add_i32 s36, s42, s5
	v_lshl_add_u64 v[228:229], v[228:229], 0, s[18:19]
	s_mov_b32 m0, s36
	s_waitcnt vmcnt(8)
	s_waitcnt lgkmcnt(0)
	s_barrier
	s_setprio 1
	s_waitcnt lgkmcnt(0)
	v_mfma_i32_16x16x64_i8 v[126:129], v[152:155], v[196:199], v[126:129]
	v_mfma_i32_16x16x64_i8 v[122:125], v[160:163], v[196:199], v[122:125]
	v_mfma_i32_16x16x64_i8 v[110:113], v[152:155], v[204:207], v[110:113]
	v_mfma_i32_16x16x64_i8 v[106:109], v[160:163], v[204:207], v[106:109]
	v_mfma_i32_16x16x64_i8 v[94:97], v[152:155], v[212:215], v[94:97]
	v_mfma_i32_16x16x64_i8 v[90:93], v[160:163], v[212:215], v[90:93]
	v_mfma_i32_16x16x64_i8 v[78:81], v[152:155], v[220:223], v[78:81]
	v_mfma_i32_16x16x64_i8 v[74:77], v[160:163], v[220:223], v[74:77]
	v_mfma_i32_16x16x64_i8 v[126:129], v[156:159], v[200:203], v[126:129]
	v_mfma_i32_16x16x64_i8 v[122:125], v[164:167], v[200:203], v[122:125]
	v_mfma_i32_16x16x64_i8 v[110:113], v[156:159], v[208:211], v[110:113]
	v_mfma_i32_16x16x64_i8 v[106:109], v[164:167], v[208:211], v[106:109]
	v_mfma_i32_16x16x64_i8 v[94:97], v[156:159], v[216:219], v[94:97]
	v_mfma_i32_16x16x64_i8 v[90:93], v[164:167], v[216:219], v[90:93]
	v_mfma_i32_16x16x64_i8 v[78:81], v[156:159], v[224:227], v[78:81]
	v_mfma_i32_16x16x64_i8 v[74:77], v[164:167], v[224:227], v[74:77]
	s_setprio 0
	s_setprio 1
	v_mfma_i32_16x16x64_i8 v[118:121], v[168:171], v[196:199], v[118:121]
	v_mfma_i32_16x16x64_i8 v[114:117], v[186:189], v[196:199], v[114:117]
	v_mfma_i32_16x16x64_i8 v[102:105], v[168:171], v[204:207], v[102:105]
	v_mfma_i32_16x16x64_i8 v[98:101], v[186:189], v[204:207], v[98:101]
	v_mfma_i32_16x16x64_i8 v[86:89], v[168:171], v[212:215], v[86:89]
	v_mfma_i32_16x16x64_i8 v[82:85], v[186:189], v[212:215], v[82:85]
	v_mfma_i32_16x16x64_i8 v[70:73], v[168:171], v[220:223], v[70:73]
	v_mfma_i32_16x16x64_i8 v[66:69], v[186:189], v[220:223], v[66:69]
	v_mfma_i32_16x16x64_i8 v[118:121], v[182:185], v[200:203], v[118:121]
	v_mfma_i32_16x16x64_i8 v[114:117], v[190:193], v[200:203], v[114:117]
	v_mfma_i32_16x16x64_i8 v[102:105], v[182:185], v[208:211], v[102:105]
	v_mfma_i32_16x16x64_i8 v[98:101], v[190:193], v[208:211], v[98:101]
	v_mfma_i32_16x16x64_i8 v[86:89], v[182:185], v[216:219], v[86:89]
	v_mfma_i32_16x16x64_i8 v[82:85], v[190:193], v[216:219], v[82:85]
	v_mfma_i32_16x16x64_i8 v[70:73], v[182:185], v[224:227], v[70:73]
	v_mfma_i32_16x16x64_i8 v[66:69], v[190:193], v[224:227], v[66:69]
	s_setprio 0
	s_barrier
	ds_read_b128 v[196:199], v177 offset:49152
	ds_read_b128 v[200:203], v177 offset:50176
	ds_read_b128 v[204:207], v177 offset:51200
	ds_read_b128 v[208:211], v177 offset:52224
	ds_read_b128 v[212:215], v177 offset:53248
	ds_read_b128 v[216:219], v177 offset:54272
	ds_read_b128 v[220:223], v177 offset:55296
	ds_read_b128 v[224:227], v177 offset:56320
	global_load_lds_dwordx4 v[228:229], off
	s_add_i32 m0, s36, 0x2000
	s_add_u32 s36, s40, 0x40080
	v_lshl_add_u64 v[228:229], v[230:231], 0, s[18:19]
	s_addc_u32 s37, s41, 0
	s_add_i32 s40, s43, s5
	global_load_lds_dwordx4 v[228:229], off
	v_lshl_add_u64 v[228:229], s[36:37], 0, v[134:135]
	s_mov_b32 m0, s40
	s_nop 0
	global_load_lds_dwordx4 v[228:229], off
	v_lshl_add_u64 v[228:229], s[36:37], 0, v[132:133]
	s_add_i32 m0, s40, 0x2000
	s_nop 0
	global_load_lds_dwordx4 v[228:229], off
	v_lshl_add_u64 v[228:229], v[232:233], 0, s[18:19]
	s_mov_b32 m0, s55
	s_nop 0
	global_load_lds_dwordx4 v[228:229], off
	v_lshl_add_u64 v[228:229], v[234:235], 0, s[18:19]
	s_mov_b32 m0, s56
	s_nop 0
	global_load_lds_dwordx4 v[228:229], off
	s_waitcnt vmcnt(8)
	s_waitcnt lgkmcnt(0)
	s_barrier
	s_setprio 1
	s_waitcnt lgkmcnt(0)
	v_mfma_i32_16x16x64_i8 v[62:65], v[152:155], v[196:199], v[62:65]
	v_mfma_i32_16x16x64_i8 v[58:61], v[160:163], v[196:199], v[58:61]
	v_mfma_i32_16x16x64_i8 v[46:49], v[152:155], v[204:207], v[46:49]
	v_mfma_i32_16x16x64_i8 v[42:45], v[160:163], v[204:207], v[42:45]
	v_mfma_i32_16x16x64_i8 v[30:33], v[152:155], v[212:215], v[30:33]
	v_mfma_i32_16x16x64_i8 v[26:29], v[160:163], v[212:215], v[26:29]
	v_mfma_i32_16x16x64_i8 v[6:9], v[152:155], v[220:223], v[6:9]
	v_mfma_i32_16x16x64_i8 v[2:5], v[160:163], v[220:223], v[2:5]
	v_mfma_i32_16x16x64_i8 v[62:65], v[156:159], v[200:203], v[62:65]
	v_mfma_i32_16x16x64_i8 v[58:61], v[164:167], v[200:203], v[58:61]
	v_mfma_i32_16x16x64_i8 v[46:49], v[156:159], v[208:211], v[46:49]
	v_mfma_i32_16x16x64_i8 v[42:45], v[164:167], v[208:211], v[42:45]
	v_mfma_i32_16x16x64_i8 v[30:33], v[156:159], v[216:219], v[30:33]
	v_mfma_i32_16x16x64_i8 v[26:29], v[164:167], v[216:219], v[26:29]
	v_mfma_i32_16x16x64_i8 v[6:9], v[156:159], v[224:227], v[6:9]
	v_mfma_i32_16x16x64_i8 v[2:5], v[164:167], v[224:227], v[2:5]
	s_setprio 0
	s_setprio 1
	v_mfma_i32_16x16x64_i8 v[54:57], v[168:171], v[196:199], v[54:57]
	v_mfma_i32_16x16x64_i8 v[50:53], v[186:189], v[196:199], v[50:53]
	v_mfma_i32_16x16x64_i8 v[38:41], v[168:171], v[204:207], v[38:41]
	v_mfma_i32_16x16x64_i8 v[34:37], v[186:189], v[204:207], v[34:37]
	v_mfma_i32_16x16x64_i8 v[14:17], v[168:171], v[212:215], v[14:17]
	v_mfma_i32_16x16x64_i8 v[10:13], v[186:189], v[212:215], v[10:13]
	v_mfma_i32_16x16x64_i8 v[22:25], v[168:171], v[220:223], v[22:25]
	v_mfma_i32_16x16x64_i8 v[18:21], v[186:189], v[220:223], v[18:21]
	v_mfma_i32_16x16x64_i8 v[54:57], v[182:185], v[200:203], v[54:57]
	v_mfma_i32_16x16x64_i8 v[50:53], v[190:193], v[200:203], v[50:53]
	v_mfma_i32_16x16x64_i8 v[38:41], v[182:185], v[208:211], v[38:41]
	v_mfma_i32_16x16x64_i8 v[34:37], v[190:193], v[208:211], v[34:37]
	v_mfma_i32_16x16x64_i8 v[14:17], v[182:185], v[216:219], v[14:17]
	v_mfma_i32_16x16x64_i8 v[10:13], v[190:193], v[216:219], v[10:13]
	v_mfma_i32_16x16x64_i8 v[22:25], v[182:185], v[224:227], v[22:25]
	v_mfma_i32_16x16x64_i8 v[18:21], v[190:193], v[224:227], v[18:21]
	s_setprio 0
	s_barrier
	s_add_i32 s67, s67, 2
	s_cmp_gt_u32 s67, 13
	s_mov_b64 s[36:37], s[38:39]
	s_cbranch_scc0 .LBB0_193
	s_and_b64 vcc, exec, s[20:21]
	s_cbranch_vccz .LBB0_196
	s_barrier

.LBB0_1018:
	ds_read_b128 v[18:21], v193
	ds_read_b128 v[22:25], v193 offset:1024
	ds_read_b128 v[26:29], v193 offset:2048
	ds_read_b128 v[30:33], v193 offset:3072
	ds_read_b128 v[2:5], v195
	ds_read_b128 v[6:9], v195 offset:1024
	ds_read_b128 v[10:13], v195 offset:2048
	ds_read_b128 v[14:17], v195 offset:3072
	s_add_u32 s34, s38, 0x100
	s_addc_u32 s35, s39, 0
	s_add_u32 s68, s63, s38
	s_addc_u32 s69, s66, s39
	s_cmp_eq_u32 s67, 12
	s_cselect_b64 s[40:41], -1, 0
	s_and_b64 s[36:37], s[40:41], exec
	s_cselect_b32 s37, s21, s69
	s_cselect_b32 s36, s23, s68
	s_cselect_b32 s68, 0, s35
	s_cselect_b32 s69, 0, s34
	v_lshl_add_u64 v[222:223], v[178:179], 0, s[38:39]
	s_add_i32 m0, s29, 0xc000
	ds_read_b128 v[182:185], v196
	ds_read_b128 v[186:189], v196 offset:1024
	ds_read_b128 v[198:201], v196 offset:2048
	ds_read_b128 v[202:205], v196 offset:3072
	ds_read_b128 v[206:209], v196 offset:4096
	ds_read_b128 v[210:213], v196 offset:5120
	ds_read_b128 v[214:217], v196 offset:6144
	ds_read_b128 v[218:221], v196 offset:7168
	global_load_lds_dwordx4 v[222:223], off
	v_lshl_add_u64 v[222:223], v[180:181], 0, s[38:39]
	s_add_i32 m0, s29, 0xe000
	s_nop 0
	global_load_lds_dwordx4 v[222:223], off
	s_waitcnt vmcnt(8)
	s_waitcnt lgkmcnt(0)
	s_barrier
	s_setprio 1
	s_waitcnt lgkmcnt(0)
	v_mfma_scale_f32_16x16x128_f8f6f4 v[158:161], v[18:25], v[182:189], v[158:161], v190, v190 op_sel_hi:[0,0,0]
	v_mfma_scale_f32_16x16x128_f8f6f4 v[154:157], v[26:33], v[182:189], v[154:157], v190, v190 op_sel_hi:[0,0,0]
	v_mfma_scale_f32_16x16x128_f8f6f4 v[150:153], v[18:25], v[198:205], v[150:153], v190, v190 op_sel_hi:[0,0,0]
	v_mfma_scale_f32_16x16x128_f8f6f4 v[142:145], v[26:33], v[198:205], v[142:145], v190, v190 op_sel_hi:[0,0,0]
	v_mfma_scale_f32_16x16x128_f8f6f4 v[134:137], v[18:25], v[206:213], v[134:137], v190, v190 op_sel_hi:[0,0,0]
	v_mfma_scale_f32_16x16x128_f8f6f4 v[126:129], v[26:33], v[206:213], v[126:129], v190, v190 op_sel_hi:[0,0,0]
	v_mfma_scale_f32_16x16x128_f8f6f4 v[118:121], v[18:25], v[214:221], v[118:121], v190, v190 op_sel_hi:[0,0,0]
	v_mfma_scale_f32_16x16x128_f8f6f4 v[110:113], v[26:33], v[214:221], v[110:113], v190, v190 op_sel_hi:[0,0,0]
	s_setprio 0
	s_setprio 1
	v_mfma_scale_f32_16x16x128_f8f6f4 v[146:149], v[2:9], v[182:189], v[146:149], v190, v190 op_sel_hi:[0,0,0]
	v_mfma_scale_f32_16x16x128_f8f6f4 v[138:141], v[10:17], v[182:189], v[138:141], v190, v190 op_sel_hi:[0,0,0]
	v_mfma_scale_f32_16x16x128_f8f6f4 v[130:133], v[2:9], v[198:205], v[130:133], v190, v190 op_sel_hi:[0,0,0]
	v_mfma_scale_f32_16x16x128_f8f6f4 v[122:125], v[10:17], v[198:205], v[122:125], v190, v190 op_sel_hi:[0,0,0]
	v_mfma_scale_f32_16x16x128_f8f6f4 v[114:117], v[2:9], v[206:213], v[114:117], v190, v190 op_sel_hi:[0,0,0]
	v_mfma_scale_f32_16x16x128_f8f6f4 v[106:109], v[10:17], v[206:213], v[106:109], v190, v190 op_sel_hi:[0,0,0]
	v_mfma_scale_f32_16x16x128_f8f6f4 v[102:105], v[2:9], v[214:221], v[102:105], v190, v190 op_sel_hi:[0,0,0]
	v_mfma_scale_f32_16x16x128_f8f6f4 v[98:101], v[10:17], v[214:221], v[98:101], v190, v190 op_sel_hi:[0,0,0]
	s_setprio 0
	s_barrier
	s_add_i32 s38, s53, s42
	v_lshl_add_u64 v[182:183], s[36:37], 0, v[162:163]
	s_mov_b32 m0, s38
	ds_read_b128 v[198:201], v196 offset:16384
	ds_read_b128 v[202:205], v196 offset:17408
	ds_read_b128 v[206:209], v196 offset:18432
	ds_read_b128 v[210:213], v196 offset:19456
	ds_read_b128 v[214:217], v196 offset:20480
	ds_read_b128 v[218:221], v196 offset:21504
	ds_read_b128 v[222:225], v196 offset:22528
	ds_read_b128 v[226:229], v196 offset:23552
	global_load_lds_dwordx4 v[182:183], off
	s_add_i32 m0, s38, 0x2000
	s_add_u32 s38, s36, 0x40000
	v_lshl_add_u64 v[184:185], s[36:37], 0, v[164:165]
	s_addc_u32 s39, s37, 0
	s_add_i32 s70, s54, s42
	global_load_lds_dwordx4 v[184:185], off
	v_lshl_add_u64 v[186:187], s[38:39], 0, v[162:163]
	s_mov_b32 m0, s70
	s_nop 0
	global_load_lds_dwordx4 v[186:187], off
	v_lshl_add_u64 v[186:187], s[38:39], 0, v[164:165]
	s_add_i32 m0, s70, 0x2000
	s_and_b64 s[38:39], s[6:7], s[40:41]
	s_and_b64 s[38:39], s[38:39], exec
	s_cselect_b32 s38, s24, s30
	s_cselect_b32 s39, s25, s31
	s_add_u32 s38, s38, s69
	s_addc_u32 s39, s39, s68
	global_load_lds_dwordx4 v[186:187], off
	v_lshl_add_u64 v[186:187], s[38:39], 0, v[166:167]
	s_mov_b32 m0, s29
	v_lshl_add_u64 v[188:189], s[38:39], 0, v[168:169]
	global_load_lds_dwordx4 v[186:187], off
	s_mov_b32 m0, s43
	s_nop 0
	global_load_lds_dwordx4 v[188:189], off
	s_waitcnt vmcnt(8)
	s_waitcnt lgkmcnt(0)
	s_barrier
	s_setprio 1
	s_waitcnt lgkmcnt(0)
	v_mfma_scale_f32_16x16x128_f8f6f4 v[94:97], v[18:25], v[198:205], v[94:97], v190, v190 op_sel_hi:[0,0,0]
	v_mfma_scale_f32_16x16x128_f8f6f4 v[90:93], v[26:33], v[198:205], v[90:93], v190, v190 op_sel_hi:[0,0,0]
	v_mfma_scale_f32_16x16x128_f8f6f4 v[86:89], v[18:25], v[206:213], v[86:89], v190, v190 op_sel_hi:[0,0,0]
	v_mfma_scale_f32_16x16x128_f8f6f4 v[78:81], v[26:33], v[206:213], v[78:81], v190, v190 op_sel_hi:[0,0,0]
	v_mfma_scale_f32_16x16x128_f8f6f4 v[62:65], v[18:25], v[214:221], v[62:65], v190, v190 op_sel_hi:[0,0,0]
	v_mfma_scale_f32_16x16x128_f8f6f4 v[54:57], v[26:33], v[214:221], v[54:57], v190, v190 op_sel_hi:[0,0,0]
	v_mfma_scale_f32_16x16x128_f8f6f4 v[46:49], v[18:25], v[222:229], v[46:49], v190, v190 op_sel_hi:[0,0,0]
	v_mfma_scale_f32_16x16x128_f8f6f4 v[38:41], v[26:33], v[222:229], v[38:41], v190, v190 op_sel_hi:[0,0,0]
	s_setprio 0
	s_setprio 1
	v_mfma_scale_f32_16x16x128_f8f6f4 v[82:85], v[2:9], v[198:205], v[82:85], v190, v190 op_sel_hi:[0,0,0]
	v_mfma_scale_f32_16x16x128_f8f6f4 v[74:77], v[10:17], v[198:205], v[74:77], v190, v190 op_sel_hi:[0,0,0]
	v_mfma_scale_f32_16x16x128_f8f6f4 v[58:61], v[2:9], v[206:213], v[58:61], v190, v190 op_sel_hi:[0,0,0]
	v_mfma_scale_f32_16x16x128_f8f6f4 v[50:53], v[10:17], v[206:213], v[50:53], v190, v190 op_sel_hi:[0,0,0]
	v_mfma_scale_f32_16x16x128_f8f6f4 v[42:45], v[2:9], v[214:221], v[42:45], v190, v190 op_sel_hi:[0,0,0]
	v_mfma_scale_f32_16x16x128_f8f6f4 v[34:37], v[10:17], v[214:221], v[34:37], v190, v190 op_sel_hi:[0,0,0]
	v_mfma_scale_f32_16x16x128_f8f6f4 v[70:73], v[2:9], v[222:229], v[70:73], v190, v190 op_sel_hi:[0,0,0]
	v_mfma_scale_f32_16x16x128_f8f6f4 v[66:69], v[10:17], v[222:229], v[66:69], v190, v190 op_sel_hi:[0,0,0]
	s_setprio 0
	s_barrier
	s_add_i32 s40, 0, 0x18000
	s_add_i32 s41, 0, 0x1c000
	v_add_u32_e32 v14, s40, v191
	v_add_u32_e32 v30, s41, v191
	ds_read_b128 v[2:5], v14
	ds_read_b128 v[6:9], v14 offset:1024
	ds_read_b128 v[10:13], v14 offset:2048
	ds_read_b128 v[14:17], v14 offset:3072
	ds_read_b128 v[18:21], v30
	ds_read_b128 v[22:25], v30 offset:1024
	ds_read_b128 v[26:29], v30 offset:2048
	ds_read_b128 v[30:33], v30 offset:3072
	s_add_u32 s38, s38, 0x40000
	s_addc_u32 s39, s39, 0
	s_mov_b32 m0, s44
	v_lshl_add_u64 v[230:231], s[38:39], 0, v[166:167]
	ds_read_b128 v[198:201], v196 offset:32768
	ds_read_b128 v[202:205], v196 offset:33792
	ds_read_b128 v[206:209], v196 offset:34816
	ds_read_b128 v[210:213], v196 offset:35840
	ds_read_b128 v[214:217], v196 offset:36864
	ds_read_b128 v[218:221], v196 offset:37888
	ds_read_b128 v[222:225], v196 offset:38912
	ds_read_b128 v[226:229], v196 offset:39936
	global_load_lds_dwordx4 v[230:231], off
	v_lshl_add_u64 v[230:231], s[38:39], 0, v[168:169]
	s_mov_b32 m0, s45
	s_nop 0
	global_load_lds_dwordx4 v[230:231], off
	s_add_i32 s38, s40, s42
	v_lshl_add_u64 v[182:183], v[182:183], 0, s[10:11]
	s_mov_b32 m0, s38
	s_waitcnt vmcnt(8)
	s_waitcnt lgkmcnt(0)
	s_barrier
	s_setprio 1
	s_waitcnt lgkmcnt(0)
	v_mfma_scale_f32_16x16x128_f8f6f4 v[158:161], v[2:9], v[198:205], v[158:161], v190, v190 op_sel_hi:[0,0,0]
	v_mfma_scale_f32_16x16x128_f8f6f4 v[154:157], v[10:17], v[198:205], v[154:157], v190, v190 op_sel_hi:[0,0,0]
	v_mfma_scale_f32_16x16x128_f8f6f4 v[150:153], v[2:9], v[206:213], v[150:153], v190, v190 op_sel_hi:[0,0,0]
	v_mfma_scale_f32_16x16x128_f8f6f4 v[142:145], v[10:17], v[206:213], v[142:145], v190, v190 op_sel_hi:[0,0,0]
	v_mfma_scale_f32_16x16x128_f8f6f4 v[134:137], v[2:9], v[214:221], v[134:137], v190, v190 op_sel_hi:[0,0,0]
	v_mfma_scale_f32_16x16x128_f8f6f4 v[126:129], v[10:17], v[214:221], v[126:129], v190, v190 op_sel_hi:[0,0,0]
	v_mfma_scale_f32_16x16x128_f8f6f4 v[118:121], v[2:9], v[222:229], v[118:121], v190, v190 op_sel_hi:[0,0,0]
	v_mfma_scale_f32_16x16x128_f8f6f4 v[110:113], v[10:17], v[222:229], v[110:113], v190, v190 op_sel_hi:[0,0,0]
	s_setprio 0
	s_setprio 1
	v_mfma_scale_f32_16x16x128_f8f6f4 v[146:149], v[18:25], v[198:205], v[146:149], v190, v190 op_sel_hi:[0,0,0]
	v_mfma_scale_f32_16x16x128_f8f6f4 v[138:141], v[26:33], v[198:205], v[138:141], v190, v190 op_sel_hi:[0,0,0]
	v_mfma_scale_f32_16x16x128_f8f6f4 v[130:133], v[18:25], v[206:213], v[130:133], v190, v190 op_sel_hi:[0,0,0]
	v_mfma_scale_f32_16x16x128_f8f6f4 v[122:125], v[26:33], v[206:213], v[122:125], v190, v190 op_sel_hi:[0,0,0]
	v_mfma_scale_f32_16x16x128_f8f6f4 v[114:117], v[18:25], v[214:221], v[114:117], v190, v190 op_sel_hi:[0,0,0]
	v_mfma_scale_f32_16x16x128_f8f6f4 v[106:109], v[26:33], v[214:221], v[106:109], v190, v190 op_sel_hi:[0,0,0]
	v_mfma_scale_f32_16x16x128_f8f6f4 v[102:105], v[18:25], v[222:229], v[102:105], v190, v190 op_sel_hi:[0,0,0]
	v_mfma_scale_f32_16x16x128_f8f6f4 v[98:101], v[26:33], v[222:229], v[98:101], v190, v190 op_sel_hi:[0,0,0]
	s_setprio 0
	s_barrier
	ds_read_b128 v[198:201], v196 offset:49152
	ds_read_b128 v[202:205], v196 offset:50176
	ds_read_b128 v[206:209], v196 offset:51200
	ds_read_b128 v[210:213], v196 offset:52224
	ds_read_b128 v[214:217], v196 offset:53248
	ds_read_b128 v[218:221], v196 offset:54272
	ds_read_b128 v[222:225], v196 offset:55296
	ds_read_b128 v[226:229], v196 offset:56320
	global_load_lds_dwordx4 v[182:183], off
	s_add_i32 m0, s38, 0x2000
	s_add_u32 s36, s36, 0x40080
	v_lshl_add_u64 v[182:183], v[184:185], 0, s[10:11]
	s_addc_u32 s37, s37, 0
	s_add_i32 s38, s41, s42
	global_load_lds_dwordx4 v[182:183], off
	v_lshl_add_u64 v[182:183], s[36:37], 0, v[162:163]
	s_mov_b32 m0, s38
	s_nop 0
	global_load_lds_dwordx4 v[182:183], off
	v_lshl_add_u64 v[182:183], s[36:37], 0, v[164:165]
	s_add_i32 m0, s38, 0x2000
	s_nop 0
	global_load_lds_dwordx4 v[182:183], off
	v_lshl_add_u64 v[182:183], v[186:187], 0, s[10:11]
	s_mov_b32 m0, s47
	s_nop 0
	global_load_lds_dwordx4 v[182:183], off
	v_lshl_add_u64 v[182:183], v[188:189], 0, s[10:11]
	s_mov_b32 m0, s49
	s_nop 0
	global_load_lds_dwordx4 v[182:183], off
	s_waitcnt vmcnt(8)
	s_waitcnt lgkmcnt(0)
	s_barrier
	s_setprio 1
	s_waitcnt lgkmcnt(0)
	v_mfma_scale_f32_16x16x128_f8f6f4 v[94:97], v[2:9], v[198:205], v[94:97], v190, v190 op_sel_hi:[0,0,0]
	v_mfma_scale_f32_16x16x128_f8f6f4 v[90:93], v[10:17], v[198:205], v[90:93], v190, v190 op_sel_hi:[0,0,0]
	v_mfma_scale_f32_16x16x128_f8f6f4 v[86:89], v[2:9], v[206:213], v[86:89], v190, v190 op_sel_hi:[0,0,0]
	v_mfma_scale_f32_16x16x128_f8f6f4 v[78:81], v[10:17], v[206:213], v[78:81], v190, v190 op_sel_hi:[0,0,0]
	v_mfma_scale_f32_16x16x128_f8f6f4 v[62:65], v[2:9], v[214:221], v[62:65], v190, v190 op_sel_hi:[0,0,0]
	v_mfma_scale_f32_16x16x128_f8f6f4 v[54:57], v[10:17], v[214:221], v[54:57], v190, v190 op_sel_hi:[0,0,0]
	v_mfma_scale_f32_16x16x128_f8f6f4 v[46:49], v[2:9], v[222:229], v[46:49], v190, v190 op_sel_hi:[0,0,0]
	v_mfma_scale_f32_16x16x128_f8f6f4 v[38:41], v[10:17], v[222:229], v[38:41], v190, v190 op_sel_hi:[0,0,0]
	s_setprio 0
	s_setprio 1
	v_mfma_scale_f32_16x16x128_f8f6f4 v[82:85], v[18:25], v[198:205], v[82:85], v190, v190 op_sel_hi:[0,0,0]
	v_mfma_scale_f32_16x16x128_f8f6f4 v[74:77], v[26:33], v[198:205], v[74:77], v190, v190 op_sel_hi:[0,0,0]
	v_mfma_scale_f32_16x16x128_f8f6f4 v[58:61], v[18:25], v[206:213], v[58:61], v190, v190 op_sel_hi:[0,0,0]
	v_mfma_scale_f32_16x16x128_f8f6f4 v[50:53], v[26:33], v[206:213], v[50:53], v190, v190 op_sel_hi:[0,0,0]
	v_mfma_scale_f32_16x16x128_f8f6f4 v[42:45], v[18:25], v[214:221], v[42:45], v190, v190 op_sel_hi:[0,0,0]
	v_mfma_scale_f32_16x16x128_f8f6f4 v[34:37], v[26:33], v[214:221], v[34:37], v190, v190 op_sel_hi:[0,0,0]
	v_mfma_scale_f32_16x16x128_f8f6f4 v[70:73], v[18:25], v[222:229], v[70:73], v190, v190 op_sel_hi:[0,0,0]
	v_mfma_scale_f32_16x16x128_f8f6f4 v[66:69], v[26:33], v[222:229], v[66:69], v190, v190 op_sel_hi:[0,0,0]
	s_setprio 0
	s_barrier
	s_add_i32 s67, s67, 2
	s_cmp_gt_u32 s67, 13
	s_mov_b64 s[38:39], s[34:35]
	s_cbranch_scc0 .LBB0_1018
	s_and_b64 vcc, exec, s[12:13]
	s_cbranch_vccz .LBB0_1021
	s_barrier

.LBB0_1154:
	ds_read_b128 v[70:73], v167
	ds_read_b128 v[156:159], v167 offset:1024
	ds_read_b128 v[160:163], v167 offset:2048
	ds_read_b128 v[172:175], v167 offset:3072
	ds_read_b128 v[176:179], v168
	ds_read_b128 v[180:183], v168 offset:1024
	ds_read_b128 v[184:187], v168 offset:2048
	ds_read_b128 v[188:191], v168 offset:3072
	s_add_u32 s30, s28, 0x100
	s_addc_u32 s31, s29, 0
	s_add_u32 s63, s56, s28
	s_addc_u32 s66, s57, s29
	s_cmp_eq_u32 s62, 12
	s_cselect_b64 s[36:37], -1, 0
	s_and_b64 s[34:35], s[36:37], exec
	s_cselect_b32 s67, 0, s30
	s_cselect_b32 s35, s17, s66
	s_cselect_b32 s34, s19, s63
	v_lshl_add_u64 v[192:193], v[66:67], 0, s[28:29]
	s_add_i32 m0, s25, 0xc000
	ds_read_b128 v[196:199], v169
	ds_read_b128 v[200:203], v169 offset:1024
	ds_read_b128 v[204:207], v169 offset:2048
	ds_read_b128 v[208:211], v169 offset:3072
	ds_read_b128 v[212:215], v169 offset:4096
	ds_read_b128 v[216:219], v169 offset:5120
	ds_read_b128 v[220:223], v169 offset:6144
	ds_read_b128 v[224:227], v169 offset:7168
	global_load_lds_dwordx4 v[192:193], off
	v_lshl_add_u64 v[192:193], v[68:69], 0, s[28:29]
	s_add_i32 m0, s25, 0xe000
	s_nop 0
	global_load_lds_dwordx4 v[192:193], off
	s_add_i32 s28, s49, s38
	v_lshl_add_u64 v[192:193], s[34:35], 0, v[140:141]
	s_mov_b32 m0, s28
	s_waitcnt vmcnt(8)
	s_waitcnt lgkmcnt(0)
	s_barrier
	s_setprio 1
	s_waitcnt lgkmcnt(0)
	v_mfma_i32_16x16x64_i8 v[134:137], v[70:73], v[196:199], v[134:137]
	v_mfma_i32_16x16x64_i8 v[126:129], v[160:163], v[196:199], v[126:129]
	v_mfma_i32_16x16x64_i8 v[118:121], v[70:73], v[204:207], v[118:121]
	v_mfma_i32_16x16x64_i8 v[110:113], v[160:163], v[204:207], v[110:113]
	v_mfma_i32_16x16x64_i8 v[102:105], v[70:73], v[212:215], v[102:105]
	v_mfma_i32_16x16x64_i8 v[94:97], v[160:163], v[212:215], v[94:97]
	v_mfma_i32_16x16x64_i8 v[86:89], v[70:73], v[220:223], v[86:89]
	v_mfma_i32_16x16x64_i8 v[78:81], v[160:163], v[220:223], v[78:81]
	v_mfma_i32_16x16x64_i8 v[134:137], v[156:159], v[200:203], v[134:137]
	v_mfma_i32_16x16x64_i8 v[126:129], v[172:175], v[200:203], v[126:129]
	v_mfma_i32_16x16x64_i8 v[118:121], v[156:159], v[208:211], v[118:121]
	v_mfma_i32_16x16x64_i8 v[110:113], v[172:175], v[208:211], v[110:113]
	v_mfma_i32_16x16x64_i8 v[102:105], v[156:159], v[216:219], v[102:105]
	v_mfma_i32_16x16x64_i8 v[94:97], v[172:175], v[216:219], v[94:97]
	v_mfma_i32_16x16x64_i8 v[86:89], v[156:159], v[224:227], v[86:89]
	v_mfma_i32_16x16x64_i8 v[78:81], v[172:175], v[224:227], v[78:81]
	s_setprio 0
	s_setprio 1
	v_mfma_i32_16x16x64_i8 v[130:133], v[176:179], v[196:199], v[130:133]
	v_mfma_i32_16x16x64_i8 v[122:125], v[184:187], v[196:199], v[122:125]
	v_mfma_i32_16x16x64_i8 v[114:117], v[176:179], v[204:207], v[114:117]
	v_mfma_i32_16x16x64_i8 v[106:109], v[184:187], v[204:207], v[106:109]
	v_mfma_i32_16x16x64_i8 v[98:101], v[176:179], v[212:215], v[98:101]
	v_mfma_i32_16x16x64_i8 v[90:93], v[184:187], v[212:215], v[90:93]
	v_mfma_i32_16x16x64_i8 v[82:85], v[176:179], v[220:223], v[82:85]
	v_mfma_i32_16x16x64_i8 v[74:77], v[184:187], v[220:223], v[74:77]
	v_mfma_i32_16x16x64_i8 v[130:133], v[180:183], v[200:203], v[130:133]
	v_mfma_i32_16x16x64_i8 v[122:125], v[188:191], v[200:203], v[122:125]
	v_mfma_i32_16x16x64_i8 v[114:117], v[180:183], v[208:211], v[114:117]
	v_mfma_i32_16x16x64_i8 v[106:109], v[188:191], v[208:211], v[106:109]
	v_mfma_i32_16x16x64_i8 v[98:101], v[180:183], v[216:219], v[98:101]
	v_mfma_i32_16x16x64_i8 v[90:93], v[188:191], v[216:219], v[90:93]
	v_mfma_i32_16x16x64_i8 v[82:85], v[180:183], v[224:227], v[82:85]
	v_mfma_i32_16x16x64_i8 v[74:77], v[188:191], v[224:227], v[74:77]
	s_setprio 0
	s_barrier
	ds_read_b128 v[196:199], v169 offset:16384
	ds_read_b128 v[200:203], v169 offset:17408
	ds_read_b128 v[204:207], v169 offset:18432
	ds_read_b128 v[208:211], v169 offset:19456
	ds_read_b128 v[212:215], v169 offset:20480
	ds_read_b128 v[216:219], v169 offset:21504
	ds_read_b128 v[220:223], v169 offset:22528
	ds_read_b128 v[224:227], v169 offset:23552
	global_load_lds_dwordx4 v[192:193], off
	s_add_i32 m0, s28, 0x2000
	s_add_u32 s28, s34, 0x40000
	v_lshl_add_u64 v[228:229], s[34:35], 0, v[138:139]
	s_addc_u32 s29, s35, 0
	s_add_i32 s63, s52, s38
	global_load_lds_dwordx4 v[228:229], off
	v_lshl_add_u64 v[230:231], s[28:29], 0, v[140:141]
	s_mov_b32 m0, s63
	s_nop 0
	global_load_lds_dwordx4 v[230:231], off
	v_lshl_add_u64 v[230:231], s[28:29], 0, v[138:139]
	s_add_i32 m0, s63, 0x2000
	s_and_b64 s[28:29], s[6:7], s[36:37]
	s_and_b64 s[28:29], s[28:29], exec
	s_cselect_b32 s28, s20, s26
	s_cselect_b32 s29, s21, s27
	s_add_u32 s28, s28, s67
	s_addc_u32 s29, s29, 0
	global_load_lds_dwordx4 v[230:231], off
	v_lshl_add_u64 v[230:231], s[28:29], 0, v[142:143]
	s_mov_b32 m0, s25
	v_lshl_add_u64 v[232:233], s[28:29], 0, v[144:145]
	global_load_lds_dwordx4 v[230:231], off
	s_mov_b32 m0, s41
	s_nop 0
	global_load_lds_dwordx4 v[232:233], off
	s_add_i32 s36, 0, 0x18000
	v_add_u32_e32 v1, s36, v165
	s_add_i32 s37, 0, 0x1c000
	s_waitcnt vmcnt(8)
	s_waitcnt lgkmcnt(0)
	s_barrier
; #define PG8_STAGE(bufoff, gbase, voff) do { _Pragma("unroll") for (int _i = 0; _i < 2; ++_i) \
;         __builtin_amdgcn_global_load_lds((const unsigned*)((const char*)(gbase) + (voff)[_i]), (LAS unsigned*)(lds + (bufoff) + ldsw + _i * 8192), 16, 0, 0); } while (0)
; #define PG8_LDA(dst, b, h) do { _Pragma("unroll") for (int m = 0; m < 4; ++m) dst[m] = PG8_LD32(lds + PG8_SA(b, h) + aoff + m * 2048); } while (0)
; #define PG8_LDB(dst, b, h) do { _Pragma("unroll") for (int n = 0; n < 2; ++n) dst[n] = PG8_LD32(lds + PG8_SB(b, h) + boff + n * 2048); } while (0)
; #define PG8_WAIT_V(n) asm volatile("s_waitcnt vmcnt(" #n ")" ::: "memory")
; #define PG8_WAIT_L(n) asm volatile("s_waitcnt lgkmcnt(" #n ")" ::: "memory")
; #define PG8_BAR __builtin_amdgcn_s_barrier()
; #define PG8_SCHED __builtin_amdgcn_sched_barrier(0)
; #define PG8_STA(bufoff, nextflag, h, koff) do { if constexpr (Sched::GATHER) { unsigned _o[2]; _o[0] = (nextflag) ? nxtA[h][0] : curA[h][0]; _o[1] = (nextflag) ? nxtA[h][1] : curA[h][1]; PG8_STAGE(bufoff, Ab + (koff), _o); } \
;         else { PG8_STAGE(bufoff, ((nextflag) ? nA : cA) + (size_t)(h) * hstep + (koff), voffA); } } while (0)
; template <class Epi, class Sched, bool ALIGN_EPI, int DT>
; __device__ __forceinline__ void gemm_phase(LAS unsigned char* lds, const int KB, const Sched& S, const Epi& E) {
;     ...
;             PG8_LDB(B0, 0, 0); PG8_LDB(B1, 0, 1); PG8_SCHED; PG8_LDA(At, 0, 0); PG8_STA(PG8_SA(1, 1), false, 1, k1);
;             PG8_WAIT_V(8); PG8_WAIT_L(0); PG8_BAR; PG8_MMA(0, 0, At, B0); PG8_MMA(0, 1, At, B1); PG8_BAR; PG8_SCHED;
;             PG8_LDA(At, 0, 1); PG8_STAGE(PG8_SB(0, 0), b2, voffB); PG8_STAGE(PG8_SB(0, 1), b2 + hstep, voffB); PG8_STA(PG8_SA(0, 0), last, 0, k2);
;             PG8_WAIT_V(8); PG8_WAIT_L(0); PG8_BAR; PG8_MMA(1, 0, At, B0); PG8_MMA(1, 1, At, B1); PG8_BAR; PG8_SCHED;
;             PG8_LDB(B0, 1, 0); PG8_LDB(B1, 1, 1); PG8_SCHED; PG8_LDA(At, 1, 0); PG8_STA(PG8_SA(0, 1), last, 1, k2);
;             PG8_WAIT_V(8); PG8_WAIT_L(0); PG8_BAR; PG8_MMA(0, 0, At, B0); PG8_MMA(0, 1, At, B1); PG8_BAR; PG8_SCHED;
;             PG8_LDA(At, 1, 1); PG8_STAGE(PG8_SB(1, 0), b3, voffB); PG8_STAGE(PG8_SB(1, 1), b3 + hstep, voffB); PG8_STA(PG8_SA(1, 0), last, 0, k3);
;             PG8_WAIT_V(8); PG8_WAIT_L(0); PG8_BAR; PG8_MMA(1, 0, At, B0); PG8_MMA(1, 1, At, B1); PG8_BAR; PG8_SCHED;
	s_setprio 1
	s_waitcnt lgkmcnt(0)
	v_mfma_i32_16x16x64_i8 v[62:65], v[70:73], v[196:199], v[62:65]
	v_mfma_i32_16x16x64_i8 v[54:57], v[160:163], v[196:199], v[54:57]
	v_mfma_i32_16x16x64_i8 v[46:49], v[70:73], v[204:207], v[46:49]
	v_mfma_i32_16x16x64_i8 v[38:41], v[160:163], v[204:207], v[38:41]
	v_mfma_i32_16x16x64_i8 v[30:33], v[70:73], v[212:215], v[30:33]
	v_mfma_i32_16x16x64_i8 v[22:25], v[160:163], v[212:215], v[22:25]
	v_mfma_i32_16x16x64_i8 v[6:9], v[70:73], v[220:223], v[6:9]
	v_mfma_i32_16x16x64_i8 v[2:5], v[160:163], v[220:223], v[2:5]
	v_mfma_i32_16x16x64_i8 v[62:65], v[156:159], v[200:203], v[62:65]
	v_mfma_i32_16x16x64_i8 v[54:57], v[172:175], v[200:203], v[54:57]
	v_mfma_i32_16x16x64_i8 v[46:49], v[156:159], v[208:211], v[46:49]
	v_mfma_i32_16x16x64_i8 v[38:41], v[172:175], v[208:211], v[38:41]
	v_mfma_i32_16x16x64_i8 v[30:33], v[156:159], v[216:219], v[30:33]
	v_mfma_i32_16x16x64_i8 v[22:25], v[172:175], v[216:219], v[22:25]
	v_mfma_i32_16x16x64_i8 v[6:9], v[156:159], v[224:227], v[6:9]
	v_mfma_i32_16x16x64_i8 v[2:5], v[172:175], v[224:227], v[2:5]
	s_setprio 0
	s_setprio 1
	v_mfma_i32_16x16x64_i8 v[58:61], v[176:179], v[196:199], v[58:61]
	v_mfma_i32_16x16x64_i8 v[50:53], v[184:187], v[196:199], v[50:53]
	v_mfma_i32_16x16x64_i8 v[42:45], v[176:179], v[204:207], v[42:45]
	v_mfma_i32_16x16x64_i8 v[34:37], v[184:187], v[204:207], v[34:37]
	v_mfma_i32_16x16x64_i8 v[26:29], v[176:179], v[212:215], v[26:29]
	v_mfma_i32_16x16x64_i8 v[18:21], v[184:187], v[212:215], v[18:21]
	v_mfma_i32_16x16x64_i8 v[14:17], v[176:179], v[220:223], v[14:17]
	v_mfma_i32_16x16x64_i8 v[10:13], v[184:187], v[220:223], v[10:13]
	v_mfma_i32_16x16x64_i8 v[58:61], v[180:183], v[200:203], v[58:61]
	v_mfma_i32_16x16x64_i8 v[50:53], v[188:191], v[200:203], v[50:53]
	v_mfma_i32_16x16x64_i8 v[42:45], v[180:183], v[208:211], v[42:45]
	v_mfma_i32_16x16x64_i8 v[34:37], v[188:191], v[208:211], v[34:37]
	v_mfma_i32_16x16x64_i8 v[26:29], v[180:183], v[216:219], v[26:29]
	v_mfma_i32_16x16x64_i8 v[18:21], v[188:191], v[216:219], v[18:21]
	v_mfma_i32_16x16x64_i8 v[14:17], v[180:183], v[224:227], v[14:17]
	v_mfma_i32_16x16x64_i8 v[10:13], v[188:191], v[224:227], v[10:13]
	s_setprio 0
	s_barrier
	ds_read_b128 v[70:73], v1
	ds_read_b128 v[156:159], v1 offset:1024
	ds_read_b128 v[160:163], v1 offset:2048
	ds_read_b128 v[172:175], v1 offset:3072
	v_add_u32_e32 v1, s37, v165
	ds_read_b128 v[176:179], v1
	ds_read_b128 v[180:183], v1 offset:1024
	ds_read_b128 v[184:187], v1 offset:2048
	ds_read_b128 v[188:191], v1 offset:3072
	s_add_u32 s28, s28, 0x40000
	s_addc_u32 s29, s29, 0
	s_mov_b32 m0, s42
	v_lshl_add_u64 v[234:235], s[28:29], 0, v[142:143]
	ds_read_b128 v[196:199], v169 offset:32768
	ds_read_b128 v[200:203], v169 offset:33792
	ds_read_b128 v[204:207], v169 offset:34816
	ds_read_b128 v[208:211], v169 offset:35840
	ds_read_b128 v[212:215], v169 offset:36864
	ds_read_b128 v[216:219], v169 offset:37888
	ds_read_b128 v[220:223], v169 offset:38912
	ds_read_b128 v[224:227], v169 offset:39936
	global_load_lds_dwordx4 v[234:235], off
	v_lshl_add_u64 v[234:235], s[28:29], 0, v[144:145]
	s_mov_b32 m0, s43
	s_nop 0
	global_load_lds_dwordx4 v[234:235], off
	s_add_i32 s28, s36, s38
	v_lshl_add_u64 v[192:193], v[192:193], 0, s[12:13]
	s_mov_b32 m0, s28
	s_waitcnt vmcnt(8)
	s_waitcnt lgkmcnt(0)
	s_barrier
	s_setprio 1
	s_waitcnt lgkmcnt(0)
	v_mfma_i32_16x16x64_i8 v[134:137], v[70:73], v[196:199], v[134:137]
	v_mfma_i32_16x16x64_i8 v[126:129], v[160:163], v[196:199], v[126:129]
	v_mfma_i32_16x16x64_i8 v[118:121], v[70:73], v[204:207], v[118:121]
	v_mfma_i32_16x16x64_i8 v[110:113], v[160:163], v[204:207], v[110:113]
	v_mfma_i32_16x16x64_i8 v[102:105], v[70:73], v[212:215], v[102:105]
	v_mfma_i32_16x16x64_i8 v[94:97], v[160:163], v[212:215], v[94:97]
	v_mfma_i32_16x16x64_i8 v[86:89], v[70:73], v[220:223], v[86:89]
	v_mfma_i32_16x16x64_i8 v[78:81], v[160:163], v[220:223], v[78:81]
	v_mfma_i32_16x16x64_i8 v[134:137], v[156:159], v[200:203], v[134:137]
	v_mfma_i32_16x16x64_i8 v[126:129], v[172:175], v[200:203], v[126:129]
	v_mfma_i32_16x16x64_i8 v[118:121], v[156:159], v[208:211], v[118:121]
	v_mfma_i32_16x16x64_i8 v[110:113], v[172:175], v[208:211], v[110:113]
	v_mfma_i32_16x16x64_i8 v[102:105], v[156:159], v[216:219], v[102:105]
	v_mfma_i32_16x16x64_i8 v[94:97], v[172:175], v[216:219], v[94:97]
	v_mfma_i32_16x16x64_i8 v[86:89], v[156:159], v[224:227], v[86:89]
	v_mfma_i32_16x16x64_i8 v[78:81], v[172:175], v[224:227], v[78:81]
	s_setprio 0
	s_setprio 1
	v_mfma_i32_16x16x64_i8 v[130:133], v[176:179], v[196:199], v[130:133]
	v_mfma_i32_16x16x64_i8 v[122:125], v[184:187], v[196:199], v[122:125]
	v_mfma_i32_16x16x64_i8 v[114:117], v[176:179], v[204:207], v[114:117]
	v_mfma_i32_16x16x64_i8 v[106:109], v[184:187], v[204:207], v[106:109]
	v_mfma_i32_16x16x64_i8 v[98:101], v[176:179], v[212:215], v[98:101]
	v_mfma_i32_16x16x64_i8 v[90:93], v[184:187], v[212:215], v[90:93]
	v_mfma_i32_16x16x64_i8 v[82:85], v[176:179], v[220:223], v[82:85]
	v_mfma_i32_16x16x64_i8 v[74:77], v[184:187], v[220:223], v[74:77]
	v_mfma_i32_16x16x64_i8 v[130:133], v[180:183], v[200:203], v[130:133]
	v_mfma_i32_16x16x64_i8 v[122:125], v[188:191], v[200:203], v[122:125]
	v_mfma_i32_16x16x64_i8 v[114:117], v[180:183], v[208:211], v[114:117]
	v_mfma_i32_16x16x64_i8 v[106:109], v[188:191], v[208:211], v[106:109]
	v_mfma_i32_16x16x64_i8 v[98:101], v[180:183], v[216:219], v[98:101]
	v_mfma_i32_16x16x64_i8 v[90:93], v[188:191], v[216:219], v[90:93]
	v_mfma_i32_16x16x64_i8 v[82:85], v[180:183], v[224:227], v[82:85]
	v_mfma_i32_16x16x64_i8 v[74:77], v[188:191], v[224:227], v[74:77]
	s_setprio 0
	s_barrier
; #define PG8_STAGE(bufoff, gbase, voff) do { _Pragma("unroll") for (int _i = 0; _i < 2; ++_i) \
;         __builtin_amdgcn_global_load_lds((const unsigned*)((const char*)(gbase) + (voff)[_i]), (LAS unsigned*)(lds + (bufoff) + ldsw + _i * 8192), 16, 0, 0); } while (0)
; #define PG8_LDA(dst, b, h) do { _Pragma("unroll") for (int m = 0; m < 4; ++m) dst[m] = PG8_LD32(lds + PG8_SA(b, h) + aoff + m * 2048); } while (0)
; #define PG8_WAIT_V(n) asm volatile("s_waitcnt vmcnt(" #n ")" ::: "memory")
; #define PG8_WAIT_L(n) asm volatile("s_waitcnt lgkmcnt(" #n ")" ::: "memory")
; #define PG8_BAR __builtin_amdgcn_s_barrier()
; #define PG8_SCHED __builtin_amdgcn_sched_barrier(0)
; #define PG8_STA(bufoff, nextflag, h, koff) do { if constexpr (Sched::GATHER) { unsigned _o[2]; _o[0] = (nextflag) ? nxtA[h][0] : curA[h][0]; _o[1] = (nextflag) ? nxtA[h][1] : curA[h][1]; PG8_STAGE(bufoff, Ab + (koff), _o); } \
;         else { PG8_STAGE(bufoff, ((nextflag) ? nA : cA) + (size_t)(h) * hstep + (koff), voffA); } } while (0)
; template <class Epi, class Sched, bool ALIGN_EPI, int DT>
; __device__ __forceinline__ void gemm_phase(LAS unsigned char* lds, const int KB, const Sched& S, const Epi& E) {
;     ...
;             PG8_LDA(At, 1, 1); PG8_STAGE(PG8_SB(1, 0), b3, voffB); PG8_STAGE(PG8_SB(1, 1), b3 + hstep, voffB); PG8_STA(PG8_SA(1, 0), last, 0, k3);
;             PG8_WAIT_V(8); PG8_WAIT_L(0); PG8_BAR; PG8_MMA(1, 0, At, B0); PG8_MMA(1, 1, At, B1); PG8_BAR; PG8_SCHED;
	ds_read_b128 v[196:199], v169 offset:49152
	ds_read_b128 v[200:203], v169 offset:50176
	ds_read_b128 v[204:207], v169 offset:51200
	ds_read_b128 v[208:211], v169 offset:52224
	ds_read_b128 v[212:215], v169 offset:53248
	ds_read_b128 v[216:219], v169 offset:54272
	ds_read_b128 v[220:223], v169 offset:55296
	ds_read_b128 v[224:227], v169 offset:56320
	global_load_lds_dwordx4 v[192:193], off
	s_add_i32 m0, s28, 0x2000
	s_add_u32 s28, s34, 0x40080
	v_lshl_add_u64 v[192:193], v[228:229], 0, s[12:13]
	s_addc_u32 s29, s35, 0
	s_add_i32 s34, s37, s38
	global_load_lds_dwordx4 v[192:193], off
	v_lshl_add_u64 v[192:193], s[28:29], 0, v[140:141]
	s_mov_b32 m0, s34
	s_nop 0
	global_load_lds_dwordx4 v[192:193], off
	v_lshl_add_u64 v[192:193], s[28:29], 0, v[138:139]
	s_add_i32 m0, s34, 0x2000
	s_nop 0
	global_load_lds_dwordx4 v[192:193], off
	v_lshl_add_u64 v[192:193], v[230:231], 0, s[12:13]
	s_mov_b32 m0, s45
	s_nop 0
	global_load_lds_dwordx4 v[192:193], off
	v_lshl_add_u64 v[192:193], v[232:233], 0, s[12:13]
	s_mov_b32 m0, s46
	s_nop 0
	global_load_lds_dwordx4 v[192:193], off
	s_waitcnt vmcnt(8)
	s_waitcnt lgkmcnt(0)
	s_barrier
	s_setprio 1
	s_waitcnt lgkmcnt(0)
	v_mfma_i32_16x16x64_i8 v[62:65], v[70:73], v[196:199], v[62:65]
	v_mfma_i32_16x16x64_i8 v[54:57], v[160:163], v[196:199], v[54:57]
	v_mfma_i32_16x16x64_i8 v[46:49], v[70:73], v[204:207], v[46:49]
	v_mfma_i32_16x16x64_i8 v[38:41], v[160:163], v[204:207], v[38:41]
	v_mfma_i32_16x16x64_i8 v[30:33], v[70:73], v[212:215], v[30:33]
	v_mfma_i32_16x16x64_i8 v[22:25], v[160:163], v[212:215], v[22:25]
	v_mfma_i32_16x16x64_i8 v[6:9], v[70:73], v[220:223], v[6:9]
	v_mfma_i32_16x16x64_i8 v[2:5], v[160:163], v[220:223], v[2:5]
	v_mfma_i32_16x16x64_i8 v[62:65], v[156:159], v[200:203], v[62:65]
	v_mfma_i32_16x16x64_i8 v[54:57], v[172:175], v[200:203], v[54:57]
	v_mfma_i32_16x16x64_i8 v[46:49], v[156:159], v[208:211], v[46:49]
	v_mfma_i32_16x16x64_i8 v[38:41], v[172:175], v[208:211], v[38:41]
	v_mfma_i32_16x16x64_i8 v[30:33], v[156:159], v[216:219], v[30:33]
	v_mfma_i32_16x16x64_i8 v[22:25], v[172:175], v[216:219], v[22:25]
	v_mfma_i32_16x16x64_i8 v[6:9], v[156:159], v[224:227], v[6:9]
	v_mfma_i32_16x16x64_i8 v[2:5], v[172:175], v[224:227], v[2:5]
	s_setprio 0
	s_setprio 1
	v_mfma_i32_16x16x64_i8 v[58:61], v[176:179], v[196:199], v[58:61]
	v_mfma_i32_16x16x64_i8 v[50:53], v[184:187], v[196:199], v[50:53]
	v_mfma_i32_16x16x64_i8 v[42:45], v[176:179], v[204:207], v[42:45]
	v_mfma_i32_16x16x64_i8 v[34:37], v[184:187], v[204:207], v[34:37]
	v_mfma_i32_16x16x64_i8 v[26:29], v[176:179], v[212:215], v[26:29]
	v_mfma_i32_16x16x64_i8 v[18:21], v[184:187], v[212:215], v[18:21]
	v_mfma_i32_16x16x64_i8 v[14:17], v[176:179], v[220:223], v[14:17]
	v_mfma_i32_16x16x64_i8 v[10:13], v[184:187], v[220:223], v[10:13]
	v_mfma_i32_16x16x64_i8 v[58:61], v[180:183], v[200:203], v[58:61]
	v_mfma_i32_16x16x64_i8 v[50:53], v[188:191], v[200:203], v[50:53]
	v_mfma_i32_16x16x64_i8 v[42:45], v[180:183], v[208:211], v[42:45]
	v_mfma_i32_16x16x64_i8 v[34:37], v[188:191], v[208:211], v[34:37]
	v_mfma_i32_16x16x64_i8 v[26:29], v[180:183], v[216:219], v[26:29]
	v_mfma_i32_16x16x64_i8 v[18:21], v[188:191], v[216:219], v[18:21]
	v_mfma_i32_16x16x64_i8 v[14:17], v[180:183], v[224:227], v[14:17]
	v_mfma_i32_16x16x64_i8 v[10:13], v[188:191], v[224:227], v[10:13]
	s_setprio 0
	s_barrier
	s_add_i32 s62, s62, 2
	s_cmp_gt_u32 s62, 13
	s_mov_b64 s[28:29], s[30:31]
	s_cbranch_scc0 .LBB0_1154
	s_and_b64 vcc, exec, s[14:15]
	s_cbranch_vccz .LBB0_1157
	s_barrier

; #define PG8_STAGE(bufoff, gbase, voff) do { _Pragma("unroll") for (int _i = 0; _i < 2; ++_i) \
;         __builtin_amdgcn_global_load_lds((const unsigned*)((const char*)(gbase) + (voff)[_i]), (LAS unsigned*)(lds + (bufoff) + ldsw + _i * 8192), 16, 0, 0); } while (0)
; #define PG8_LDA(dst, b, h) do { _Pragma("unroll") for (int m = 0; m < 4; ++m) dst[m] = PG8_LD32(lds + PG8_SA(b, h) + aoff + m * 2048); } while (0)
; #define PG8_LDB(dst, b, h) do { _Pragma("unroll") for (int n = 0; n < 2; ++n) dst[n] = PG8_LD32(lds + PG8_SB(b, h) + boff + n * 2048); } while (0)
; #define PG8_WAIT_V(n) asm volatile("s_waitcnt vmcnt(" #n ")" ::: "memory")
; #define PG8_WAIT_L(n) asm volatile("s_waitcnt lgkmcnt(" #n ")" ::: "memory")
; #define PG8_BAR __builtin_amdgcn_s_barrier()
; #define PG8_SCHED __builtin_amdgcn_sched_barrier(0)
; #define PG8_STA(bufoff, nextflag, h, koff) do { if constexpr (Sched::GATHER) { unsigned _o[2]; _o[0] = (nextflag) ? nxtA[h][0] : curA[h][0]; _o[1] = (nextflag) ? nxtA[h][1] : curA[h][1]; PG8_STAGE(bufoff, Ab + (koff), _o); } \
;         else { PG8_STAGE(bufoff, ((nextflag) ? nA : cA) + (size_t)(h) * hstep + (koff), voffA); } } while (0)
; template <class Epi, class Sched, bool ALIGN_EPI, int DT>
; __device__ __forceinline__ void gemm_phase(LAS unsigned char* lds, const int KB, const Sched& S, const Epi& E) {
;     ...
;             PG8_LDB(B0, 0, 0); PG8_LDB(B1, 0, 1); PG8_SCHED; PG8_LDA(At, 0, 0); PG8_STA(PG8_SA(1, 1), false, 1, k1);
;             PG8_WAIT_V(8); PG8_WAIT_L(0); PG8_BAR; PG8_MMA(0, 0, At, B0); PG8_MMA(0, 1, At, B1); PG8_BAR; PG8_SCHED;
;             PG8_LDA(At, 0, 1); PG8_STAGE(PG8_SB(0, 0), b2, voffB); PG8_STAGE(PG8_SB(0, 1), b2 + hstep, voffB); PG8_STA(PG8_SA(0, 0), last, 0, k2);
;             PG8_WAIT_V(8); PG8_WAIT_L(0); PG8_BAR; PG8_MMA(1, 0, At, B0); PG8_MMA(1, 1, At, B1); PG8_BAR; PG8_SCHED;
.LBB0_1237:
	ds_read_b128 v[18:21], v193
	ds_read_b128 v[22:25], v193 offset:1024
	ds_read_b128 v[26:29], v193 offset:2048
	ds_read_b128 v[30:33], v193 offset:3072
	ds_read_b128 v[2:5], v195
	ds_read_b128 v[6:9], v195 offset:1024
	ds_read_b128 v[10:13], v195 offset:2048
	ds_read_b128 v[14:17], v195 offset:3072
	s_add_u32 s26, s30, 0x100
	s_addc_u32 s27, s31, 0
	s_add_u32 s28, s56, s30
	s_addc_u32 s29, s57, s31
	s_add_i32 s68, s43, s34
	s_add_i32 m0, s35, 0xc000
	s_add_i32 s69, s35, 0xe000
	s_add_i32 s63, s68, 0x2000
	s_cmp_eq_u32 s62, 40
	s_cselect_b32 s29, s23, s29
	s_cselect_b32 s28, s22, s28
	s_cselect_b32 s66, 0, s27
	s_cselect_b32 s67, 0, s26
	v_lshl_add_u64 v[222:223], v[178:179], 0, s[30:31]
	ds_read_b128 v[182:185], v196
	ds_read_b128 v[186:189], v196 offset:1024
	ds_read_b128 v[198:201], v196 offset:2048
	ds_read_b128 v[202:205], v196 offset:3072
	ds_read_b128 v[206:209], v196 offset:4096
	ds_read_b128 v[210:213], v196 offset:5120
	ds_read_b128 v[214:217], v196 offset:6144
	ds_read_b128 v[218:221], v196 offset:7168
	global_load_lds_dwordx4 v[222:223], off
	v_lshl_add_u64 v[222:223], v[180:181], 0, s[30:31]
	s_mov_b32 m0, s69
	s_nop 0
	global_load_lds_dwordx4 v[222:223], off
	s_waitcnt vmcnt(8)
	s_waitcnt lgkmcnt(0)
	s_barrier
	s_setprio 1
	s_waitcnt lgkmcnt(0)
	v_mfma_scale_f32_16x16x128_f8f6f4 v[158:161], v[18:25], v[182:189], v[158:161], v190, v190 op_sel_hi:[0,0,0]
	v_mfma_scale_f32_16x16x128_f8f6f4 v[154:157], v[26:33], v[182:189], v[154:157], v190, v190 op_sel_hi:[0,0,0]
	v_mfma_scale_f32_16x16x128_f8f6f4 v[150:153], v[18:25], v[198:205], v[150:153], v190, v190 op_sel_hi:[0,0,0]
	v_mfma_scale_f32_16x16x128_f8f6f4 v[142:145], v[26:33], v[198:205], v[142:145], v190, v190 op_sel_hi:[0,0,0]
	v_mfma_scale_f32_16x16x128_f8f6f4 v[134:137], v[18:25], v[206:213], v[134:137], v190, v190 op_sel_hi:[0,0,0]
	v_mfma_scale_f32_16x16x128_f8f6f4 v[126:129], v[26:33], v[206:213], v[126:129], v190, v190 op_sel_hi:[0,0,0]
	v_mfma_scale_f32_16x16x128_f8f6f4 v[118:121], v[18:25], v[214:221], v[118:121], v190, v190 op_sel_hi:[0,0,0]
	v_mfma_scale_f32_16x16x128_f8f6f4 v[110:113], v[26:33], v[214:221], v[110:113], v190, v190 op_sel_hi:[0,0,0]
	s_setprio 0
	s_setprio 1
	v_mfma_scale_f32_16x16x128_f8f6f4 v[146:149], v[2:9], v[182:189], v[146:149], v190, v190 op_sel_hi:[0,0,0]
	v_mfma_scale_f32_16x16x128_f8f6f4 v[138:141], v[10:17], v[182:189], v[138:141], v190, v190 op_sel_hi:[0,0,0]
	v_mfma_scale_f32_16x16x128_f8f6f4 v[130:133], v[2:9], v[198:205], v[130:133], v190, v190 op_sel_hi:[0,0,0]
	v_mfma_scale_f32_16x16x128_f8f6f4 v[122:125], v[10:17], v[198:205], v[122:125], v190, v190 op_sel_hi:[0,0,0]
	v_mfma_scale_f32_16x16x128_f8f6f4 v[114:117], v[2:9], v[206:213], v[114:117], v190, v190 op_sel_hi:[0,0,0]
	v_mfma_scale_f32_16x16x128_f8f6f4 v[106:109], v[10:17], v[206:213], v[106:109], v190, v190 op_sel_hi:[0,0,0]
	v_mfma_scale_f32_16x16x128_f8f6f4 v[102:105], v[2:9], v[214:221], v[102:105], v190, v190 op_sel_hi:[0,0,0]
	v_mfma_scale_f32_16x16x128_f8f6f4 v[98:101], v[10:17], v[214:221], v[98:101], v190, v190 op_sel_hi:[0,0,0]
	s_setprio 0
	s_barrier
	s_mov_b32 m0, s68
	v_lshl_add_u64 v[184:185], s[28:29], 0, v[162:163]
	ds_read_b128 v[198:201], v196 offset:16384
	ds_read_b128 v[202:205], v196 offset:17408
	ds_read_b128 v[206:209], v196 offset:18432
	ds_read_b128 v[210:213], v196 offset:19456
	ds_read_b128 v[214:217], v196 offset:20480
	ds_read_b128 v[218:221], v196 offset:21504
	ds_read_b128 v[222:225], v196 offset:22528
	ds_read_b128 v[226:229], v196 offset:23552
	global_load_lds_dwordx4 v[184:185], off
	s_mov_b32 m0, s63
	s_cselect_b32 s63, s9, s25
	s_cselect_b32 s68, s8, s24
	s_add_u32 s30, s28, 0xb0000
	v_lshl_add_u64 v[182:183], s[28:29], 0, v[164:165]
	s_addc_u32 s31, s29, 0
	s_add_i32 s69, s44, s34
	global_load_lds_dwordx4 v[182:183], off
	v_lshl_add_u64 v[186:187], s[30:31], 0, v[162:163]
	s_mov_b32 m0, s69
	s_nop 0
	global_load_lds_dwordx4 v[186:187], off
	s_add_i32 m0, s69, 0x2000
	v_lshl_add_u64 v[186:187], s[30:31], 0, v[164:165]
	s_add_u32 s30, s68, s67
	s_addc_u32 s31, s63, s66
	global_load_lds_dwordx4 v[186:187], off
	v_lshl_add_u64 v[186:187], s[30:31], 0, v[166:167]
	s_mov_b32 m0, s35
	v_lshl_add_u64 v[188:189], s[30:31], 0, v[168:169]
	global_load_lds_dwordx4 v[186:187], off
	s_mov_b32 m0, s36
	s_nop 0
	global_load_lds_dwordx4 v[188:189], off
	s_waitcnt vmcnt(8)
	s_waitcnt lgkmcnt(0)
	s_barrier
	s_setprio 1
	s_waitcnt lgkmcnt(0)
	v_mfma_scale_f32_16x16x128_f8f6f4 v[94:97], v[18:25], v[198:205], v[94:97], v190, v190 op_sel_hi:[0,0,0]
	v_mfma_scale_f32_16x16x128_f8f6f4 v[90:93], v[26:33], v[198:205], v[90:93], v190, v190 op_sel_hi:[0,0,0]
	v_mfma_scale_f32_16x16x128_f8f6f4 v[86:89], v[18:25], v[206:213], v[86:89], v190, v190 op_sel_hi:[0,0,0]
	v_mfma_scale_f32_16x16x128_f8f6f4 v[78:81], v[26:33], v[206:213], v[78:81], v190, v190 op_sel_hi:[0,0,0]
	v_mfma_scale_f32_16x16x128_f8f6f4 v[62:65], v[18:25], v[214:221], v[62:65], v190, v190 op_sel_hi:[0,0,0]
	v_mfma_scale_f32_16x16x128_f8f6f4 v[54:57], v[26:33], v[214:221], v[54:57], v190, v190 op_sel_hi:[0,0,0]
	v_mfma_scale_f32_16x16x128_f8f6f4 v[46:49], v[18:25], v[222:229], v[46:49], v190, v190 op_sel_hi:[0,0,0]
	v_mfma_scale_f32_16x16x128_f8f6f4 v[38:41], v[26:33], v[222:229], v[38:41], v190, v190 op_sel_hi:[0,0,0]
	s_setprio 0
	s_setprio 1
	v_mfma_scale_f32_16x16x128_f8f6f4 v[82:85], v[2:9], v[198:205], v[82:85], v190, v190 op_sel_hi:[0,0,0]
	v_mfma_scale_f32_16x16x128_f8f6f4 v[74:77], v[10:17], v[198:205], v[74:77], v190, v190 op_sel_hi:[0,0,0]
	v_mfma_scale_f32_16x16x128_f8f6f4 v[58:61], v[2:9], v[206:213], v[58:61], v190, v190 op_sel_hi:[0,0,0]
	v_mfma_scale_f32_16x16x128_f8f6f4 v[50:53], v[10:17], v[206:213], v[50:53], v190, v190 op_sel_hi:[0,0,0]
	v_mfma_scale_f32_16x16x128_f8f6f4 v[42:45], v[2:9], v[214:221], v[42:45], v190, v190 op_sel_hi:[0,0,0]
	v_mfma_scale_f32_16x16x128_f8f6f4 v[34:37], v[10:17], v[214:221], v[34:37], v190, v190 op_sel_hi:[0,0,0]
	v_mfma_scale_f32_16x16x128_f8f6f4 v[70:73], v[2:9], v[222:229], v[70:73], v190, v190 op_sel_hi:[0,0,0]
	v_mfma_scale_f32_16x16x128_f8f6f4 v[66:69], v[10:17], v[222:229], v[66:69], v190, v190 op_sel_hi:[0,0,0]
	s_setprio 0
	s_barrier
; #define PG8_STAGE(bufoff, gbase, voff) do { _Pragma("unroll") for (int _i = 0; _i < 2; ++_i) \
;         __builtin_amdgcn_global_load_lds((const unsigned*)((const char*)(gbase) + (voff)[_i]), (LAS unsigned*)(lds + (bufoff) + ldsw + _i * 8192), 16, 0, 0); } while (0)
; #define PG8_LDA(dst, b, h) do { _Pragma("unroll") for (int m = 0; m < 4; ++m) dst[m] = PG8_LD32(lds + PG8_SA(b, h) + aoff + m * 2048); } while (0)
; #define PG8_LDB(dst, b, h) do { _Pragma("unroll") for (int n = 0; n < 2; ++n) dst[n] = PG8_LD32(lds + PG8_SB(b, h) + boff + n * 2048); } while (0)
; #define PG8_WAIT_V(n) asm volatile("s_waitcnt vmcnt(" #n ")" ::: "memory")
; #define PG8_WAIT_L(n) asm volatile("s_waitcnt lgkmcnt(" #n ")" ::: "memory")
; #define PG8_BAR __builtin_amdgcn_s_barrier()
; #define PG8_SCHED __builtin_amdgcn_sched_barrier(0)
; #define PG8_STA(bufoff, nextflag, h, koff) do { if constexpr (Sched::GATHER) { unsigned _o[2]; _o[0] = (nextflag) ? nxtA[h][0] : curA[h][0]; _o[1] = (nextflag) ? nxtA[h][1] : curA[h][1]; PG8_STAGE(bufoff, Ab + (koff), _o); } \
;         else { PG8_STAGE(bufoff, ((nextflag) ? nA : cA) + (size_t)(h) * hstep + (koff), voffA); } } while (0)
; template <class Epi, class Sched, bool ALIGN_EPI, int DT>
; __device__ __forceinline__ void gemm_phase(LAS unsigned char* lds, const int KB, const Sched& S, const Epi& E) {
;     ...
;             PG8_LDB(B0, 1, 0); PG8_LDB(B1, 1, 1); PG8_SCHED; PG8_LDA(At, 1, 0); PG8_STA(PG8_SA(0, 1), last, 1, k2);
;             PG8_WAIT_V(8); PG8_WAIT_L(0); PG8_BAR; PG8_MMA(0, 0, At, B0); PG8_MMA(0, 1, At, B1); PG8_BAR; PG8_SCHED;
;             PG8_LDA(At, 1, 1); PG8_STAGE(PG8_SB(1, 0), b3, voffB); PG8_STAGE(PG8_SB(1, 1), b3 + hstep, voffB); PG8_STA(PG8_SA(1, 0), last, 0, k3);
;             PG8_WAIT_V(8); PG8_WAIT_L(0); PG8_BAR; PG8_MMA(1, 0, At, B0); PG8_MMA(1, 1, At, B1); PG8_BAR; PG8_SCHED;
	s_add_i32 s63, 0, 0x18000
	s_add_i32 s66, 0, 0x1c000
	v_add_u32_e32 v14, s63, v191
	v_add_u32_e32 v30, s66, v191
	ds_read_b128 v[2:5], v14
	ds_read_b128 v[6:9], v14 offset:1024
	ds_read_b128 v[10:13], v14 offset:2048
	ds_read_b128 v[14:17], v14 offset:3072
	ds_read_b128 v[18:21], v30
	ds_read_b128 v[22:25], v30 offset:1024
	ds_read_b128 v[26:29], v30 offset:2048
	ds_read_b128 v[30:33], v30 offset:3072
	s_add_u32 s30, s30, 0xb0000
	s_addc_u32 s31, s31, 0
	s_mov_b32 m0, s37
	v_lshl_add_u64 v[230:231], s[30:31], 0, v[166:167]
	ds_read_b128 v[198:201], v196 offset:32768
	ds_read_b128 v[202:205], v196 offset:33792
	ds_read_b128 v[206:209], v196 offset:34816
	ds_read_b128 v[210:213], v196 offset:35840
	ds_read_b128 v[214:217], v196 offset:36864
	ds_read_b128 v[218:221], v196 offset:37888
	ds_read_b128 v[222:225], v196 offset:38912
	ds_read_b128 v[226:229], v196 offset:39936
	global_load_lds_dwordx4 v[230:231], off
	v_lshl_add_u64 v[230:231], s[30:31], 0, v[168:169]
	s_mov_b32 m0, s38
	s_nop 0
	global_load_lds_dwordx4 v[230:231], off
	s_add_i32 s30, s63, s34
	v_lshl_add_u64 v[184:185], v[184:185], 0, s[12:13]
	s_mov_b32 m0, s30
	s_waitcnt vmcnt(8)
	s_waitcnt lgkmcnt(0)
	s_barrier
	s_setprio 1
	s_waitcnt lgkmcnt(0)
	v_mfma_scale_f32_16x16x128_f8f6f4 v[158:161], v[2:9], v[198:205], v[158:161], v190, v190 op_sel_hi:[0,0,0]
	v_mfma_scale_f32_16x16x128_f8f6f4 v[154:157], v[10:17], v[198:205], v[154:157], v190, v190 op_sel_hi:[0,0,0]
	v_mfma_scale_f32_16x16x128_f8f6f4 v[150:153], v[2:9], v[206:213], v[150:153], v190, v190 op_sel_hi:[0,0,0]
	v_mfma_scale_f32_16x16x128_f8f6f4 v[142:145], v[10:17], v[206:213], v[142:145], v190, v190 op_sel_hi:[0,0,0]
	v_mfma_scale_f32_16x16x128_f8f6f4 v[134:137], v[2:9], v[214:221], v[134:137], v190, v190 op_sel_hi:[0,0,0]
	v_mfma_scale_f32_16x16x128_f8f6f4 v[126:129], v[10:17], v[214:221], v[126:129], v190, v190 op_sel_hi:[0,0,0]
	v_mfma_scale_f32_16x16x128_f8f6f4 v[118:121], v[2:9], v[222:229], v[118:121], v190, v190 op_sel_hi:[0,0,0]
	v_mfma_scale_f32_16x16x128_f8f6f4 v[110:113], v[10:17], v[222:229], v[110:113], v190, v190 op_sel_hi:[0,0,0]
	s_setprio 0
	s_setprio 1
	v_mfma_scale_f32_16x16x128_f8f6f4 v[146:149], v[18:25], v[198:205], v[146:149], v190, v190 op_sel_hi:[0,0,0]
	v_mfma_scale_f32_16x16x128_f8f6f4 v[138:141], v[26:33], v[198:205], v[138:141], v190, v190 op_sel_hi:[0,0,0]
	v_mfma_scale_f32_16x16x128_f8f6f4 v[130:133], v[18:25], v[206:213], v[130:133], v190, v190 op_sel_hi:[0,0,0]
	v_mfma_scale_f32_16x16x128_f8f6f4 v[122:125], v[26:33], v[206:213], v[122:125], v190, v190 op_sel_hi:[0,0,0]
	v_mfma_scale_f32_16x16x128_f8f6f4 v[114:117], v[18:25], v[214:221], v[114:117], v190, v190 op_sel_hi:[0,0,0]
	v_mfma_scale_f32_16x16x128_f8f6f4 v[106:109], v[26:33], v[214:221], v[106:109], v190, v190 op_sel_hi:[0,0,0]
	v_mfma_scale_f32_16x16x128_f8f6f4 v[102:105], v[18:25], v[222:229], v[102:105], v190, v190 op_sel_hi:[0,0,0]
	v_mfma_scale_f32_16x16x128_f8f6f4 v[98:101], v[26:33], v[222:229], v[98:101], v190, v190 op_sel_hi:[0,0,0]
	s_setprio 0
	s_barrier
	ds_read_b128 v[198:201], v196 offset:49152
	ds_read_b128 v[202:205], v196 offset:50176
	ds_read_b128 v[206:209], v196 offset:51200
	ds_read_b128 v[210:213], v196 offset:52224
	ds_read_b128 v[214:217], v196 offset:53248
	ds_read_b128 v[218:221], v196 offset:54272
	ds_read_b128 v[222:225], v196 offset:55296
	ds_read_b128 v[226:229], v196 offset:56320
	global_load_lds_dwordx4 v[184:185], off
	s_add_i32 m0, s30, 0x2000
	s_add_u32 s28, s28, 0xb0080
	v_lshl_add_u64 v[182:183], v[182:183], 0, s[12:13]
	s_addc_u32 s29, s29, 0
	s_add_i32 s30, s66, s34
	global_load_lds_dwordx4 v[182:183], off
	v_lshl_add_u64 v[182:183], s[28:29], 0, v[162:163]
	s_mov_b32 m0, s30
	s_nop 0
	global_load_lds_dwordx4 v[182:183], off
	v_lshl_add_u64 v[182:183], s[28:29], 0, v[164:165]
	s_add_i32 m0, s30, 0x2000
	s_nop 0
	global_load_lds_dwordx4 v[182:183], off
	v_lshl_add_u64 v[182:183], v[186:187], 0, s[12:13]
	s_mov_b32 m0, s40
	s_nop 0
	global_load_lds_dwordx4 v[182:183], off
	v_lshl_add_u64 v[182:183], v[188:189], 0, s[12:13]
	s_mov_b32 m0, s41
	s_nop 0
	global_load_lds_dwordx4 v[182:183], off
	s_waitcnt vmcnt(8)
	s_waitcnt lgkmcnt(0)
	s_barrier
	s_setprio 1
	s_waitcnt lgkmcnt(0)
	v_mfma_scale_f32_16x16x128_f8f6f4 v[94:97], v[2:9], v[198:205], v[94:97], v190, v190 op_sel_hi:[0,0,0]
	v_mfma_scale_f32_16x16x128_f8f6f4 v[90:93], v[10:17], v[198:205], v[90:93], v190, v190 op_sel_hi:[0,0,0]
	v_mfma_scale_f32_16x16x128_f8f6f4 v[86:89], v[2:9], v[206:213], v[86:89], v190, v190 op_sel_hi:[0,0,0]
	v_mfma_scale_f32_16x16x128_f8f6f4 v[78:81], v[10:17], v[206:213], v[78:81], v190, v190 op_sel_hi:[0,0,0]
	v_mfma_scale_f32_16x16x128_f8f6f4 v[62:65], v[2:9], v[214:221], v[62:65], v190, v190 op_sel_hi:[0,0,0]
	v_mfma_scale_f32_16x16x128_f8f6f4 v[54:57], v[10:17], v[214:221], v[54:57], v190, v190 op_sel_hi:[0,0,0]
	v_mfma_scale_f32_16x16x128_f8f6f4 v[46:49], v[2:9], v[222:229], v[46:49], v190, v190 op_sel_hi:[0,0,0]
	v_mfma_scale_f32_16x16x128_f8f6f4 v[38:41], v[10:17], v[222:229], v[38:41], v190, v190 op_sel_hi:[0,0,0]
	s_setprio 0
	s_setprio 1
	v_mfma_scale_f32_16x16x128_f8f6f4 v[82:85], v[18:25], v[198:205], v[82:85], v190, v190 op_sel_hi:[0,0,0]
	v_mfma_scale_f32_16x16x128_f8f6f4 v[74:77], v[26:33], v[198:205], v[74:77], v190, v190 op_sel_hi:[0,0,0]
	v_mfma_scale_f32_16x16x128_f8f6f4 v[58:61], v[18:25], v[206:213], v[58:61], v190, v190 op_sel_hi:[0,0,0]
	v_mfma_scale_f32_16x16x128_f8f6f4 v[50:53], v[26:33], v[206:213], v[50:53], v190, v190 op_sel_hi:[0,0,0]
	v_mfma_scale_f32_16x16x128_f8f6f4 v[42:45], v[18:25], v[214:221], v[42:45], v190, v190 op_sel_hi:[0,0,0]
	v_mfma_scale_f32_16x16x128_f8f6f4 v[34:37], v[26:33], v[214:221], v[34:37], v190, v190 op_sel_hi:[0,0,0]
	v_mfma_scale_f32_16x16x128_f8f6f4 v[70:73], v[18:25], v[222:229], v[70:73], v190, v190 op_sel_hi:[0,0,0]
	v_mfma_scale_f32_16x16x128_f8f6f4 v[66:69], v[26:33], v[222:229], v[66:69], v190, v190 op_sel_hi:[0,0,0]
	s_setprio 0
	s_barrier
	s_add_i32 s62, s62, 2
	s_cmp_gt_u32 s62, 41
	s_mov_b64 s[30:31], s[26:27]
	s_cbranch_scc0 .LBB0_1237
	s_and_b64 vcc, exec, s[14:15]
	s_cbranch_vccz .LBB0_1240
	s_barrier

; #define PG8_STAGE(bufoff, gbase, voff) do { _Pragma("unroll") for (int _i = 0; _i < 2; ++_i) \
;         __builtin_amdgcn_global_load_lds((const unsigned*)((const char*)(gbase) + (voff)[_i]), (LAS unsigned*)(lds + (bufoff) + ldsw + _i * 8192), 16, 0, 0); } while (0)
; #define PG8_LDA(dst, b, h) do { _Pragma("unroll") for (int m = 0; m < 4; ++m) dst[m] = PG8_LD32(lds + PG8_SA(b, h) + aoff + m * 2048); } while (0)
; #define PG8_LDB(dst, b, h) do { _Pragma("unroll") for (int n = 0; n < 2; ++n) dst[n] = PG8_LD32(lds + PG8_SB(b, h) + boff + n * 2048); } while (0)
; #define PG8_WAIT_V(n) asm volatile("s_waitcnt vmcnt(" #n ")" ::: "memory")
; #define PG8_WAIT_L(n) asm volatile("s_waitcnt lgkmcnt(" #n ")" ::: "memory")
; #define PG8_BAR __builtin_amdgcn_s_barrier()
; #define PG8_SCHED __builtin_amdgcn_sched_barrier(0)
; #define PG8_STA(bufoff, nextflag, h, koff) do { if constexpr (Sched::GATHER) { unsigned _o[2]; _o[0] = (nextflag) ? nxtA[h][0] : curA[h][0]; _o[1] = (nextflag) ? nxtA[h][1] : curA[h][1]; PG8_STAGE(bufoff, Ab + (koff), _o); } \
;         else { PG8_STAGE(bufoff, ((nextflag) ? nA : cA) + (size_t)(h) * hstep + (koff), voffA); } } while (0)
; template <class Epi, class Sched, bool ALIGN_EPI, int DT>
; __device__ __forceinline__ void gemm_phase(LAS unsigned char* lds, const int KB, const Sched& S, const Epi& E) {
;     ...
;             PG8_LDB(B0, 0, 0); PG8_LDB(B1, 0, 1); PG8_SCHED; PG8_LDA(At, 0, 0); PG8_STA(PG8_SA(1, 1), false, 1, k1);
;             PG8_WAIT_V(8); PG8_WAIT_L(0); PG8_BAR; PG8_MMA(0, 0, At, B0); PG8_MMA(0, 1, At, B1); PG8_BAR; PG8_SCHED;
;             PG8_LDA(At, 0, 1); PG8_STAGE(PG8_SB(0, 0), b2, voffB); PG8_STAGE(PG8_SB(0, 1), b2 + hstep, voffB); PG8_STA(PG8_SA(0, 0), last, 0, k2);
;             PG8_WAIT_V(8); PG8_WAIT_L(0); PG8_BAR; PG8_MMA(1, 0, At, B0); PG8_MMA(1, 1, At, B1); PG8_BAR; PG8_SCHED;
.LBB0_1385:
	ds_read_b128 v[152:155], v174
	ds_read_b128 v[156:159], v174 offset:1024
	ds_read_b128 v[160:163], v174 offset:2048
	ds_read_b128 v[164:167], v174 offset:3072
	ds_read_b128 v[168:171], v175
	ds_read_b128 v[180:183], v175 offset:1024
	ds_read_b128 v[184:187], v175 offset:2048
	ds_read_b128 v[188:191], v175 offset:3072
	s_add_u32 s38, s36, 0x100
	s_addc_u32 s39, s37, 0
	s_add_u32 s74, s25, s36
	s_addc_u32 s75, s70, s37
	s_cmp_eq_u32 s71, 12
	s_cselect_b64 s[42:43], -1, 0
	s_and_b64 s[40:41], s[42:43], exec
	s_cselect_b32 s76, 0, s38
	s_cselect_b32 s41, s0, s75
	s_cselect_b32 s40, s23, s74
	v_lshl_add_u64 v[192:193], v[148:149], 0, s[36:37]
	s_add_i32 m0, s47, 0xc000
	ds_read_b128 v[196:199], v176
	ds_read_b128 v[200:203], v176 offset:1024
	ds_read_b128 v[204:207], v176 offset:2048
	ds_read_b128 v[208:211], v176 offset:3072
	ds_read_b128 v[212:215], v176 offset:4096
	ds_read_b128 v[216:219], v176 offset:5120
	ds_read_b128 v[220:223], v176 offset:6144
	ds_read_b128 v[224:227], v176 offset:7168
	global_load_lds_dwordx4 v[192:193], off
	v_lshl_add_u64 v[192:193], v[150:151], 0, s[36:37]
	s_add_i32 m0, s47, 0xe000
	s_nop 0
	global_load_lds_dwordx4 v[192:193], off
	s_add_i32 s36, s66, s44
	v_lshl_add_u64 v[192:193], s[40:41], 0, v[134:135]
	s_mov_b32 m0, s36
	s_waitcnt vmcnt(8)
	s_waitcnt lgkmcnt(0)
	s_barrier
	s_setprio 1
	s_waitcnt lgkmcnt(0)
	v_mfma_i32_16x16x64_i8 v[126:129], v[152:155], v[196:199], v[126:129]
	v_mfma_i32_16x16x64_i8 v[122:125], v[160:163], v[196:199], v[122:125]
	v_mfma_i32_16x16x64_i8 v[110:113], v[152:155], v[204:207], v[110:113]
	v_mfma_i32_16x16x64_i8 v[106:109], v[160:163], v[204:207], v[106:109]
	v_mfma_i32_16x16x64_i8 v[94:97], v[152:155], v[212:215], v[94:97]
	v_mfma_i32_16x16x64_i8 v[90:93], v[160:163], v[212:215], v[90:93]
	v_mfma_i32_16x16x64_i8 v[78:81], v[152:155], v[220:223], v[78:81]
	v_mfma_i32_16x16x64_i8 v[74:77], v[160:163], v[220:223], v[74:77]
	v_mfma_i32_16x16x64_i8 v[126:129], v[156:159], v[200:203], v[126:129]
	v_mfma_i32_16x16x64_i8 v[122:125], v[164:167], v[200:203], v[122:125]
	v_mfma_i32_16x16x64_i8 v[110:113], v[156:159], v[208:211], v[110:113]
	v_mfma_i32_16x16x64_i8 v[106:109], v[164:167], v[208:211], v[106:109]
	v_mfma_i32_16x16x64_i8 v[94:97], v[156:159], v[216:219], v[94:97]
	v_mfma_i32_16x16x64_i8 v[90:93], v[164:167], v[216:219], v[90:93]
	v_mfma_i32_16x16x64_i8 v[78:81], v[156:159], v[224:227], v[78:81]
	v_mfma_i32_16x16x64_i8 v[74:77], v[164:167], v[224:227], v[74:77]
	s_setprio 0
	s_setprio 1
	v_mfma_i32_16x16x64_i8 v[118:121], v[168:171], v[196:199], v[118:121]
	v_mfma_i32_16x16x64_i8 v[114:117], v[184:187], v[196:199], v[114:117]
	v_mfma_i32_16x16x64_i8 v[102:105], v[168:171], v[204:207], v[102:105]
	v_mfma_i32_16x16x64_i8 v[98:101], v[184:187], v[204:207], v[98:101]
	v_mfma_i32_16x16x64_i8 v[86:89], v[168:171], v[212:215], v[86:89]
	v_mfma_i32_16x16x64_i8 v[82:85], v[184:187], v[212:215], v[82:85]
	v_mfma_i32_16x16x64_i8 v[70:73], v[168:171], v[220:223], v[70:73]
	v_mfma_i32_16x16x64_i8 v[66:69], v[184:187], v[220:223], v[66:69]
	v_mfma_i32_16x16x64_i8 v[118:121], v[180:183], v[200:203], v[118:121]
	v_mfma_i32_16x16x64_i8 v[114:117], v[188:191], v[200:203], v[114:117]
	v_mfma_i32_16x16x64_i8 v[102:105], v[180:183], v[208:211], v[102:105]
	v_mfma_i32_16x16x64_i8 v[98:101], v[188:191], v[208:211], v[98:101]
	v_mfma_i32_16x16x64_i8 v[86:89], v[180:183], v[216:219], v[86:89]
	v_mfma_i32_16x16x64_i8 v[82:85], v[188:191], v[216:219], v[82:85]
	v_mfma_i32_16x16x64_i8 v[70:73], v[180:183], v[224:227], v[70:73]
	v_mfma_i32_16x16x64_i8 v[66:69], v[188:191], v[224:227], v[66:69]
	s_setprio 0
	s_barrier
	ds_read_b128 v[196:199], v176 offset:16384
	ds_read_b128 v[200:203], v176 offset:17408
	ds_read_b128 v[204:207], v176 offset:18432
	ds_read_b128 v[208:211], v176 offset:19456
	ds_read_b128 v[212:215], v176 offset:20480
	ds_read_b128 v[216:219], v176 offset:21504
	ds_read_b128 v[220:223], v176 offset:22528
	ds_read_b128 v[224:227], v176 offset:23552
	global_load_lds_dwordx4 v[192:193], off
	s_add_i32 m0, s36, 0x2000
	s_add_u32 s36, s40, 0x40000
	v_lshl_add_u64 v[228:229], s[40:41], 0, v[132:133]
	s_addc_u32 s37, s41, 0
	s_add_i32 s74, s67, s44
	global_load_lds_dwordx4 v[228:229], off
	v_lshl_add_u64 v[230:231], s[36:37], 0, v[134:135]
	s_mov_b32 m0, s74
	s_nop 0
	global_load_lds_dwordx4 v[230:231], off
	v_lshl_add_u64 v[230:231], s[36:37], 0, v[132:133]
	s_add_i32 m0, s74, 0x2000
	s_and_b64 s[36:37], s[8:9], s[42:43]
	s_and_b64 s[36:37], s[36:37], exec
	s_cselect_b32 s36, s26, s34
	s_cselect_b32 s37, s27, s35
	s_add_u32 s36, s36, s76
	s_addc_u32 s37, s37, 0
	global_load_lds_dwordx4 v[230:231], off
	v_lshl_add_u64 v[230:231], s[36:37], 0, v[136:137]
	s_mov_b32 m0, s47
	v_lshl_add_u64 v[232:233], s[36:37], 0, v[138:139]
	global_load_lds_dwordx4 v[230:231], off
	s_mov_b32 m0, s49
	s_nop 0
	global_load_lds_dwordx4 v[232:233], off
	s_add_i32 s42, 0, 0x18000
	v_add_u32_e32 v1, s42, v172
	s_add_i32 s43, 0, 0x1c000
	s_waitcnt vmcnt(8)
	s_waitcnt lgkmcnt(0)
	s_barrier
; #define PG8_STAGE(bufoff, gbase, voff) do { _Pragma("unroll") for (int _i = 0; _i < 2; ++_i) \
;         __builtin_amdgcn_global_load_lds((const unsigned*)((const char*)(gbase) + (voff)[_i]), (LAS unsigned*)(lds + (bufoff) + ldsw + _i * 8192), 16, 0, 0); } while (0)
; #define PG8_LDA(dst, b, h) do { _Pragma("unroll") for (int m = 0; m < 4; ++m) dst[m] = PG8_LD32(lds + PG8_SA(b, h) + aoff + m * 2048); } while (0)
; #define PG8_LDB(dst, b, h) do { _Pragma("unroll") for (int n = 0; n < 2; ++n) dst[n] = PG8_LD32(lds + PG8_SB(b, h) + boff + n * 2048); } while (0)
; #define PG8_WAIT_V(n) asm volatile("s_waitcnt vmcnt(" #n ")" ::: "memory")
; #define PG8_WAIT_L(n) asm volatile("s_waitcnt lgkmcnt(" #n ")" ::: "memory")
; #define PG8_BAR __builtin_amdgcn_s_barrier()
; #define PG8_SCHED __builtin_amdgcn_sched_barrier(0)
; #define PG8_STA(bufoff, nextflag, h, koff) do { if constexpr (Sched::GATHER) { unsigned _o[2]; _o[0] = (nextflag) ? nxtA[h][0] : curA[h][0]; _o[1] = (nextflag) ? nxtA[h][1] : curA[h][1]; PG8_STAGE(bufoff, Ab + (koff), _o); } \
;         else { PG8_STAGE(bufoff, ((nextflag) ? nA : cA) + (size_t)(h) * hstep + (koff), voffA); } } while (0)
; template <class Epi, class Sched, bool ALIGN_EPI, int DT>
; __device__ __forceinline__ void gemm_phase(LAS unsigned char* lds, const int KB, const Sched& S, const Epi& E) {
;     ...
;             PG8_LDA(At, 0, 1); PG8_STAGE(PG8_SB(0, 0), b2, voffB); PG8_STAGE(PG8_SB(0, 1), b2 + hstep, voffB); PG8_STA(PG8_SA(0, 0), last, 0, k2);
;             PG8_WAIT_V(8); PG8_WAIT_L(0); PG8_BAR; PG8_MMA(1, 0, At, B0); PG8_MMA(1, 1, At, B1); PG8_BAR; PG8_SCHED;
;             PG8_LDB(B0, 1, 0); PG8_LDB(B1, 1, 1); PG8_SCHED; PG8_LDA(At, 1, 0); PG8_STA(PG8_SA(0, 1), last, 1, k2);
;             PG8_WAIT_V(8); PG8_WAIT_L(0); PG8_BAR; PG8_MMA(0, 0, At, B0); PG8_MMA(0, 1, At, B1); PG8_BAR; PG8_SCHED;
	s_setprio 1
	s_waitcnt lgkmcnt(0)
	v_mfma_i32_16x16x64_i8 v[62:65], v[152:155], v[196:199], v[62:65]
	v_mfma_i32_16x16x64_i8 v[58:61], v[160:163], v[196:199], v[58:61]
	v_mfma_i32_16x16x64_i8 v[46:49], v[152:155], v[204:207], v[46:49]
	v_mfma_i32_16x16x64_i8 v[42:45], v[160:163], v[204:207], v[42:45]
	v_mfma_i32_16x16x64_i8 v[30:33], v[152:155], v[212:215], v[30:33]
	v_mfma_i32_16x16x64_i8 v[26:29], v[160:163], v[212:215], v[26:29]
	v_mfma_i32_16x16x64_i8 v[6:9], v[152:155], v[220:223], v[6:9]
	v_mfma_i32_16x16x64_i8 v[2:5], v[160:163], v[220:223], v[2:5]
	v_mfma_i32_16x16x64_i8 v[62:65], v[156:159], v[200:203], v[62:65]
	v_mfma_i32_16x16x64_i8 v[58:61], v[164:167], v[200:203], v[58:61]
	v_mfma_i32_16x16x64_i8 v[46:49], v[156:159], v[208:211], v[46:49]
	v_mfma_i32_16x16x64_i8 v[42:45], v[164:167], v[208:211], v[42:45]
	v_mfma_i32_16x16x64_i8 v[30:33], v[156:159], v[216:219], v[30:33]
	v_mfma_i32_16x16x64_i8 v[26:29], v[164:167], v[216:219], v[26:29]
	v_mfma_i32_16x16x64_i8 v[6:9], v[156:159], v[224:227], v[6:9]
	v_mfma_i32_16x16x64_i8 v[2:5], v[164:167], v[224:227], v[2:5]
	s_setprio 0
	s_setprio 1
	v_mfma_i32_16x16x64_i8 v[54:57], v[168:171], v[196:199], v[54:57]
	v_mfma_i32_16x16x64_i8 v[50:53], v[184:187], v[196:199], v[50:53]
	v_mfma_i32_16x16x64_i8 v[38:41], v[168:171], v[204:207], v[38:41]
	v_mfma_i32_16x16x64_i8 v[34:37], v[184:187], v[204:207], v[34:37]
	v_mfma_i32_16x16x64_i8 v[14:17], v[168:171], v[212:215], v[14:17]
	v_mfma_i32_16x16x64_i8 v[10:13], v[184:187], v[212:215], v[10:13]
	v_mfma_i32_16x16x64_i8 v[22:25], v[168:171], v[220:223], v[22:25]
	v_mfma_i32_16x16x64_i8 v[18:21], v[184:187], v[220:223], v[18:21]
	v_mfma_i32_16x16x64_i8 v[54:57], v[180:183], v[200:203], v[54:57]
	v_mfma_i32_16x16x64_i8 v[50:53], v[188:191], v[200:203], v[50:53]
	v_mfma_i32_16x16x64_i8 v[38:41], v[180:183], v[208:211], v[38:41]
	v_mfma_i32_16x16x64_i8 v[34:37], v[188:191], v[208:211], v[34:37]
	v_mfma_i32_16x16x64_i8 v[14:17], v[180:183], v[216:219], v[14:17]
	v_mfma_i32_16x16x64_i8 v[10:13], v[188:191], v[216:219], v[10:13]
	v_mfma_i32_16x16x64_i8 v[22:25], v[180:183], v[224:227], v[22:25]
	v_mfma_i32_16x16x64_i8 v[18:21], v[188:191], v[224:227], v[18:21]
	s_setprio 0
	s_barrier
	ds_read_b128 v[152:155], v1
	ds_read_b128 v[156:159], v1 offset:1024
	ds_read_b128 v[160:163], v1 offset:2048
	ds_read_b128 v[164:167], v1 offset:3072
	v_add_u32_e32 v1, s43, v172
	ds_read_b128 v[168:171], v1
	ds_read_b128 v[180:183], v1 offset:1024
	ds_read_b128 v[184:187], v1 offset:2048
	ds_read_b128 v[188:191], v1 offset:3072
	s_add_u32 s36, s36, 0x40000
	s_addc_u32 s37, s37, 0
	s_mov_b32 m0, s52
	v_lshl_add_u64 v[234:235], s[36:37], 0, v[136:137]
	ds_read_b128 v[196:199], v176 offset:32768
	ds_read_b128 v[200:203], v176 offset:33792
	ds_read_b128 v[204:207], v176 offset:34816
	ds_read_b128 v[208:211], v176 offset:35840
	ds_read_b128 v[212:215], v176 offset:36864
	ds_read_b128 v[216:219], v176 offset:37888
	ds_read_b128 v[220:223], v176 offset:38912
	ds_read_b128 v[224:227], v176 offset:39936
	global_load_lds_dwordx4 v[234:235], off
	v_lshl_add_u64 v[234:235], s[36:37], 0, v[138:139]
	s_mov_b32 m0, s53
	s_nop 0
	global_load_lds_dwordx4 v[234:235], off
	s_add_i32 s36, s42, s44
	v_lshl_add_u64 v[192:193], v[192:193], 0, s[18:19]
	s_mov_b32 m0, s36
	s_waitcnt vmcnt(8)
	s_waitcnt lgkmcnt(0)
	s_barrier
	s_setprio 1
	s_waitcnt lgkmcnt(0)
	v_mfma_i32_16x16x64_i8 v[126:129], v[152:155], v[196:199], v[126:129]
	v_mfma_i32_16x16x64_i8 v[122:125], v[160:163], v[196:199], v[122:125]
	v_mfma_i32_16x16x64_i8 v[110:113], v[152:155], v[204:207], v[110:113]
	v_mfma_i32_16x16x64_i8 v[106:109], v[160:163], v[204:207], v[106:109]
	v_mfma_i32_16x16x64_i8 v[94:97], v[152:155], v[212:215], v[94:97]
	v_mfma_i32_16x16x64_i8 v[90:93], v[160:163], v[212:215], v[90:93]
	v_mfma_i32_16x16x64_i8 v[78:81], v[152:155], v[220:223], v[78:81]
	v_mfma_i32_16x16x64_i8 v[74:77], v[160:163], v[220:223], v[74:77]
	v_mfma_i32_16x16x64_i8 v[126:129], v[156:159], v[200:203], v[126:129]
	v_mfma_i32_16x16x64_i8 v[122:125], v[164:167], v[200:203], v[122:125]
	v_mfma_i32_16x16x64_i8 v[110:113], v[156:159], v[208:211], v[110:113]
	v_mfma_i32_16x16x64_i8 v[106:109], v[164:167], v[208:211], v[106:109]
	v_mfma_i32_16x16x64_i8 v[94:97], v[156:159], v[216:219], v[94:97]
	v_mfma_i32_16x16x64_i8 v[90:93], v[164:167], v[216:219], v[90:93]
	v_mfma_i32_16x16x64_i8 v[78:81], v[156:159], v[224:227], v[78:81]
	v_mfma_i32_16x16x64_i8 v[74:77], v[164:167], v[224:227], v[74:77]
	s_setprio 0
	s_setprio 1
	v_mfma_i32_16x16x64_i8 v[118:121], v[168:171], v[196:199], v[118:121]
	v_mfma_i32_16x16x64_i8 v[114:117], v[184:187], v[196:199], v[114:117]
	v_mfma_i32_16x16x64_i8 v[102:105], v[168:171], v[204:207], v[102:105]
	v_mfma_i32_16x16x64_i8 v[98:101], v[184:187], v[204:207], v[98:101]
	v_mfma_i32_16x16x64_i8 v[86:89], v[168:171], v[212:215], v[86:89]
	v_mfma_i32_16x16x64_i8 v[82:85], v[184:187], v[212:215], v[82:85]
	v_mfma_i32_16x16x64_i8 v[70:73], v[168:171], v[220:223], v[70:73]
	v_mfma_i32_16x16x64_i8 v[66:69], v[184:187], v[220:223], v[66:69]
	v_mfma_i32_16x16x64_i8 v[118:121], v[180:183], v[200:203], v[118:121]
	v_mfma_i32_16x16x64_i8 v[114:117], v[188:191], v[200:203], v[114:117]
	v_mfma_i32_16x16x64_i8 v[102:105], v[180:183], v[208:211], v[102:105]
	v_mfma_i32_16x16x64_i8 v[98:101], v[188:191], v[208:211], v[98:101]
	v_mfma_i32_16x16x64_i8 v[86:89], v[180:183], v[216:219], v[86:89]
	v_mfma_i32_16x16x64_i8 v[82:85], v[188:191], v[216:219], v[82:85]
	v_mfma_i32_16x16x64_i8 v[70:73], v[180:183], v[224:227], v[70:73]
	v_mfma_i32_16x16x64_i8 v[66:69], v[188:191], v[224:227], v[66:69]
	s_setprio 0
	s_barrier
; #define PG8_STAGE(bufoff, gbase, voff) do { _Pragma("unroll") for (int _i = 0; _i < 2; ++_i) \
;         __builtin_amdgcn_global_load_lds((const unsigned*)((const char*)(gbase) + (voff)[_i]), (LAS unsigned*)(lds + (bufoff) + ldsw + _i * 8192), 16, 0, 0); } while (0)
; #define PG8_LDA(dst, b, h) do { _Pragma("unroll") for (int m = 0; m < 4; ++m) dst[m] = PG8_LD32(lds + PG8_SA(b, h) + aoff + m * 2048); } while (0)
; #define PG8_WAIT_V(n) asm volatile("s_waitcnt vmcnt(" #n ")" ::: "memory")
; #define PG8_WAIT_L(n) asm volatile("s_waitcnt lgkmcnt(" #n ")" ::: "memory")
; #define PG8_BAR __builtin_amdgcn_s_barrier()
; #define PG8_SCHED __builtin_amdgcn_sched_barrier(0)
; #define PG8_STA(bufoff, nextflag, h, koff) do { if constexpr (Sched::GATHER) { unsigned _o[2]; _o[0] = (nextflag) ? nxtA[h][0] : curA[h][0]; _o[1] = (nextflag) ? nxtA[h][1] : curA[h][1]; PG8_STAGE(bufoff, Ab + (koff), _o); } \
;         else { PG8_STAGE(bufoff, ((nextflag) ? nA : cA) + (size_t)(h) * hstep + (koff), voffA); } } while (0)
; template <class Epi, class Sched, bool ALIGN_EPI, int DT>
; __device__ __forceinline__ void gemm_phase(LAS unsigned char* lds, const int KB, const Sched& S, const Epi& E) {
;     ...
;             PG8_LDA(At, 1, 1); PG8_STAGE(PG8_SB(1, 0), b3, voffB); PG8_STAGE(PG8_SB(1, 1), b3 + hstep, voffB); PG8_STA(PG8_SA(1, 0), last, 0, k3);
;             PG8_WAIT_V(8); PG8_WAIT_L(0); PG8_BAR; PG8_MMA(1, 0, At, B0); PG8_MMA(1, 1, At, B1); PG8_BAR; PG8_SCHED;
	ds_read_b128 v[196:199], v176 offset:49152
	ds_read_b128 v[200:203], v176 offset:50176
	ds_read_b128 v[204:207], v176 offset:51200
	ds_read_b128 v[208:211], v176 offset:52224
	ds_read_b128 v[212:215], v176 offset:53248
	ds_read_b128 v[216:219], v176 offset:54272
	ds_read_b128 v[220:223], v176 offset:55296
	ds_read_b128 v[224:227], v176 offset:56320
	global_load_lds_dwordx4 v[192:193], off
	s_add_i32 m0, s36, 0x2000
	s_add_u32 s36, s40, 0x40080
	v_lshl_add_u64 v[192:193], v[228:229], 0, s[18:19]
	s_addc_u32 s37, s41, 0
	s_add_i32 s40, s43, s44
	global_load_lds_dwordx4 v[192:193], off
	v_lshl_add_u64 v[192:193], s[36:37], 0, v[134:135]
	s_mov_b32 m0, s40
	s_nop 0
	global_load_lds_dwordx4 v[192:193], off
	v_lshl_add_u64 v[192:193], s[36:37], 0, v[132:133]
	s_add_i32 m0, s40, 0x2000
	s_nop 0
	global_load_lds_dwordx4 v[192:193], off
	v_lshl_add_u64 v[192:193], v[230:231], 0, s[18:19]
	s_mov_b32 m0, s57
	s_nop 0
	global_load_lds_dwordx4 v[192:193], off
	v_lshl_add_u64 v[192:193], v[232:233], 0, s[18:19]
	s_mov_b32 m0, s62
	s_nop 0
	global_load_lds_dwordx4 v[192:193], off
	s_waitcnt vmcnt(8)
	s_waitcnt lgkmcnt(0)
	s_barrier
	s_setprio 1
	s_waitcnt lgkmcnt(0)
	v_mfma_i32_16x16x64_i8 v[62:65], v[152:155], v[196:199], v[62:65]
	v_mfma_i32_16x16x64_i8 v[58:61], v[160:163], v[196:199], v[58:61]
	v_mfma_i32_16x16x64_i8 v[46:49], v[152:155], v[204:207], v[46:49]
	v_mfma_i32_16x16x64_i8 v[42:45], v[160:163], v[204:207], v[42:45]
	v_mfma_i32_16x16x64_i8 v[30:33], v[152:155], v[212:215], v[30:33]
	v_mfma_i32_16x16x64_i8 v[26:29], v[160:163], v[212:215], v[26:29]
	v_mfma_i32_16x16x64_i8 v[6:9], v[152:155], v[220:223], v[6:9]
	v_mfma_i32_16x16x64_i8 v[2:5], v[160:163], v[220:223], v[2:5]
	v_mfma_i32_16x16x64_i8 v[62:65], v[156:159], v[200:203], v[62:65]
	v_mfma_i32_16x16x64_i8 v[58:61], v[164:167], v[200:203], v[58:61]
	v_mfma_i32_16x16x64_i8 v[46:49], v[156:159], v[208:211], v[46:49]
	v_mfma_i32_16x16x64_i8 v[42:45], v[164:167], v[208:211], v[42:45]
	v_mfma_i32_16x16x64_i8 v[30:33], v[156:159], v[216:219], v[30:33]
	v_mfma_i32_16x16x64_i8 v[26:29], v[164:167], v[216:219], v[26:29]
	v_mfma_i32_16x16x64_i8 v[6:9], v[156:159], v[224:227], v[6:9]
	v_mfma_i32_16x16x64_i8 v[2:5], v[164:167], v[224:227], v[2:5]
	s_setprio 0
	s_setprio 1
	v_mfma_i32_16x16x64_i8 v[54:57], v[168:171], v[196:199], v[54:57]
	v_mfma_i32_16x16x64_i8 v[50:53], v[184:187], v[196:199], v[50:53]
	v_mfma_i32_16x16x64_i8 v[38:41], v[168:171], v[204:207], v[38:41]
	v_mfma_i32_16x16x64_i8 v[34:37], v[184:187], v[204:207], v[34:37]
	v_mfma_i32_16x16x64_i8 v[14:17], v[168:171], v[212:215], v[14:17]
	v_mfma_i32_16x16x64_i8 v[10:13], v[184:187], v[212:215], v[10:13]
	v_mfma_i32_16x16x64_i8 v[22:25], v[168:171], v[220:223], v[22:25]
	v_mfma_i32_16x16x64_i8 v[18:21], v[184:187], v[220:223], v[18:21]
	v_mfma_i32_16x16x64_i8 v[54:57], v[180:183], v[200:203], v[54:57]
	v_mfma_i32_16x16x64_i8 v[50:53], v[188:191], v[200:203], v[50:53]
	v_mfma_i32_16x16x64_i8 v[38:41], v[180:183], v[208:211], v[38:41]
	v_mfma_i32_16x16x64_i8 v[34:37], v[188:191], v[208:211], v[34:37]
	v_mfma_i32_16x16x64_i8 v[14:17], v[180:183], v[216:219], v[14:17]
	v_mfma_i32_16x16x64_i8 v[10:13], v[188:191], v[216:219], v[10:13]
	v_mfma_i32_16x16x64_i8 v[22:25], v[180:183], v[224:227], v[22:25]
	v_mfma_i32_16x16x64_i8 v[18:21], v[188:191], v[224:227], v[18:21]
	s_setprio 0
	s_barrier
	s_add_i32 s71, s71, 2
	s_cmp_gt_u32 s71, 13
	s_mov_b64 s[36:37], s[38:39]
	s_cbranch_scc0 .LBB0_1385
	s_and_b64 vcc, exec, s[20:21]
	s_cbranch_vccz .LBB0_1388
	s_barrier

; #define PG8_STAGE(bufoff, gbase, voff) do { _Pragma("unroll") for (int _i = 0; _i < 2; ++_i) \
;         __builtin_amdgcn_global_load_lds((const unsigned*)((const char*)(gbase) + (voff)[_i]), (LAS unsigned*)(lds + (bufoff) + ldsw + _i * 8192), 16, 0, 0); } while (0)
; #define PG8_LDA(dst, b, h) do { _Pragma("unroll") for (int m = 0; m < 4; ++m) dst[m] = PG8_LD32(lds + PG8_SA(b, h) + aoff + m * 2048); } while (0)
; #define PG8_LDB(dst, b, h) do { _Pragma("unroll") for (int n = 0; n < 2; ++n) dst[n] = PG8_LD32(lds + PG8_SB(b, h) + boff + n * 2048); } while (0)
; #define PG8_WAIT_V(n) asm volatile("s_waitcnt vmcnt(" #n ")" ::: "memory")
; #define PG8_WAIT_L(n) asm volatile("s_waitcnt lgkmcnt(" #n ")" ::: "memory")
; #define PG8_BAR __builtin_amdgcn_s_barrier()
; #define PG8_SCHED __builtin_amdgcn_sched_barrier(0)
; #define PG8_STA(bufoff, nextflag, h, koff) do { if constexpr (Sched::GATHER) { unsigned _o[2]; _o[0] = (nextflag) ? nxtA[h][0] : curA[h][0]; _o[1] = (nextflag) ? nxtA[h][1] : curA[h][1]; PG8_STAGE(bufoff, Ab + (koff), _o); } \
;         else { PG8_STAGE(bufoff, ((nextflag) ? nA : cA) + (size_t)(h) * hstep + (koff), voffA); } } while (0)
; template <class Epi, class Sched, bool ALIGN_EPI, int DT>
; __device__ __forceinline__ void gemm_phase(LAS unsigned char* lds, const int KB, const Sched& S, const Epi& E) {
;     ...
;             PG8_LDB(B0, 0, 0); PG8_LDB(B1, 0, 1); PG8_SCHED; PG8_LDA(At, 0, 0); PG8_STA(PG8_SA(1, 1), false, 1, k1);
;             PG8_WAIT_V(8); PG8_WAIT_L(0); PG8_BAR; PG8_MMA(0, 0, At, B0); PG8_MMA(0, 1, At, B1); PG8_BAR; PG8_SCHED;
;             PG8_LDA(At, 0, 1); PG8_STAGE(PG8_SB(0, 0), b2, voffB); PG8_STAGE(PG8_SB(0, 1), b2 + hstep, voffB); PG8_STA(PG8_SA(0, 0), last, 0, k2);
;             PG8_WAIT_V(8); PG8_WAIT_L(0); PG8_BAR; PG8_MMA(1, 0, At, B0); PG8_MMA(1, 1, At, B1); PG8_BAR; PG8_SCHED;
.LBB0_2108:
	ds_read_b128 v[18:21], v193
	ds_read_b128 v[22:25], v193 offset:1024
	ds_read_b128 v[26:29], v193 offset:2048
	ds_read_b128 v[30:33], v193 offset:3072
	ds_read_b128 v[2:5], v195
	ds_read_b128 v[6:9], v195 offset:1024
	ds_read_b128 v[10:13], v195 offset:2048
	ds_read_b128 v[14:17], v195 offset:3072
	s_add_u32 s38, s42, 0x100
	s_addc_u32 s39, s43, 0
	s_add_u32 s71, s68, s42
	s_addc_u32 s74, s69, s43
	s_cmp_eq_u32 s70, 12
	s_cselect_b64 s[44:45], -1, 0
	s_and_b64 s[40:41], s[44:45], exec
	s_cselect_b32 s41, s25, s74
	s_cselect_b32 s40, s27, s71
	s_cselect_b32 s71, 0, s39
	s_cselect_b32 s74, 0, s38
	v_lshl_add_u64 v[222:223], v[178:179], 0, s[42:43]
	s_add_i32 m0, s35, 0xc000
	ds_read_b128 v[182:185], v196
	ds_read_b128 v[186:189], v196 offset:1024
	ds_read_b128 v[198:201], v196 offset:2048
	ds_read_b128 v[202:205], v196 offset:3072
	ds_read_b128 v[206:209], v196 offset:4096
	ds_read_b128 v[210:213], v196 offset:5120
	ds_read_b128 v[214:217], v196 offset:6144
	ds_read_b128 v[218:221], v196 offset:7168
	global_load_lds_dwordx4 v[222:223], off
	v_lshl_add_u64 v[222:223], v[180:181], 0, s[42:43]
	s_add_i32 m0, s35, 0xe000
	s_nop 0
	global_load_lds_dwordx4 v[222:223], off
	s_waitcnt vmcnt(8)
	s_waitcnt lgkmcnt(0)
	s_barrier
	s_setprio 1
	s_waitcnt lgkmcnt(0)
	v_mfma_scale_f32_16x16x128_f8f6f4 v[158:161], v[18:25], v[182:189], v[158:161], v1, v1 op_sel_hi:[0,0,0]
	v_mfma_scale_f32_16x16x128_f8f6f4 v[154:157], v[26:33], v[182:189], v[154:157], v1, v1 op_sel_hi:[0,0,0]
	v_mfma_scale_f32_16x16x128_f8f6f4 v[150:153], v[18:25], v[198:205], v[150:153], v1, v1 op_sel_hi:[0,0,0]
	v_mfma_scale_f32_16x16x128_f8f6f4 v[142:145], v[26:33], v[198:205], v[142:145], v1, v1 op_sel_hi:[0,0,0]
	v_mfma_scale_f32_16x16x128_f8f6f4 v[134:137], v[18:25], v[206:213], v[134:137], v1, v1 op_sel_hi:[0,0,0]
	v_mfma_scale_f32_16x16x128_f8f6f4 v[126:129], v[26:33], v[206:213], v[126:129], v1, v1 op_sel_hi:[0,0,0]
	v_mfma_scale_f32_16x16x128_f8f6f4 v[118:121], v[18:25], v[214:221], v[118:121], v1, v1 op_sel_hi:[0,0,0]
	v_mfma_scale_f32_16x16x128_f8f6f4 v[110:113], v[26:33], v[214:221], v[110:113], v1, v1 op_sel_hi:[0,0,0]
	s_setprio 0
	s_setprio 1
	v_mfma_scale_f32_16x16x128_f8f6f4 v[146:149], v[2:9], v[182:189], v[146:149], v1, v1 op_sel_hi:[0,0,0]
	v_mfma_scale_f32_16x16x128_f8f6f4 v[138:141], v[10:17], v[182:189], v[138:141], v1, v1 op_sel_hi:[0,0,0]
	v_mfma_scale_f32_16x16x128_f8f6f4 v[130:133], v[2:9], v[198:205], v[130:133], v1, v1 op_sel_hi:[0,0,0]
	v_mfma_scale_f32_16x16x128_f8f6f4 v[122:125], v[10:17], v[198:205], v[122:125], v1, v1 op_sel_hi:[0,0,0]
	v_mfma_scale_f32_16x16x128_f8f6f4 v[114:117], v[2:9], v[206:213], v[114:117], v1, v1 op_sel_hi:[0,0,0]
	v_mfma_scale_f32_16x16x128_f8f6f4 v[106:109], v[10:17], v[206:213], v[106:109], v1, v1 op_sel_hi:[0,0,0]
	v_mfma_scale_f32_16x16x128_f8f6f4 v[102:105], v[2:9], v[214:221], v[102:105], v1, v1 op_sel_hi:[0,0,0]
	v_mfma_scale_f32_16x16x128_f8f6f4 v[98:101], v[10:17], v[214:221], v[98:101], v1, v1 op_sel_hi:[0,0,0]
	s_setprio 0
	s_barrier
	s_add_i32 s42, s57, s46
	v_lshl_add_u64 v[182:183], s[40:41], 0, v[162:163]
	s_mov_b32 m0, s42
	ds_read_b128 v[198:201], v196 offset:16384
	ds_read_b128 v[202:205], v196 offset:17408
	ds_read_b128 v[206:209], v196 offset:18432
	ds_read_b128 v[210:213], v196 offset:19456
	ds_read_b128 v[214:217], v196 offset:20480
	ds_read_b128 v[218:221], v196 offset:21504
	ds_read_b128 v[222:225], v196 offset:22528
	ds_read_b128 v[226:229], v196 offset:23552
	global_load_lds_dwordx4 v[182:183], off
	s_add_i32 m0, s42, 0x2000
	s_add_u32 s42, s40, 0x40000
	v_lshl_add_u64 v[184:185], s[40:41], 0, v[164:165]
	s_addc_u32 s43, s41, 0
	s_add_i32 s75, s62, s46
	global_load_lds_dwordx4 v[184:185], off
	v_lshl_add_u64 v[186:187], s[42:43], 0, v[162:163]
	s_mov_b32 m0, s75
	s_nop 0
	global_load_lds_dwordx4 v[186:187], off
	v_lshl_add_u64 v[186:187], s[42:43], 0, v[164:165]
	s_add_i32 m0, s75, 0x2000
	s_and_b64 s[42:43], s[6:7], s[44:45]
	s_and_b64 s[42:43], s[42:43], exec
	s_cselect_b32 s42, s28, s36
	s_cselect_b32 s43, s29, s37
	s_add_u32 s42, s42, s74
	s_addc_u32 s43, s43, s71
	global_load_lds_dwordx4 v[186:187], off
	v_lshl_add_u64 v[186:187], s[42:43], 0, v[166:167]
	s_mov_b32 m0, s35
	v_lshl_add_u64 v[188:189], s[42:43], 0, v[168:169]
	global_load_lds_dwordx4 v[186:187], off
	s_mov_b32 m0, s47
	s_nop 0
	global_load_lds_dwordx4 v[188:189], off
	s_waitcnt vmcnt(8)
	s_waitcnt lgkmcnt(0)
	s_barrier
	s_setprio 1
	s_waitcnt lgkmcnt(0)
	v_mfma_scale_f32_16x16x128_f8f6f4 v[94:97], v[18:25], v[198:205], v[94:97], v1, v1 op_sel_hi:[0,0,0]
	v_mfma_scale_f32_16x16x128_f8f6f4 v[90:93], v[26:33], v[198:205], v[90:93], v1, v1 op_sel_hi:[0,0,0]
	v_mfma_scale_f32_16x16x128_f8f6f4 v[86:89], v[18:25], v[206:213], v[86:89], v1, v1 op_sel_hi:[0,0,0]
	v_mfma_scale_f32_16x16x128_f8f6f4 v[78:81], v[26:33], v[206:213], v[78:81], v1, v1 op_sel_hi:[0,0,0]
	v_mfma_scale_f32_16x16x128_f8f6f4 v[62:65], v[18:25], v[214:221], v[62:65], v1, v1 op_sel_hi:[0,0,0]
	v_mfma_scale_f32_16x16x128_f8f6f4 v[54:57], v[26:33], v[214:221], v[54:57], v1, v1 op_sel_hi:[0,0,0]
	v_mfma_scale_f32_16x16x128_f8f6f4 v[46:49], v[18:25], v[222:229], v[46:49], v1, v1 op_sel_hi:[0,0,0]
	v_mfma_scale_f32_16x16x128_f8f6f4 v[38:41], v[26:33], v[222:229], v[38:41], v1, v1 op_sel_hi:[0,0,0]
	s_setprio 0
	s_setprio 1
	v_mfma_scale_f32_16x16x128_f8f6f4 v[82:85], v[2:9], v[198:205], v[82:85], v1, v1 op_sel_hi:[0,0,0]
	v_mfma_scale_f32_16x16x128_f8f6f4 v[74:77], v[10:17], v[198:205], v[74:77], v1, v1 op_sel_hi:[0,0,0]
	v_mfma_scale_f32_16x16x128_f8f6f4 v[58:61], v[2:9], v[206:213], v[58:61], v1, v1 op_sel_hi:[0,0,0]
	v_mfma_scale_f32_16x16x128_f8f6f4 v[50:53], v[10:17], v[206:213], v[50:53], v1, v1 op_sel_hi:[0,0,0]
	v_mfma_scale_f32_16x16x128_f8f6f4 v[42:45], v[2:9], v[214:221], v[42:45], v1, v1 op_sel_hi:[0,0,0]
	v_mfma_scale_f32_16x16x128_f8f6f4 v[34:37], v[10:17], v[214:221], v[34:37], v1, v1 op_sel_hi:[0,0,0]
	v_mfma_scale_f32_16x16x128_f8f6f4 v[70:73], v[2:9], v[222:229], v[70:73], v1, v1 op_sel_hi:[0,0,0]
	v_mfma_scale_f32_16x16x128_f8f6f4 v[66:69], v[10:17], v[222:229], v[66:69], v1, v1 op_sel_hi:[0,0,0]
	s_setprio 0
	s_barrier
; #define PG8_STAGE(bufoff, gbase, voff) do { _Pragma("unroll") for (int _i = 0; _i < 2; ++_i) \
;         __builtin_amdgcn_global_load_lds((const unsigned*)((const char*)(gbase) + (voff)[_i]), (LAS unsigned*)(lds + (bufoff) + ldsw + _i * 8192), 16, 0, 0); } while (0)
; #define PG8_LDA(dst, b, h) do { _Pragma("unroll") for (int m = 0; m < 4; ++m) dst[m] = PG8_LD32(lds + PG8_SA(b, h) + aoff + m * 2048); } while (0)
; #define PG8_LDB(dst, b, h) do { _Pragma("unroll") for (int n = 0; n < 2; ++n) dst[n] = PG8_LD32(lds + PG8_SB(b, h) + boff + n * 2048); } while (0)
; #define PG8_WAIT_V(n) asm volatile("s_waitcnt vmcnt(" #n ")" ::: "memory")
; #define PG8_WAIT_L(n) asm volatile("s_waitcnt lgkmcnt(" #n ")" ::: "memory")
; #define PG8_BAR __builtin_amdgcn_s_barrier()
; #define PG8_SCHED __builtin_amdgcn_sched_barrier(0)
; #define PG8_STA(bufoff, nextflag, h, koff) do { if constexpr (Sched::GATHER) { unsigned _o[2]; _o[0] = (nextflag) ? nxtA[h][0] : curA[h][0]; _o[1] = (nextflag) ? nxtA[h][1] : curA[h][1]; PG8_STAGE(bufoff, Ab + (koff), _o); } \
;         else { PG8_STAGE(bufoff, ((nextflag) ? nA : cA) + (size_t)(h) * hstep + (koff), voffA); } } while (0)
; template <class Epi, class Sched, bool ALIGN_EPI, int DT>
; __device__ __forceinline__ void gemm_phase(LAS unsigned char* lds, const int KB, const Sched& S, const Epi& E) {
;     ...
;             PG8_LDB(B0, 1, 0); PG8_LDB(B1, 1, 1); PG8_SCHED; PG8_LDA(At, 1, 0); PG8_STA(PG8_SA(0, 1), last, 1, k2);
;             PG8_WAIT_V(8); PG8_WAIT_L(0); PG8_BAR; PG8_MMA(0, 0, At, B0); PG8_MMA(0, 1, At, B1); PG8_BAR; PG8_SCHED;
;             PG8_LDA(At, 1, 1); PG8_STAGE(PG8_SB(1, 0), b3, voffB); PG8_STAGE(PG8_SB(1, 1), b3 + hstep, voffB); PG8_STA(PG8_SA(1, 0), last, 0, k3);
;             PG8_WAIT_V(8); PG8_WAIT_L(0); PG8_BAR; PG8_MMA(1, 0, At, B0); PG8_MMA(1, 1, At, B1); PG8_BAR; PG8_SCHED;
	s_add_i32 s44, 0, 0x18000
	s_add_i32 s45, 0, 0x1c000
	v_add_u32_e32 v14, s44, v191
	v_add_u32_e32 v30, s45, v191
	ds_read_b128 v[2:5], v14
	ds_read_b128 v[6:9], v14 offset:1024
	ds_read_b128 v[10:13], v14 offset:2048
	ds_read_b128 v[14:17], v14 offset:3072
	ds_read_b128 v[18:21], v30
	ds_read_b128 v[22:25], v30 offset:1024
	ds_read_b128 v[26:29], v30 offset:2048
	ds_read_b128 v[30:33], v30 offset:3072
	s_add_u32 s42, s42, 0x40000
	s_addc_u32 s43, s43, 0
	s_mov_b32 m0, s49
	v_lshl_add_u64 v[230:231], s[42:43], 0, v[166:167]
	ds_read_b128 v[198:201], v196 offset:32768
	ds_read_b128 v[202:205], v196 offset:33792
	ds_read_b128 v[206:209], v196 offset:34816
	ds_read_b128 v[210:213], v196 offset:35840
	ds_read_b128 v[214:217], v196 offset:36864
	ds_read_b128 v[218:221], v196 offset:37888
	ds_read_b128 v[222:225], v196 offset:38912
	ds_read_b128 v[226:229], v196 offset:39936
	global_load_lds_dwordx4 v[230:231], off
	v_lshl_add_u64 v[230:231], s[42:43], 0, v[168:169]
	s_mov_b32 m0, s52
	s_nop 0
	global_load_lds_dwordx4 v[230:231], off
	s_add_i32 s42, s44, s46
	v_lshl_add_u64 v[182:183], v[182:183], 0, s[10:11]
	s_mov_b32 m0, s42
	s_waitcnt vmcnt(8)
	s_waitcnt lgkmcnt(0)
	s_barrier
	s_setprio 1
	s_waitcnt lgkmcnt(0)
	v_mfma_scale_f32_16x16x128_f8f6f4 v[158:161], v[2:9], v[198:205], v[158:161], v1, v1 op_sel_hi:[0,0,0]
	v_mfma_scale_f32_16x16x128_f8f6f4 v[154:157], v[10:17], v[198:205], v[154:157], v1, v1 op_sel_hi:[0,0,0]
	v_mfma_scale_f32_16x16x128_f8f6f4 v[150:153], v[2:9], v[206:213], v[150:153], v1, v1 op_sel_hi:[0,0,0]
	v_mfma_scale_f32_16x16x128_f8f6f4 v[142:145], v[10:17], v[206:213], v[142:145], v1, v1 op_sel_hi:[0,0,0]
	v_mfma_scale_f32_16x16x128_f8f6f4 v[134:137], v[2:9], v[214:221], v[134:137], v1, v1 op_sel_hi:[0,0,0]
	v_mfma_scale_f32_16x16x128_f8f6f4 v[126:129], v[10:17], v[214:221], v[126:129], v1, v1 op_sel_hi:[0,0,0]
	v_mfma_scale_f32_16x16x128_f8f6f4 v[118:121], v[2:9], v[222:229], v[118:121], v1, v1 op_sel_hi:[0,0,0]
	v_mfma_scale_f32_16x16x128_f8f6f4 v[110:113], v[10:17], v[222:229], v[110:113], v1, v1 op_sel_hi:[0,0,0]
	s_setprio 0
	s_setprio 1
	v_mfma_scale_f32_16x16x128_f8f6f4 v[146:149], v[18:25], v[198:205], v[146:149], v1, v1 op_sel_hi:[0,0,0]
	v_mfma_scale_f32_16x16x128_f8f6f4 v[138:141], v[26:33], v[198:205], v[138:141], v1, v1 op_sel_hi:[0,0,0]
	v_mfma_scale_f32_16x16x128_f8f6f4 v[130:133], v[18:25], v[206:213], v[130:133], v1, v1 op_sel_hi:[0,0,0]
	v_mfma_scale_f32_16x16x128_f8f6f4 v[122:125], v[26:33], v[206:213], v[122:125], v1, v1 op_sel_hi:[0,0,0]
	v_mfma_scale_f32_16x16x128_f8f6f4 v[114:117], v[18:25], v[214:221], v[114:117], v1, v1 op_sel_hi:[0,0,0]
	v_mfma_scale_f32_16x16x128_f8f6f4 v[106:109], v[26:33], v[214:221], v[106:109], v1, v1 op_sel_hi:[0,0,0]
	v_mfma_scale_f32_16x16x128_f8f6f4 v[102:105], v[18:25], v[222:229], v[102:105], v1, v1 op_sel_hi:[0,0,0]
	v_mfma_scale_f32_16x16x128_f8f6f4 v[98:101], v[26:33], v[222:229], v[98:101], v1, v1 op_sel_hi:[0,0,0]
	s_setprio 0
	s_barrier
	ds_read_b128 v[198:201], v196 offset:49152
	ds_read_b128 v[202:205], v196 offset:50176
	ds_read_b128 v[206:209], v196 offset:51200
	ds_read_b128 v[210:213], v196 offset:52224
	ds_read_b128 v[214:217], v196 offset:53248
	ds_read_b128 v[218:221], v196 offset:54272
	ds_read_b128 v[222:225], v196 offset:55296
	ds_read_b128 v[226:229], v196 offset:56320
	global_load_lds_dwordx4 v[182:183], off
	s_add_i32 m0, s42, 0x2000
	s_add_u32 s40, s40, 0x40080
	v_lshl_add_u64 v[182:183], v[184:185], 0, s[10:11]
	s_addc_u32 s41, s41, 0
	s_add_i32 s42, s45, s46
	global_load_lds_dwordx4 v[182:183], off
	v_lshl_add_u64 v[182:183], s[40:41], 0, v[162:163]
	s_mov_b32 m0, s42
	s_nop 0
	global_load_lds_dwordx4 v[182:183], off
	v_lshl_add_u64 v[182:183], s[40:41], 0, v[164:165]
	s_add_i32 m0, s42, 0x2000
	s_nop 0
	global_load_lds_dwordx4 v[182:183], off
	v_lshl_add_u64 v[182:183], v[186:187], 0, s[10:11]
	s_mov_b32 m0, s54
	s_nop 0
	global_load_lds_dwordx4 v[182:183], off
	v_lshl_add_u64 v[182:183], v[188:189], 0, s[10:11]
	s_mov_b32 m0, s55
	s_nop 0
	global_load_lds_dwordx4 v[182:183], off
	s_waitcnt vmcnt(8)
	s_waitcnt lgkmcnt(0)
	s_barrier
	s_setprio 1
	s_waitcnt lgkmcnt(0)
	v_mfma_scale_f32_16x16x128_f8f6f4 v[94:97], v[2:9], v[198:205], v[94:97], v1, v1 op_sel_hi:[0,0,0]
	v_mfma_scale_f32_16x16x128_f8f6f4 v[90:93], v[10:17], v[198:205], v[90:93], v1, v1 op_sel_hi:[0,0,0]
	v_mfma_scale_f32_16x16x128_f8f6f4 v[86:89], v[2:9], v[206:213], v[86:89], v1, v1 op_sel_hi:[0,0,0]
	v_mfma_scale_f32_16x16x128_f8f6f4 v[78:81], v[10:17], v[206:213], v[78:81], v1, v1 op_sel_hi:[0,0,0]
	v_mfma_scale_f32_16x16x128_f8f6f4 v[62:65], v[2:9], v[214:221], v[62:65], v1, v1 op_sel_hi:[0,0,0]
	v_mfma_scale_f32_16x16x128_f8f6f4 v[54:57], v[10:17], v[214:221], v[54:57], v1, v1 op_sel_hi:[0,0,0]
	v_mfma_scale_f32_16x16x128_f8f6f4 v[46:49], v[2:9], v[222:229], v[46:49], v1, v1 op_sel_hi:[0,0,0]
	v_mfma_scale_f32_16x16x128_f8f6f4 v[38:41], v[10:17], v[222:229], v[38:41], v1, v1 op_sel_hi:[0,0,0]
	s_setprio 0
	s_setprio 1
	v_mfma_scale_f32_16x16x128_f8f6f4 v[82:85], v[18:25], v[198:205], v[82:85], v1, v1 op_sel_hi:[0,0,0]
	v_mfma_scale_f32_16x16x128_f8f6f4 v[74:77], v[26:33], v[198:205], v[74:77], v1, v1 op_sel_hi:[0,0,0]
	v_mfma_scale_f32_16x16x128_f8f6f4 v[58:61], v[18:25], v[206:213], v[58:61], v1, v1 op_sel_hi:[0,0,0]
	v_mfma_scale_f32_16x16x128_f8f6f4 v[50:53], v[26:33], v[206:213], v[50:53], v1, v1 op_sel_hi:[0,0,0]
	v_mfma_scale_f32_16x16x128_f8f6f4 v[42:45], v[18:25], v[214:221], v[42:45], v1, v1 op_sel_hi:[0,0,0]
	v_mfma_scale_f32_16x16x128_f8f6f4 v[34:37], v[26:33], v[214:221], v[34:37], v1, v1 op_sel_hi:[0,0,0]
	v_mfma_scale_f32_16x16x128_f8f6f4 v[70:73], v[18:25], v[222:229], v[70:73], v1, v1 op_sel_hi:[0,0,0]
	v_mfma_scale_f32_16x16x128_f8f6f4 v[66:69], v[26:33], v[222:229], v[66:69], v1, v1 op_sel_hi:[0,0,0]
	s_setprio 0
	s_barrier
	s_add_i32 s70, s70, 2
	s_cmp_gt_u32 s70, 13
	s_mov_b64 s[42:43], s[38:39]
	s_cbranch_scc0 .LBB0_2108
	s_and_b64 vcc, exec, s[12:13]
	s_cbranch_vccz .LBB0_2111
	s_barrier

; #define PG8_STAGE(bufoff, gbase, voff) do { _Pragma("unroll") for (int _i = 0; _i < 2; ++_i) \
;         __builtin_amdgcn_global_load_lds((const unsigned*)((const char*)(gbase) + (voff)[_i]), (LAS unsigned*)(lds + (bufoff) + ldsw + _i * 8192), 16, 0, 0); } while (0)
; #define PG8_LDA(dst, b, h) do { _Pragma("unroll") for (int m = 0; m < 4; ++m) dst[m] = PG8_LD32(lds + PG8_SA(b, h) + aoff + m * 2048); } while (0)
; #define PG8_LDB(dst, b, h) do { _Pragma("unroll") for (int n = 0; n < 2; ++n) dst[n] = PG8_LD32(lds + PG8_SB(b, h) + boff + n * 2048); } while (0)
; #define PG8_WAIT_V(n) asm volatile("s_waitcnt vmcnt(" #n ")" ::: "memory")
; #define PG8_WAIT_L(n) asm volatile("s_waitcnt lgkmcnt(" #n ")" ::: "memory")
; #define PG8_BAR __builtin_amdgcn_s_barrier()
; #define PG8_SCHED __builtin_amdgcn_sched_barrier(0)
; #define PG8_STA(bufoff, nextflag, h, koff) do { if constexpr (Sched::GATHER) { unsigned _o[2]; _o[0] = (nextflag) ? nxtA[h][0] : curA[h][0]; _o[1] = (nextflag) ? nxtA[h][1] : curA[h][1]; PG8_STAGE(bufoff, Ab + (koff), _o); } \
;         else { PG8_STAGE(bufoff, ((nextflag) ? nA : cA) + (size_t)(h) * hstep + (koff), voffA); } } while (0)
; template <class Epi, class Sched, bool ALIGN_EPI, int DT>
; __device__ __forceinline__ void gemm_phase(LAS unsigned char* lds, const int KB, const Sched& S, const Epi& E) {
;     ...
;             PG8_LDB(B0, 0, 0); PG8_LDB(B1, 0, 1); PG8_SCHED; PG8_LDA(At, 0, 0); PG8_STA(PG8_SA(1, 1), false, 1, k1);
;             PG8_WAIT_V(8); PG8_WAIT_L(0); PG8_BAR; PG8_MMA(0, 0, At, B0); PG8_MMA(0, 1, At, B1); PG8_BAR; PG8_SCHED;
;             PG8_LDA(At, 0, 1); PG8_STAGE(PG8_SB(0, 0), b2, voffB); PG8_STAGE(PG8_SB(0, 1), b2 + hstep, voffB); PG8_STA(PG8_SA(0, 0), last, 0, k2);
;             PG8_WAIT_V(8); PG8_WAIT_L(0); PG8_BAR; PG8_MMA(1, 0, At, B0); PG8_MMA(1, 1, At, B1); PG8_BAR; PG8_SCHED;
.LBB0_2294:
	v_add_u32_e32 v79, s65, v167
	ds_read_b128 v[142:145], v79
	ds_read_b128 v[156:159], v79 offset:1024
	ds_read_b128 v[178:181], v79 offset:2048
	ds_read_b128 v[182:185], v79 offset:3072
	v_add_u32_e32 v79, s66, v167
	ds_read_b128 v[186:189], v79
	ds_read_b128 v[190:193], v79 offset:1024
	ds_read_b128 v[196:199], v79 offset:2048
	ds_read_b128 v[200:203], v79 offset:3072
	s_add_u32 s40, s8, 0x100
	s_addc_u32 s41, s9, 0
	s_cmpk_eq_i32 s8, 0x700
	s_cselect_b64 vcc, -1, 0
	v_lshl_add_u64 v[160:161], v[88:89], 0, s[8:9]
	s_and_b64 s[76:77], vcc, exec
	v_cndmask_b32_e32 v161, v161, v155, vcc
	s_cselect_b32 s75, 0, s40
	v_cndmask_b32_e32 v160, v160, v154, vcc
	v_lshl_add_u64 v[236:237], v[140:141], 0, s[8:9]
	s_add_i32 m0, s42, 0xc000
	ds_read_b128 v[204:207], v169
	ds_read_b128 v[208:211], v169 offset:1024
	ds_read_b128 v[212:215], v169 offset:2048
	ds_read_b128 v[216:219], v169 offset:3072
	ds_read_b128 v[220:223], v169 offset:4096
	ds_read_b128 v[224:227], v169 offset:5120
	ds_read_b128 v[228:231], v169 offset:6144
	ds_read_b128 v[232:235], v169 offset:7168
	global_load_lds_dwordx4 v[236:237], off
	v_lshl_add_u64 v[236:237], v[138:139], 0, s[8:9]
	s_add_i32 m0, s42, 0xe000
	s_nop 0
	global_load_lds_dwordx4 v[236:237], off
	s_add_i32 s8, s65, s33
	v_lshl_add_u64 v[236:237], v[160:161], 0, v[148:149]
	s_mov_b32 m0, s8
	s_waitcnt vmcnt(8)
	s_waitcnt lgkmcnt(0)
	s_barrier
	s_setprio 1
	s_waitcnt lgkmcnt(0)
	v_mfma_i32_16x16x64_i8 v[134:137], v[142:145], v[204:207], v[134:137]
	v_mfma_i32_16x16x64_i8 v[126:129], v[178:181], v[204:207], v[126:129]
	v_mfma_i32_16x16x64_i8 v[118:121], v[142:145], v[212:215], v[118:121]
	v_mfma_i32_16x16x64_i8 v[110:113], v[178:181], v[212:215], v[110:113]
	v_mfma_i32_16x16x64_i8 v[102:105], v[142:145], v[220:223], v[102:105]
	v_mfma_i32_16x16x64_i8 v[94:97], v[178:181], v[220:223], v[94:97]
	v_mfma_i32_16x16x64_i8 v[82:85], v[142:145], v[228:231], v[82:85]
	v_mfma_i32_16x16x64_i8 v[70:73], v[178:181], v[228:231], v[70:73]
	v_mfma_i32_16x16x64_i8 v[134:137], v[156:159], v[208:211], v[134:137]
	v_mfma_i32_16x16x64_i8 v[126:129], v[182:185], v[208:211], v[126:129]
	v_mfma_i32_16x16x64_i8 v[118:121], v[156:159], v[216:219], v[118:121]
	v_mfma_i32_16x16x64_i8 v[110:113], v[182:185], v[216:219], v[110:113]
	v_mfma_i32_16x16x64_i8 v[102:105], v[156:159], v[224:227], v[102:105]
	v_mfma_i32_16x16x64_i8 v[94:97], v[182:185], v[224:227], v[94:97]
	v_mfma_i32_16x16x64_i8 v[82:85], v[156:159], v[232:235], v[82:85]
	v_mfma_i32_16x16x64_i8 v[70:73], v[182:185], v[232:235], v[70:73]
	s_setprio 0
	s_setprio 1
	v_mfma_i32_16x16x64_i8 v[130:133], v[186:189], v[204:207], v[130:133]
	v_mfma_i32_16x16x64_i8 v[122:125], v[196:199], v[204:207], v[122:125]
	v_mfma_i32_16x16x64_i8 v[114:117], v[186:189], v[212:215], v[114:117]
	v_mfma_i32_16x16x64_i8 v[106:109], v[196:199], v[212:215], v[106:109]
	v_mfma_i32_16x16x64_i8 v[98:101], v[186:189], v[220:223], v[98:101]
	v_mfma_i32_16x16x64_i8 v[90:93], v[196:199], v[220:223], v[90:93]
	v_mfma_i32_16x16x64_i8 v[74:77], v[186:189], v[228:231], v[74:77]
	v_mfma_i32_16x16x64_i8 v[66:69], v[196:199], v[228:231], v[66:69]
	v_mfma_i32_16x16x64_i8 v[130:133], v[190:193], v[208:211], v[130:133]
	v_mfma_i32_16x16x64_i8 v[122:125], v[200:203], v[208:211], v[122:125]
	v_mfma_i32_16x16x64_i8 v[114:117], v[190:193], v[216:219], v[114:117]
	v_mfma_i32_16x16x64_i8 v[106:109], v[200:203], v[216:219], v[106:109]
	v_mfma_i32_16x16x64_i8 v[98:101], v[190:193], v[224:227], v[98:101]
	v_mfma_i32_16x16x64_i8 v[90:93], v[200:203], v[224:227], v[90:93]
	v_mfma_i32_16x16x64_i8 v[74:77], v[190:193], v[232:235], v[74:77]
	v_mfma_i32_16x16x64_i8 v[66:69], v[200:203], v[232:235], v[66:69]
	s_setprio 0
	s_barrier
	ds_read_b128 v[204:207], v169 offset:16384
	ds_read_b128 v[208:211], v169 offset:17408
	ds_read_b128 v[212:215], v169 offset:18432
	ds_read_b128 v[216:219], v169 offset:19456
	ds_read_b128 v[220:223], v169 offset:20480
	ds_read_b128 v[224:227], v169 offset:21504
	ds_read_b128 v[228:231], v169 offset:22528
	ds_read_b128 v[232:235], v169 offset:23552
	global_load_lds_dwordx4 v[236:237], off
	v_lshl_add_u64 v[238:239], v[160:161], 0, v[150:151]
	s_add_i32 m0, s8, 0x2000
	v_lshl_add_u64 v[240:241], v[160:161], 0, s[10:11]
	s_add_i32 s8, s66, s33
	global_load_lds_dwordx4 v[238:239], off
	v_lshl_add_u64 v[242:243], v[240:241], 0, v[148:149]
	s_mov_b32 m0, s8
	v_lshl_add_u64 v[240:241], v[240:241], 0, v[150:151]
	global_load_lds_dwordx4 v[242:243], off
	s_add_i32 m0, s8, 0x2000
	s_add_u32 s8, s60, s75
	global_load_lds_dwordx4 v[240:241], off
	v_cndmask_b32_e32 v146, v81, v173, vcc
	s_addc_u32 s9, s61, 0
	s_mov_b32 m0, s42
	v_cndmask_b32_e32 v240, v80, v174, vcc
	global_load_lds_dwordx4 v146, s[8:9]
	s_mov_b32 m0, s43
	v_mov_b32_e32 v241, v147
	global_load_lds_dwordx4 v240, s[8:9]
	s_add_i32 s75, 0, 0x18000
	v_add_u32_e32 v79, s75, v167
	s_add_i32 s76, 0, 0x1c000
	s_waitcnt vmcnt(8)
	s_waitcnt lgkmcnt(0)
	v_lshl_add_u64 v[242:243], s[8:9], 0, v[146:147]
	v_lshl_add_u64 v[240:241], s[8:9], 0, v[240:241]
	s_barrier
; #define PG8_STAGE(bufoff, gbase, voff) do { _Pragma("unroll") for (int _i = 0; _i < 2; ++_i) \
;         __builtin_amdgcn_global_load_lds((const unsigned*)((const char*)(gbase) + (voff)[_i]), (LAS unsigned*)(lds + (bufoff) + ldsw + _i * 8192), 16, 0, 0); } while (0)
; #define PG8_LDA(dst, b, h) do { _Pragma("unroll") for (int m = 0; m < 4; ++m) dst[m] = PG8_LD32(lds + PG8_SA(b, h) + aoff + m * 2048); } while (0)
; #define PG8_LDB(dst, b, h) do { _Pragma("unroll") for (int n = 0; n < 2; ++n) dst[n] = PG8_LD32(lds + PG8_SB(b, h) + boff + n * 2048); } while (0)
; #define PG8_WAIT_V(n) asm volatile("s_waitcnt vmcnt(" #n ")" ::: "memory")
; #define PG8_WAIT_L(n) asm volatile("s_waitcnt lgkmcnt(" #n ")" ::: "memory")
; #define PG8_BAR __builtin_amdgcn_s_barrier()
; #define PG8_SCHED __builtin_amdgcn_sched_barrier(0)
; #define PG8_STA(bufoff, nextflag, h, koff) do { if constexpr (Sched::GATHER) { unsigned _o[2]; _o[0] = (nextflag) ? nxtA[h][0] : curA[h][0]; _o[1] = (nextflag) ? nxtA[h][1] : curA[h][1]; PG8_STAGE(bufoff, Ab + (koff), _o); } \
;         else { PG8_STAGE(bufoff, ((nextflag) ? nA : cA) + (size_t)(h) * hstep + (koff), voffA); } } while (0)
; template <class Epi, class Sched, bool ALIGN_EPI, int DT>
; __device__ __forceinline__ void gemm_phase(LAS unsigned char* lds, const int KB, const Sched& S, const Epi& E) {
;     ...
;             PG8_LDA(At, 0, 1); PG8_STAGE(PG8_SB(0, 0), b2, voffB); PG8_STAGE(PG8_SB(0, 1), b2 + hstep, voffB); PG8_STA(PG8_SA(0, 0), last, 0, k2);
;             PG8_WAIT_V(8); PG8_WAIT_L(0); PG8_BAR; PG8_MMA(1, 0, At, B0); PG8_MMA(1, 1, At, B1); PG8_BAR; PG8_SCHED;
;             PG8_LDB(B0, 1, 0); PG8_LDB(B1, 1, 1); PG8_SCHED; PG8_LDA(At, 1, 0); PG8_STA(PG8_SA(0, 1), last, 1, k2);
;             PG8_WAIT_V(8); PG8_WAIT_L(0); PG8_BAR; PG8_MMA(0, 0, At, B0); PG8_MMA(0, 1, At, B1); PG8_BAR; PG8_SCHED;
	s_setprio 1
	s_waitcnt lgkmcnt(0)
	v_mfma_i32_16x16x64_i8 v[54:57], v[142:145], v[204:207], v[54:57]
	v_mfma_i32_16x16x64_i8 v[50:53], v[178:181], v[204:207], v[50:53]
	v_mfma_i32_16x16x64_i8 v[42:45], v[142:145], v[212:215], v[42:45]
	v_mfma_i32_16x16x64_i8 v[34:37], v[178:181], v[212:215], v[34:37]
	v_mfma_i32_16x16x64_i8 v[26:29], v[142:145], v[220:223], v[26:29]
	v_mfma_i32_16x16x64_i8 v[18:21], v[178:181], v[220:223], v[18:21]
	v_mfma_i32_16x16x64_i8 v[10:13], v[142:145], v[228:231], v[10:13]
	v_mfma_i32_16x16x64_i8 v[2:5], v[178:181], v[228:231], v[2:5]
	v_mfma_i32_16x16x64_i8 v[54:57], v[156:159], v[208:211], v[54:57]
	v_mfma_i32_16x16x64_i8 v[50:53], v[182:185], v[208:211], v[50:53]
	v_mfma_i32_16x16x64_i8 v[42:45], v[156:159], v[216:219], v[42:45]
	v_mfma_i32_16x16x64_i8 v[34:37], v[182:185], v[216:219], v[34:37]
	v_mfma_i32_16x16x64_i8 v[26:29], v[156:159], v[224:227], v[26:29]
	v_mfma_i32_16x16x64_i8 v[18:21], v[182:185], v[224:227], v[18:21]
	v_mfma_i32_16x16x64_i8 v[10:13], v[156:159], v[232:235], v[10:13]
	v_mfma_i32_16x16x64_i8 v[2:5], v[182:185], v[232:235], v[2:5]
	s_setprio 0
	s_setprio 1
	v_mfma_i32_16x16x64_i8 v[62:65], v[186:189], v[204:207], v[62:65]
	v_mfma_i32_16x16x64_i8 v[58:61], v[196:199], v[204:207], v[58:61]
	v_mfma_i32_16x16x64_i8 v[46:49], v[186:189], v[212:215], v[46:49]
	v_mfma_i32_16x16x64_i8 v[38:41], v[196:199], v[212:215], v[38:41]
	v_mfma_i32_16x16x64_i8 v[30:33], v[186:189], v[220:223], v[30:33]
	v_mfma_i32_16x16x64_i8 v[22:25], v[196:199], v[220:223], v[22:25]
	v_mfma_i32_16x16x64_i8 v[14:17], v[186:189], v[228:231], v[14:17]
	v_mfma_i32_16x16x64_i8 v[6:9], v[196:199], v[228:231], v[6:9]
	v_mfma_i32_16x16x64_i8 v[62:65], v[190:193], v[208:211], v[62:65]
	v_mfma_i32_16x16x64_i8 v[58:61], v[200:203], v[208:211], v[58:61]
	v_mfma_i32_16x16x64_i8 v[46:49], v[190:193], v[216:219], v[46:49]
	v_mfma_i32_16x16x64_i8 v[38:41], v[200:203], v[216:219], v[38:41]
	v_mfma_i32_16x16x64_i8 v[30:33], v[190:193], v[224:227], v[30:33]
	v_mfma_i32_16x16x64_i8 v[22:25], v[200:203], v[224:227], v[22:25]
	v_mfma_i32_16x16x64_i8 v[14:17], v[190:193], v[232:235], v[14:17]
	v_mfma_i32_16x16x64_i8 v[6:9], v[200:203], v[232:235], v[6:9]
	s_setprio 0
	s_barrier
	ds_read_b128 v[142:145], v79
	ds_read_b128 v[156:159], v79 offset:1024
	ds_read_b128 v[178:181], v79 offset:2048
	ds_read_b128 v[182:185], v79 offset:3072
	v_add_u32_e32 v79, s76, v167
	ds_read_b128 v[186:189], v79
	ds_read_b128 v[190:193], v79 offset:1024
	ds_read_b128 v[196:199], v79 offset:2048
	ds_read_b128 v[200:203], v79 offset:3072
	s_mov_b32 m0, s44
	v_cndmask_b32_e32 v79, v78, v175, vcc
	ds_read_b128 v[204:207], v169 offset:32768
	ds_read_b128 v[208:211], v169 offset:33792
	ds_read_b128 v[212:215], v169 offset:34816
	ds_read_b128 v[216:219], v169 offset:35840
	ds_read_b128 v[220:223], v169 offset:36864
	ds_read_b128 v[224:227], v169 offset:37888
	ds_read_b128 v[228:231], v169 offset:38912
	ds_read_b128 v[232:235], v169 offset:39936
	v_cndmask_b32_e32 v87, v86, v176, vcc
	global_load_lds_dwordx4 v79, s[8:9]
	s_mov_b32 m0, s45
	s_nop 0
	global_load_lds_dwordx4 v87, s[8:9]
	s_add_i32 s8, s75, s33
	v_lshl_add_u64 v[236:237], v[236:237], 0, s[20:21]
	s_mov_b32 m0, s8
	s_waitcnt vmcnt(8)
	s_waitcnt lgkmcnt(0)
	s_barrier
	s_setprio 1
	s_waitcnt lgkmcnt(0)
	v_mfma_i32_16x16x64_i8 v[134:137], v[142:145], v[204:207], v[134:137]
	v_mfma_i32_16x16x64_i8 v[126:129], v[178:181], v[204:207], v[126:129]
	v_mfma_i32_16x16x64_i8 v[118:121], v[142:145], v[212:215], v[118:121]
	v_mfma_i32_16x16x64_i8 v[110:113], v[178:181], v[212:215], v[110:113]
	v_mfma_i32_16x16x64_i8 v[102:105], v[142:145], v[220:223], v[102:105]
	v_mfma_i32_16x16x64_i8 v[94:97], v[178:181], v[220:223], v[94:97]
	v_mfma_i32_16x16x64_i8 v[82:85], v[142:145], v[228:231], v[82:85]
	v_mfma_i32_16x16x64_i8 v[70:73], v[178:181], v[228:231], v[70:73]
	v_mfma_i32_16x16x64_i8 v[134:137], v[156:159], v[208:211], v[134:137]
	v_mfma_i32_16x16x64_i8 v[126:129], v[182:185], v[208:211], v[126:129]
	v_mfma_i32_16x16x64_i8 v[118:121], v[156:159], v[216:219], v[118:121]
	v_mfma_i32_16x16x64_i8 v[110:113], v[182:185], v[216:219], v[110:113]
	v_mfma_i32_16x16x64_i8 v[102:105], v[156:159], v[224:227], v[102:105]
	v_mfma_i32_16x16x64_i8 v[94:97], v[182:185], v[224:227], v[94:97]
	v_mfma_i32_16x16x64_i8 v[82:85], v[156:159], v[232:235], v[82:85]
	v_mfma_i32_16x16x64_i8 v[70:73], v[182:185], v[232:235], v[70:73]
	s_setprio 0
	s_setprio 1
	v_mfma_i32_16x16x64_i8 v[130:133], v[186:189], v[204:207], v[130:133]
	v_mfma_i32_16x16x64_i8 v[122:125], v[196:199], v[204:207], v[122:125]
	v_mfma_i32_16x16x64_i8 v[114:117], v[186:189], v[212:215], v[114:117]
	v_mfma_i32_16x16x64_i8 v[106:109], v[196:199], v[212:215], v[106:109]
	v_mfma_i32_16x16x64_i8 v[98:101], v[186:189], v[220:223], v[98:101]
	v_mfma_i32_16x16x64_i8 v[90:93], v[196:199], v[220:223], v[90:93]
	v_mfma_i32_16x16x64_i8 v[74:77], v[186:189], v[228:231], v[74:77]
	v_mfma_i32_16x16x64_i8 v[66:69], v[196:199], v[228:231], v[66:69]
	v_mfma_i32_16x16x64_i8 v[130:133], v[190:193], v[208:211], v[130:133]
	v_mfma_i32_16x16x64_i8 v[122:125], v[200:203], v[208:211], v[122:125]
	v_mfma_i32_16x16x64_i8 v[114:117], v[190:193], v[216:219], v[114:117]
	v_mfma_i32_16x16x64_i8 v[106:109], v[200:203], v[216:219], v[106:109]
	v_mfma_i32_16x16x64_i8 v[98:101], v[190:193], v[224:227], v[98:101]
	v_mfma_i32_16x16x64_i8 v[90:93], v[200:203], v[224:227], v[90:93]
	v_mfma_i32_16x16x64_i8 v[74:77], v[190:193], v[232:235], v[74:77]
	v_mfma_i32_16x16x64_i8 v[66:69], v[200:203], v[232:235], v[66:69]
	s_setprio 0
	s_barrier
; #define PG8_STAGE(bufoff, gbase, voff) do { _Pragma("unroll") for (int _i = 0; _i < 2; ++_i) \
;         __builtin_amdgcn_global_load_lds((const unsigned*)((const char*)(gbase) + (voff)[_i]), (LAS unsigned*)(lds + (bufoff) + ldsw + _i * 8192), 16, 0, 0); } while (0)
; #define PG8_LDA(dst, b, h) do { _Pragma("unroll") for (int m = 0; m < 4; ++m) dst[m] = PG8_LD32(lds + PG8_SA(b, h) + aoff + m * 2048); } while (0)
; #define PG8_WAIT_V(n) asm volatile("s_waitcnt vmcnt(" #n ")" ::: "memory")
; #define PG8_WAIT_L(n) asm volatile("s_waitcnt lgkmcnt(" #n ")" ::: "memory")
; #define PG8_BAR __builtin_amdgcn_s_barrier()
; #define PG8_SCHED __builtin_amdgcn_sched_barrier(0)
; #define PG8_STA(bufoff, nextflag, h, koff) do { if constexpr (Sched::GATHER) { unsigned _o[2]; _o[0] = (nextflag) ? nxtA[h][0] : curA[h][0]; _o[1] = (nextflag) ? nxtA[h][1] : curA[h][1]; PG8_STAGE(bufoff, Ab + (koff), _o); } \
;         else { PG8_STAGE(bufoff, ((nextflag) ? nA : cA) + (size_t)(h) * hstep + (koff), voffA); } } while (0)
; template <class Epi, class Sched, bool ALIGN_EPI, int DT>
; __device__ __forceinline__ void gemm_phase(LAS unsigned char* lds, const int KB, const Sched& S, const Epi& E) {
;     ...
;             PG8_LDA(At, 1, 1); PG8_STAGE(PG8_SB(1, 0), b3, voffB); PG8_STAGE(PG8_SB(1, 1), b3 + hstep, voffB); PG8_STA(PG8_SA(1, 0), last, 0, k3);
;             PG8_WAIT_V(8); PG8_WAIT_L(0); PG8_BAR; PG8_MMA(1, 0, At, B0); PG8_MMA(1, 1, At, B1); PG8_BAR; PG8_SCHED;
	ds_read_b128 v[204:207], v169 offset:49152
	ds_read_b128 v[208:211], v169 offset:50176
	ds_read_b128 v[212:215], v169 offset:51200
	ds_read_b128 v[216:219], v169 offset:52224
	ds_read_b128 v[220:223], v169 offset:53248
	ds_read_b128 v[224:227], v169 offset:54272
	ds_read_b128 v[228:231], v169 offset:55296
	ds_read_b128 v[232:235], v169 offset:56320
	global_load_lds_dwordx4 v[236:237], off
	v_lshl_add_u64 v[236:237], v[238:239], 0, s[20:21]
	s_add_i32 m0, s8, 0x2000
	v_lshl_add_u64 v[160:161], v[160:161], 0, s[24:25]
	s_add_i32 s8, s76, s33
	global_load_lds_dwordx4 v[236:237], off
	v_lshl_add_u64 v[236:237], v[160:161], 0, v[148:149]
	s_mov_b32 m0, s8
	v_lshl_add_u64 v[160:161], v[160:161], 0, v[150:151]
	global_load_lds_dwordx4 v[236:237], off
	s_add_i32 m0, s8, 0x2000
	s_nop 0
	global_load_lds_dwordx4 v[160:161], off
	v_lshl_add_u64 v[160:161], v[242:243], 0, s[20:21]
	s_mov_b32 m0, s46
	s_nop 0
	global_load_lds_dwordx4 v[160:161], off
	v_lshl_add_u64 v[160:161], v[240:241], 0, s[20:21]
	s_mov_b32 m0, s47
	s_nop 0
	global_load_lds_dwordx4 v[160:161], off
	s_waitcnt vmcnt(8)
	s_waitcnt lgkmcnt(0)
	s_barrier
	s_setprio 1
	s_waitcnt lgkmcnt(0)
	v_mfma_i32_16x16x64_i8 v[54:57], v[142:145], v[204:207], v[54:57]
	v_mfma_i32_16x16x64_i8 v[50:53], v[178:181], v[204:207], v[50:53]
	v_mfma_i32_16x16x64_i8 v[42:45], v[142:145], v[212:215], v[42:45]
	v_mfma_i32_16x16x64_i8 v[34:37], v[178:181], v[212:215], v[34:37]
	v_mfma_i32_16x16x64_i8 v[26:29], v[142:145], v[220:223], v[26:29]
	v_mfma_i32_16x16x64_i8 v[18:21], v[178:181], v[220:223], v[18:21]
	v_mfma_i32_16x16x64_i8 v[10:13], v[142:145], v[228:231], v[10:13]
	v_mfma_i32_16x16x64_i8 v[2:5], v[178:181], v[228:231], v[2:5]
	v_mfma_i32_16x16x64_i8 v[54:57], v[156:159], v[208:211], v[54:57]
	v_mfma_i32_16x16x64_i8 v[50:53], v[182:185], v[208:211], v[50:53]
	v_mfma_i32_16x16x64_i8 v[42:45], v[156:159], v[216:219], v[42:45]
	v_mfma_i32_16x16x64_i8 v[34:37], v[182:185], v[216:219], v[34:37]
	v_mfma_i32_16x16x64_i8 v[26:29], v[156:159], v[224:227], v[26:29]
	v_mfma_i32_16x16x64_i8 v[18:21], v[182:185], v[224:227], v[18:21]
	v_mfma_i32_16x16x64_i8 v[10:13], v[156:159], v[232:235], v[10:13]
	v_mfma_i32_16x16x64_i8 v[2:5], v[182:185], v[232:235], v[2:5]
	s_setprio 0
	s_setprio 1
	v_mfma_i32_16x16x64_i8 v[62:65], v[186:189], v[204:207], v[62:65]
	v_mfma_i32_16x16x64_i8 v[58:61], v[196:199], v[204:207], v[58:61]
	v_mfma_i32_16x16x64_i8 v[46:49], v[186:189], v[212:215], v[46:49]
	v_mfma_i32_16x16x64_i8 v[38:41], v[196:199], v[212:215], v[38:41]
	v_mfma_i32_16x16x64_i8 v[30:33], v[186:189], v[220:223], v[30:33]
	v_mfma_i32_16x16x64_i8 v[22:25], v[196:199], v[220:223], v[22:25]
	v_mfma_i32_16x16x64_i8 v[14:17], v[186:189], v[228:231], v[14:17]
	v_mfma_i32_16x16x64_i8 v[6:9], v[196:199], v[228:231], v[6:9]
	v_mfma_i32_16x16x64_i8 v[62:65], v[190:193], v[208:211], v[62:65]
	v_mfma_i32_16x16x64_i8 v[58:61], v[200:203], v[208:211], v[58:61]
	v_mfma_i32_16x16x64_i8 v[46:49], v[190:193], v[216:219], v[46:49]
	v_mfma_i32_16x16x64_i8 v[38:41], v[200:203], v[216:219], v[38:41]
	v_mfma_i32_16x16x64_i8 v[30:33], v[190:193], v[224:227], v[30:33]
	v_mfma_i32_16x16x64_i8 v[22:25], v[200:203], v[224:227], v[22:25]
	v_mfma_i32_16x16x64_i8 v[14:17], v[190:193], v[232:235], v[14:17]
	v_mfma_i32_16x16x64_i8 v[6:9], v[200:203], v[232:235], v[6:9]
	s_setprio 0
	s_barrier
	s_add_i32 s37, s37, 2
	s_cmp_gt_u32 s37, 13
	s_mov_b64 s[8:9], s[40:41]
	s_cbranch_scc0 .LBB0_2294
	s_and_b64 vcc, exec, s[26:27]
	s_cbranch_vccz .LBB0_2297
	s_barrier

; #define PG8_STAGE(bufoff, gbase, voff) do { _Pragma("unroll") for (int _i = 0; _i < 2; ++_i) \
;         __builtin_amdgcn_global_load_lds((const unsigned*)((const char*)(gbase) + (voff)[_i]), (LAS unsigned*)(lds + (bufoff) + ldsw + _i * 8192), 16, 0, 0); } while (0)
; #define PG8_LDA(dst, b, h) do { _Pragma("unroll") for (int m = 0; m < 4; ++m) dst[m] = PG8_LD32(lds + PG8_SA(b, h) + aoff + m * 2048); } while (0)
; #define PG8_LDB(dst, b, h) do { _Pragma("unroll") for (int n = 0; n < 2; ++n) dst[n] = PG8_LD32(lds + PG8_SB(b, h) + boff + n * 2048); } while (0)
; #define PG8_WAIT_V(n) asm volatile("s_waitcnt vmcnt(" #n ")" ::: "memory")
; #define PG8_WAIT_L(n) asm volatile("s_waitcnt lgkmcnt(" #n ")" ::: "memory")
; #define PG8_BAR __builtin_amdgcn_s_barrier()
; #define PG8_SCHED __builtin_amdgcn_sched_barrier(0)
; #define PG8_STA(bufoff, nextflag, h, koff) do { if constexpr (Sched::GATHER) { unsigned _o[2]; _o[0] = (nextflag) ? nxtA[h][0] : curA[h][0]; _o[1] = (nextflag) ? nxtA[h][1] : curA[h][1]; PG8_STAGE(bufoff, Ab + (koff), _o); } \
;         else { PG8_STAGE(bufoff, ((nextflag) ? nA : cA) + (size_t)(h) * hstep + (koff), voffA); } } while (0)
; template <class Epi, class Sched, bool ALIGN_EPI, int DT>
; __device__ __forceinline__ void gemm_phase(LAS unsigned char* lds, const int KB, const Sched& S, const Epi& E) {
;     ...
;             PG8_LDB(B0, 0, 0); PG8_LDB(B1, 0, 1); PG8_SCHED; PG8_LDA(At, 0, 0); PG8_STA(PG8_SA(1, 1), false, 1, k1);
;             PG8_WAIT_V(8); PG8_WAIT_L(0); PG8_BAR; PG8_MMA(0, 0, At, B0); PG8_MMA(0, 1, At, B1); PG8_BAR; PG8_SCHED;
;             PG8_LDA(At, 0, 1); PG8_STAGE(PG8_SB(0, 0), b2, voffB); PG8_STAGE(PG8_SB(0, 1), b2 + hstep, voffB); PG8_STA(PG8_SA(0, 0), last, 0, k2);
;             PG8_WAIT_V(8); PG8_WAIT_L(0); PG8_BAR; PG8_MMA(1, 0, At, B0); PG8_MMA(1, 1, At, B1); PG8_BAR; PG8_SCHED;
.LBB0_2387:
	ds_read_b128 v[18:21], v198
	ds_read_b128 v[22:25], v198 offset:1024
	ds_read_b128 v[26:29], v198 offset:2048
	ds_read_b128 v[30:33], v198 offset:3072
	ds_read_b128 v[2:5], v199
	ds_read_b128 v[6:9], v199 offset:1024
	ds_read_b128 v[10:13], v199 offset:2048
	ds_read_b128 v[14:17], v199 offset:3072
	s_add_u32 s42, s44, 0x100
	s_addc_u32 s43, s45, 0
	s_add_i32 s76, s63, s4
	s_add_i32 m0, s33, 0xc000
	s_add_i32 s77, s33, 0xe000
	s_add_i32 s74, s76, 0x2000
	s_cmp_eq_u32 s71, 18
	v_lshl_add_u64 v[184:185], v[178:179], 0, s[44:45]
	s_cselect_b64 vcc, -1, 0
	s_cselect_b32 s75, 0, s42
	v_cndmask_b32_e32 v185, v185, v177, vcc
	v_cndmask_b32_e32 v184, v184, v176, vcc
	v_lshl_add_u64 v[226:227], v[180:181], 0, s[44:45]
	ds_read_b128 v[186:189], v200
	ds_read_b128 v[190:193], v200 offset:1024
	ds_read_b128 v[202:205], v200 offset:2048
	ds_read_b128 v[206:209], v200 offset:3072
	ds_read_b128 v[210:213], v200 offset:4096
	ds_read_b128 v[214:217], v200 offset:5120
	ds_read_b128 v[218:221], v200 offset:6144
	ds_read_b128 v[222:225], v200 offset:7168
	global_load_lds_dwordx4 v[226:227], off
	v_lshl_add_u64 v[226:227], v[182:183], 0, s[44:45]
	s_mov_b32 m0, s77
	s_nop 0
	global_load_lds_dwordx4 v[226:227], off
	s_waitcnt vmcnt(8)
	s_waitcnt lgkmcnt(0)
	s_barrier
	s_setprio 1
	s_waitcnt lgkmcnt(0)
	v_mfma_scale_f32_16x16x128_f8f6f4 v[158:161], v[18:25], v[186:193], v[158:161], v1, v1 op_sel_hi:[0,0,0]
	v_mfma_scale_f32_16x16x128_f8f6f4 v[154:157], v[26:33], v[186:193], v[154:157], v1, v1 op_sel_hi:[0,0,0]
	v_mfma_scale_f32_16x16x128_f8f6f4 v[150:153], v[18:25], v[202:209], v[150:153], v1, v1 op_sel_hi:[0,0,0]
	v_mfma_scale_f32_16x16x128_f8f6f4 v[142:145], v[26:33], v[202:209], v[142:145], v1, v1 op_sel_hi:[0,0,0]
	v_mfma_scale_f32_16x16x128_f8f6f4 v[134:137], v[18:25], v[210:217], v[134:137], v1, v1 op_sel_hi:[0,0,0]
	v_mfma_scale_f32_16x16x128_f8f6f4 v[126:129], v[26:33], v[210:217], v[126:129], v1, v1 op_sel_hi:[0,0,0]
	v_mfma_scale_f32_16x16x128_f8f6f4 v[118:121], v[18:25], v[218:225], v[118:121], v1, v1 op_sel_hi:[0,0,0]
	v_mfma_scale_f32_16x16x128_f8f6f4 v[110:113], v[26:33], v[218:225], v[110:113], v1, v1 op_sel_hi:[0,0,0]
	s_setprio 0
	s_setprio 1
	v_mfma_scale_f32_16x16x128_f8f6f4 v[146:149], v[2:9], v[186:193], v[146:149], v1, v1 op_sel_hi:[0,0,0]
	v_mfma_scale_f32_16x16x128_f8f6f4 v[138:141], v[10:17], v[186:193], v[138:141], v1, v1 op_sel_hi:[0,0,0]
	v_mfma_scale_f32_16x16x128_f8f6f4 v[130:133], v[2:9], v[202:209], v[130:133], v1, v1 op_sel_hi:[0,0,0]
	v_mfma_scale_f32_16x16x128_f8f6f4 v[122:125], v[10:17], v[202:209], v[122:125], v1, v1 op_sel_hi:[0,0,0]
	v_mfma_scale_f32_16x16x128_f8f6f4 v[114:117], v[2:9], v[210:217], v[114:117], v1, v1 op_sel_hi:[0,0,0]
	v_mfma_scale_f32_16x16x128_f8f6f4 v[106:109], v[10:17], v[210:217], v[106:109], v1, v1 op_sel_hi:[0,0,0]
	v_mfma_scale_f32_16x16x128_f8f6f4 v[102:105], v[2:9], v[218:225], v[102:105], v1, v1 op_sel_hi:[0,0,0]
	v_mfma_scale_f32_16x16x128_f8f6f4 v[98:101], v[10:17], v[218:225], v[98:101], v1, v1 op_sel_hi:[0,0,0]
	s_setprio 0
	s_barrier
	s_mov_b32 m0, s76
	v_lshl_add_u64 v[188:189], v[184:185], 0, v[170:171]
	ds_read_b128 v[202:205], v200 offset:16384
	ds_read_b128 v[206:209], v200 offset:17408
	ds_read_b128 v[210:213], v200 offset:18432
	ds_read_b128 v[214:217], v200 offset:19456
	ds_read_b128 v[218:221], v200 offset:20480
	ds_read_b128 v[222:225], v200 offset:21504
	ds_read_b128 v[226:229], v200 offset:22528
	ds_read_b128 v[230:233], v200 offset:23552
	global_load_lds_dwordx4 v[188:189], off
	v_lshl_add_u64 v[186:187], v[184:185], 0, v[164:165]
	s_mov_b32 m0, s74
	s_cselect_b32 s45, s9, s41
	s_cselect_b32 s44, s8, s40
	v_lshl_add_u64 v[190:191], v[184:185], 0, s[12:13]
	s_add_i32 s74, s64, s4
	global_load_lds_dwordx4 v[186:187], off
	v_lshl_add_u64 v[192:193], v[190:191], 0, v[170:171]
	s_mov_b32 m0, s74
	v_lshl_add_u64 v[190:191], v[190:191], 0, v[164:165]
	global_load_lds_dwordx4 v[192:193], off
	s_add_i32 m0, s74, 0x2000
	s_add_u32 s44, s44, s75
	s_addc_u32 s45, s45, 0
	global_load_lds_dwordx4 v[190:191], off
	v_lshl_add_u64 v[190:191], s[44:45], 0, v[166:167]
	s_mov_b32 m0, s33
	v_lshl_add_u64 v[192:193], s[44:45], 0, v[168:169]
	global_load_lds_dwordx4 v[190:191], off
	s_mov_b32 m0, s39
	s_nop 0
	global_load_lds_dwordx4 v[192:193], off
	s_waitcnt vmcnt(8)
	s_waitcnt lgkmcnt(0)
	s_barrier
	s_setprio 1
	s_waitcnt lgkmcnt(0)
	v_mfma_scale_f32_16x16x128_f8f6f4 v[94:97], v[18:25], v[202:209], v[94:97], v1, v1 op_sel_hi:[0,0,0]
	v_mfma_scale_f32_16x16x128_f8f6f4 v[90:93], v[26:33], v[202:209], v[90:93], v1, v1 op_sel_hi:[0,0,0]
	v_mfma_scale_f32_16x16x128_f8f6f4 v[86:89], v[18:25], v[210:217], v[86:89], v1, v1 op_sel_hi:[0,0,0]
	v_mfma_scale_f32_16x16x128_f8f6f4 v[78:81], v[26:33], v[210:217], v[78:81], v1, v1 op_sel_hi:[0,0,0]
	v_mfma_scale_f32_16x16x128_f8f6f4 v[62:65], v[18:25], v[218:225], v[62:65], v1, v1 op_sel_hi:[0,0,0]
	v_mfma_scale_f32_16x16x128_f8f6f4 v[54:57], v[26:33], v[218:225], v[54:57], v1, v1 op_sel_hi:[0,0,0]
	v_mfma_scale_f32_16x16x128_f8f6f4 v[46:49], v[18:25], v[226:233], v[46:49], v1, v1 op_sel_hi:[0,0,0]
	v_mfma_scale_f32_16x16x128_f8f6f4 v[38:41], v[26:33], v[226:233], v[38:41], v1, v1 op_sel_hi:[0,0,0]
	s_setprio 0
	s_setprio 1
	v_mfma_scale_f32_16x16x128_f8f6f4 v[82:85], v[2:9], v[202:209], v[82:85], v1, v1 op_sel_hi:[0,0,0]
	v_mfma_scale_f32_16x16x128_f8f6f4 v[74:77], v[10:17], v[202:209], v[74:77], v1, v1 op_sel_hi:[0,0,0]
	v_mfma_scale_f32_16x16x128_f8f6f4 v[58:61], v[2:9], v[210:217], v[58:61], v1, v1 op_sel_hi:[0,0,0]
	v_mfma_scale_f32_16x16x128_f8f6f4 v[50:53], v[10:17], v[210:217], v[50:53], v1, v1 op_sel_hi:[0,0,0]
	v_mfma_scale_f32_16x16x128_f8f6f4 v[42:45], v[2:9], v[218:225], v[42:45], v1, v1 op_sel_hi:[0,0,0]
	v_mfma_scale_f32_16x16x128_f8f6f4 v[34:37], v[10:17], v[218:225], v[34:37], v1, v1 op_sel_hi:[0,0,0]
	v_mfma_scale_f32_16x16x128_f8f6f4 v[70:73], v[2:9], v[226:233], v[70:73], v1, v1 op_sel_hi:[0,0,0]
	v_mfma_scale_f32_16x16x128_f8f6f4 v[66:69], v[10:17], v[226:233], v[66:69], v1, v1 op_sel_hi:[0,0,0]
	s_setprio 0
	s_barrier
; #define PG8_STAGE(bufoff, gbase, voff) do { _Pragma("unroll") for (int _i = 0; _i < 2; ++_i) \
;         __builtin_amdgcn_global_load_lds((const unsigned*)((const char*)(gbase) + (voff)[_i]), (LAS unsigned*)(lds + (bufoff) + ldsw + _i * 8192), 16, 0, 0); } while (0)
; #define PG8_LDA(dst, b, h) do { _Pragma("unroll") for (int m = 0; m < 4; ++m) dst[m] = PG8_LD32(lds + PG8_SA(b, h) + aoff + m * 2048); } while (0)
; #define PG8_LDB(dst, b, h) do { _Pragma("unroll") for (int n = 0; n < 2; ++n) dst[n] = PG8_LD32(lds + PG8_SB(b, h) + boff + n * 2048); } while (0)
; #define PG8_WAIT_V(n) asm volatile("s_waitcnt vmcnt(" #n ")" ::: "memory")
; #define PG8_WAIT_L(n) asm volatile("s_waitcnt lgkmcnt(" #n ")" ::: "memory")
; #define PG8_BAR __builtin_amdgcn_s_barrier()
; #define PG8_SCHED __builtin_amdgcn_sched_barrier(0)
; #define PG8_STA(bufoff, nextflag, h, koff) do { if constexpr (Sched::GATHER) { unsigned _o[2]; _o[0] = (nextflag) ? nxtA[h][0] : curA[h][0]; _o[1] = (nextflag) ? nxtA[h][1] : curA[h][1]; PG8_STAGE(bufoff, Ab + (koff), _o); } \
;         else { PG8_STAGE(bufoff, ((nextflag) ? nA : cA) + (size_t)(h) * hstep + (koff), voffA); } } while (0)
; template <class Epi, class Sched, bool ALIGN_EPI, int DT>
; __device__ __forceinline__ void gemm_phase(LAS unsigned char* lds, const int KB, const Sched& S, const Epi& E) {
;     ...
;             PG8_LDB(B0, 1, 0); PG8_LDB(B1, 1, 1); PG8_SCHED; PG8_LDA(At, 1, 0); PG8_STA(PG8_SA(0, 1), last, 1, k2);
;             PG8_WAIT_V(8); PG8_WAIT_L(0); PG8_BAR; PG8_MMA(0, 0, At, B0); PG8_MMA(0, 1, At, B1); PG8_BAR; PG8_SCHED;
;             PG8_LDA(At, 1, 1); PG8_STAGE(PG8_SB(1, 0), b3, voffB); PG8_STAGE(PG8_SB(1, 1), b3 + hstep, voffB); PG8_STA(PG8_SA(1, 0), last, 0, k3);
;             PG8_WAIT_V(8); PG8_WAIT_L(0); PG8_BAR; PG8_MMA(1, 0, At, B0); PG8_MMA(1, 1, At, B1); PG8_BAR; PG8_SCHED;
	s_add_i32 s74, 0, 0x18000
	s_add_i32 s75, 0, 0x1c000
	v_add_u32_e32 v14, s74, v196
	v_add_u32_e32 v30, s75, v196
	ds_read_b128 v[2:5], v14
	ds_read_b128 v[6:9], v14 offset:1024
	ds_read_b128 v[10:13], v14 offset:2048
	ds_read_b128 v[14:17], v14 offset:3072
	ds_read_b128 v[18:21], v30
	ds_read_b128 v[22:25], v30 offset:1024
	ds_read_b128 v[26:29], v30 offset:2048
	ds_read_b128 v[30:33], v30 offset:3072
	s_add_u32 s44, s44, 0x58000
	s_addc_u32 s45, s45, 0
	s_mov_b32 m0, s46
	v_lshl_add_u64 v[234:235], s[44:45], 0, v[166:167]
	ds_read_b128 v[202:205], v200 offset:32768
	ds_read_b128 v[206:209], v200 offset:33792
	ds_read_b128 v[210:213], v200 offset:34816
	ds_read_b128 v[214:217], v200 offset:35840
	ds_read_b128 v[218:221], v200 offset:36864
	ds_read_b128 v[222:225], v200 offset:37888
	ds_read_b128 v[226:229], v200 offset:38912
	ds_read_b128 v[230:233], v200 offset:39936
	global_load_lds_dwordx4 v[234:235], off
	v_lshl_add_u64 v[234:235], s[44:45], 0, v[168:169]
	s_mov_b32 m0, s47
	s_nop 0
	global_load_lds_dwordx4 v[234:235], off
	s_add_i32 s44, s74, s4
	v_lshl_add_u64 v[188:189], v[188:189], 0, s[16:17]
	s_mov_b32 m0, s44
	s_waitcnt vmcnt(8)
	s_waitcnt lgkmcnt(0)
	s_barrier
	s_setprio 1
	s_waitcnt lgkmcnt(0)
	v_mfma_scale_f32_16x16x128_f8f6f4 v[158:161], v[2:9], v[202:209], v[158:161], v1, v1 op_sel_hi:[0,0,0]
	v_mfma_scale_f32_16x16x128_f8f6f4 v[154:157], v[10:17], v[202:209], v[154:157], v1, v1 op_sel_hi:[0,0,0]
	v_mfma_scale_f32_16x16x128_f8f6f4 v[150:153], v[2:9], v[210:217], v[150:153], v1, v1 op_sel_hi:[0,0,0]
	v_mfma_scale_f32_16x16x128_f8f6f4 v[142:145], v[10:17], v[210:217], v[142:145], v1, v1 op_sel_hi:[0,0,0]
	v_mfma_scale_f32_16x16x128_f8f6f4 v[134:137], v[2:9], v[218:225], v[134:137], v1, v1 op_sel_hi:[0,0,0]
	v_mfma_scale_f32_16x16x128_f8f6f4 v[126:129], v[10:17], v[218:225], v[126:129], v1, v1 op_sel_hi:[0,0,0]
	v_mfma_scale_f32_16x16x128_f8f6f4 v[118:121], v[2:9], v[226:233], v[118:121], v1, v1 op_sel_hi:[0,0,0]
	v_mfma_scale_f32_16x16x128_f8f6f4 v[110:113], v[10:17], v[226:233], v[110:113], v1, v1 op_sel_hi:[0,0,0]
	s_setprio 0
	s_setprio 1
	v_mfma_scale_f32_16x16x128_f8f6f4 v[146:149], v[18:25], v[202:209], v[146:149], v1, v1 op_sel_hi:[0,0,0]
	v_mfma_scale_f32_16x16x128_f8f6f4 v[138:141], v[26:33], v[202:209], v[138:141], v1, v1 op_sel_hi:[0,0,0]
	v_mfma_scale_f32_16x16x128_f8f6f4 v[130:133], v[18:25], v[210:217], v[130:133], v1, v1 op_sel_hi:[0,0,0]
	v_mfma_scale_f32_16x16x128_f8f6f4 v[122:125], v[26:33], v[210:217], v[122:125], v1, v1 op_sel_hi:[0,0,0]
	v_mfma_scale_f32_16x16x128_f8f6f4 v[114:117], v[18:25], v[218:225], v[114:117], v1, v1 op_sel_hi:[0,0,0]
	v_mfma_scale_f32_16x16x128_f8f6f4 v[106:109], v[26:33], v[218:225], v[106:109], v1, v1 op_sel_hi:[0,0,0]
	v_mfma_scale_f32_16x16x128_f8f6f4 v[102:105], v[18:25], v[226:233], v[102:105], v1, v1 op_sel_hi:[0,0,0]
	v_mfma_scale_f32_16x16x128_f8f6f4 v[98:101], v[26:33], v[226:233], v[98:101], v1, v1 op_sel_hi:[0,0,0]
	s_setprio 0
	s_barrier
	ds_read_b128 v[202:205], v200 offset:49152
	ds_read_b128 v[206:209], v200 offset:50176
	ds_read_b128 v[210:213], v200 offset:51200
	ds_read_b128 v[214:217], v200 offset:52224
	ds_read_b128 v[218:221], v200 offset:53248
	ds_read_b128 v[222:225], v200 offset:54272
	ds_read_b128 v[226:229], v200 offset:55296
	ds_read_b128 v[230:233], v200 offset:56320
	global_load_lds_dwordx4 v[188:189], off
	v_lshl_add_u64 v[186:187], v[186:187], 0, s[16:17]
	s_add_i32 m0, s44, 0x2000
	v_lshl_add_u64 v[184:185], v[184:185], 0, s[18:19]
	s_add_i32 s44, s75, s4
	global_load_lds_dwordx4 v[186:187], off
	v_lshl_add_u64 v[186:187], v[184:185], 0, v[170:171]
	s_mov_b32 m0, s44
	v_lshl_add_u64 v[184:185], v[184:185], 0, v[164:165]
	global_load_lds_dwordx4 v[186:187], off
	s_add_i32 m0, s44, 0x2000
	s_nop 0
	global_load_lds_dwordx4 v[184:185], off
	v_lshl_add_u64 v[184:185], v[190:191], 0, s[16:17]
	s_mov_b32 m0, s52
	s_nop 0
	global_load_lds_dwordx4 v[184:185], off
	v_lshl_add_u64 v[184:185], v[192:193], 0, s[16:17]
	s_mov_b32 m0, s53
	s_nop 0
	global_load_lds_dwordx4 v[184:185], off
	s_waitcnt vmcnt(8)
	s_waitcnt lgkmcnt(0)
	s_barrier
	s_setprio 1
	s_waitcnt lgkmcnt(0)
	v_mfma_scale_f32_16x16x128_f8f6f4 v[94:97], v[2:9], v[202:209], v[94:97], v1, v1 op_sel_hi:[0,0,0]
	v_mfma_scale_f32_16x16x128_f8f6f4 v[90:93], v[10:17], v[202:209], v[90:93], v1, v1 op_sel_hi:[0,0,0]
	v_mfma_scale_f32_16x16x128_f8f6f4 v[86:89], v[2:9], v[210:217], v[86:89], v1, v1 op_sel_hi:[0,0,0]
	v_mfma_scale_f32_16x16x128_f8f6f4 v[78:81], v[10:17], v[210:217], v[78:81], v1, v1 op_sel_hi:[0,0,0]
	v_mfma_scale_f32_16x16x128_f8f6f4 v[62:65], v[2:9], v[218:225], v[62:65], v1, v1 op_sel_hi:[0,0,0]
	v_mfma_scale_f32_16x16x128_f8f6f4 v[54:57], v[10:17], v[218:225], v[54:57], v1, v1 op_sel_hi:[0,0,0]
	v_mfma_scale_f32_16x16x128_f8f6f4 v[46:49], v[2:9], v[226:233], v[46:49], v1, v1 op_sel_hi:[0,0,0]
	v_mfma_scale_f32_16x16x128_f8f6f4 v[38:41], v[10:17], v[226:233], v[38:41], v1, v1 op_sel_hi:[0,0,0]
	s_setprio 0
	s_setprio 1
	v_mfma_scale_f32_16x16x128_f8f6f4 v[82:85], v[18:25], v[202:209], v[82:85], v1, v1 op_sel_hi:[0,0,0]
	v_mfma_scale_f32_16x16x128_f8f6f4 v[74:77], v[26:33], v[202:209], v[74:77], v1, v1 op_sel_hi:[0,0,0]
	v_mfma_scale_f32_16x16x128_f8f6f4 v[58:61], v[18:25], v[210:217], v[58:61], v1, v1 op_sel_hi:[0,0,0]
	v_mfma_scale_f32_16x16x128_f8f6f4 v[50:53], v[26:33], v[210:217], v[50:53], v1, v1 op_sel_hi:[0,0,0]
	v_mfma_scale_f32_16x16x128_f8f6f4 v[42:45], v[18:25], v[218:225], v[42:45], v1, v1 op_sel_hi:[0,0,0]
	v_mfma_scale_f32_16x16x128_f8f6f4 v[34:37], v[26:33], v[218:225], v[34:37], v1, v1 op_sel_hi:[0,0,0]
	v_mfma_scale_f32_16x16x128_f8f6f4 v[70:73], v[18:25], v[226:233], v[70:73], v1, v1 op_sel_hi:[0,0,0]
	v_mfma_scale_f32_16x16x128_f8f6f4 v[66:69], v[26:33], v[226:233], v[66:69], v1, v1 op_sel_hi:[0,0,0]
	s_setprio 0
	s_barrier
	s_add_i32 s71, s71, 2
	s_cmp_gt_u32 s71, 19
	s_mov_b64 s[44:45], s[42:43]
	s_cbranch_scc0 .LBB0_2387
	s_and_b64 vcc, exec, s[20:21]
	s_cbranch_vccz .LBB0_2390
	s_barrier
